# strategy 9 loop-edge edit: in the ten GEMM K-loops the counter/pointer update and exit compare moved in front of the loop-back s_barrier, only the branch stays behind it
# baseline (speedup 1.0000x reference)
.LBB0_135:
	ds_read_b128 v[134:137], v130
	ds_read_b128 v[138:141], v130 offset:1024
	ds_read_b128 v[142:145], v130 offset:2048
	ds_read_b128 v[156:159], v130 offset:3072
	ds_read_b128 v[160:163], v131
	ds_read_b128 v[164:167], v131 offset:1024
	ds_read_b128 v[168:171], v131 offset:2048
	ds_read_b128 v[172:175], v131 offset:3072
	s_add_u32 s8, s30, 0xfffe0080
	s_addc_u32 s9, s31, -1
	s_cmp_eq_u32 vcc_lo, 4
	s_cselect_b32 s35, s25, s9
	s_cselect_b32 s34, s45, s8
	s_cselect_b32 s9, s23, s58
	s_cselect_b32 s8, s80, s48
	s_mov_b32 m0, s88
	v_lshl_add_u64 v[210:211], s[30:31], 0, v[152:153]
	ds_read_b128 v[176:179], v193
	ds_read_b128 v[180:183], v193 offset:1024
	ds_read_b128 v[184:187], v193 offset:2048
	ds_read_b128 v[188:191], v193 offset:3072
	ds_read_b128 v[194:197], v193 offset:4096
	ds_read_b128 v[198:201], v193 offset:5120
	ds_read_b128 v[202:205], v193 offset:6144
	ds_read_b128 v[206:209], v193 offset:7168
	global_load_lds_dwordx4 v[210:211], off
	v_lshl_add_u64 v[210:211], s[30:31], 0, v[154:155]
	s_mov_b32 m0, s89
	s_nop 0
	global_load_lds_dwordx4 v[210:211], off
	s_waitcnt vmcnt(8)
	s_waitcnt lgkmcnt(0)
	s_barrier
	s_setprio 1
	s_waitcnt lgkmcnt(0)
	v_mfma_i32_16x16x64_i8 v[122:125], v[134:137], v[176:179], v[122:125]
	v_mfma_i32_16x16x64_i8 v[114:117], v[142:145], v[176:179], v[114:117]
	v_mfma_i32_16x16x64_i8 v[106:109], v[134:137], v[184:187], v[106:109]
	v_mfma_i32_16x16x64_i8 v[98:101], v[142:145], v[184:187], v[98:101]
	v_mfma_i32_16x16x64_i8 v[90:93], v[134:137], v[194:197], v[90:93]
	v_mfma_i32_16x16x64_i8 v[82:85], v[142:145], v[194:197], v[82:85]
	v_mfma_i32_16x16x64_i8 v[74:77], v[134:137], v[202:205], v[74:77]
	v_mfma_i32_16x16x64_i8 v[66:69], v[142:145], v[202:205], v[66:69]
	v_mfma_i32_16x16x64_i8 v[122:125], v[138:141], v[180:183], v[122:125]
	v_mfma_i32_16x16x64_i8 v[114:117], v[156:159], v[180:183], v[114:117]
	v_mfma_i32_16x16x64_i8 v[106:109], v[138:141], v[188:191], v[106:109]
	v_mfma_i32_16x16x64_i8 v[98:101], v[156:159], v[188:191], v[98:101]
	v_mfma_i32_16x16x64_i8 v[90:93], v[138:141], v[198:201], v[90:93]
	v_mfma_i32_16x16x64_i8 v[82:85], v[156:159], v[198:201], v[82:85]
	v_mfma_i32_16x16x64_i8 v[74:77], v[138:141], v[206:209], v[74:77]
	v_mfma_i32_16x16x64_i8 v[66:69], v[156:159], v[206:209], v[66:69]
	s_setprio 0
	s_setprio 1
	v_mfma_i32_16x16x64_i8 v[126:129], v[160:163], v[176:179], v[126:129]
	v_mfma_i32_16x16x64_i8 v[118:121], v[168:171], v[176:179], v[118:121]
	v_mfma_i32_16x16x64_i8 v[110:113], v[160:163], v[184:187], v[110:113]
	v_mfma_i32_16x16x64_i8 v[102:105], v[168:171], v[184:187], v[102:105]
	v_mfma_i32_16x16x64_i8 v[94:97], v[160:163], v[194:197], v[94:97]
	v_mfma_i32_16x16x64_i8 v[86:89], v[168:171], v[194:197], v[86:89]
	v_mfma_i32_16x16x64_i8 v[78:81], v[160:163], v[202:205], v[78:81]
	v_mfma_i32_16x16x64_i8 v[70:73], v[168:171], v[202:205], v[70:73]
	v_mfma_i32_16x16x64_i8 v[126:129], v[164:167], v[180:183], v[126:129]
	v_mfma_i32_16x16x64_i8 v[118:121], v[172:175], v[180:183], v[118:121]
	v_mfma_i32_16x16x64_i8 v[110:113], v[164:167], v[188:191], v[110:113]
	v_mfma_i32_16x16x64_i8 v[102:105], v[172:175], v[188:191], v[102:105]
	v_mfma_i32_16x16x64_i8 v[94:97], v[164:167], v[198:201], v[94:97]
	v_mfma_i32_16x16x64_i8 v[86:89], v[172:175], v[198:201], v[86:89]
	v_mfma_i32_16x16x64_i8 v[78:81], v[164:167], v[206:209], v[78:81]
	v_mfma_i32_16x16x64_i8 v[70:73], v[172:175], v[206:209], v[70:73]
	s_setprio 0
	s_barrier
	s_mov_b32 m0, s4
	v_lshl_add_u64 v[210:211], s[8:9], 0, v[0:1]
	s_add_u32 s54, s8, 0x20000
	ds_read_b128 v[176:179], v193 offset:16384
	ds_read_b128 v[180:183], v193 offset:17408
	ds_read_b128 v[184:187], v193 offset:18432
	ds_read_b128 v[188:191], v193 offset:19456
	ds_read_b128 v[194:197], v193 offset:20480
	ds_read_b128 v[198:201], v193 offset:21504
	ds_read_b128 v[202:205], v193 offset:22528
	ds_read_b128 v[206:209], v193 offset:23552
	global_load_lds_dwordx4 v[210:211], off
	v_lshl_add_u64 v[212:213], s[8:9], 0, v[146:147]
	s_mov_b32 m0, s5
	s_addc_u32 s55, s9, 0
	global_load_lds_dwordx4 v[212:213], off
	v_lshl_add_u64 v[214:215], s[54:55], 0, v[0:1]
	s_mov_b32 m0, s90
	v_lshl_add_u64 v[216:217], s[34:35], 0, v[148:149]
	global_load_lds_dwordx4 v[214:215], off
	v_lshl_add_u64 v[214:215], s[54:55], 0, v[146:147]
	s_mov_b32 m0, vcc_hi
	s_nop 0
	global_load_lds_dwordx4 v[214:215], off
	v_lshl_add_u64 v[214:215], s[34:35], 0, v[150:151]
	s_mov_b32 m0, s52
	s_nop 0
	global_load_lds_dwordx4 v[214:215], off
	s_mov_b32 m0, s70
	s_nop 0
	global_load_lds_dwordx4 v[216:217], off
	s_waitcnt vmcnt(8)
	s_waitcnt lgkmcnt(0)
	s_barrier
	s_setprio 1
	s_waitcnt lgkmcnt(0)
	v_mfma_i32_16x16x64_i8 v[58:61], v[134:137], v[176:179], v[58:61]
	v_mfma_i32_16x16x64_i8 v[50:53], v[142:145], v[176:179], v[50:53]
	v_mfma_i32_16x16x64_i8 v[42:45], v[134:137], v[184:187], v[42:45]
	v_mfma_i32_16x16x64_i8 v[34:37], v[142:145], v[184:187], v[34:37]
	v_mfma_i32_16x16x64_i8 v[30:33], v[134:137], v[194:197], v[30:33]
	v_mfma_i32_16x16x64_i8 v[18:21], v[142:145], v[194:197], v[18:21]
	v_mfma_i32_16x16x64_i8 v[14:17], v[134:137], v[202:205], v[14:17]
	v_mfma_i32_16x16x64_i8 v[2:5], v[142:145], v[202:205], v[2:5]
	v_mfma_i32_16x16x64_i8 v[58:61], v[138:141], v[180:183], v[58:61]
	v_mfma_i32_16x16x64_i8 v[50:53], v[156:159], v[180:183], v[50:53]
	v_mfma_i32_16x16x64_i8 v[42:45], v[138:141], v[188:191], v[42:45]
	v_mfma_i32_16x16x64_i8 v[34:37], v[156:159], v[188:191], v[34:37]
	v_mfma_i32_16x16x64_i8 v[30:33], v[138:141], v[198:201], v[30:33]
	v_mfma_i32_16x16x64_i8 v[18:21], v[156:159], v[198:201], v[18:21]
	v_mfma_i32_16x16x64_i8 v[14:17], v[138:141], v[206:209], v[14:17]
	v_mfma_i32_16x16x64_i8 v[2:5], v[156:159], v[206:209], v[2:5]
	s_setprio 0
	s_setprio 1
	v_mfma_i32_16x16x64_i8 v[62:65], v[160:163], v[176:179], v[62:65]
	v_mfma_i32_16x16x64_i8 v[54:57], v[168:171], v[176:179], v[54:57]
	v_mfma_i32_16x16x64_i8 v[46:49], v[160:163], v[184:187], v[46:49]
	v_mfma_i32_16x16x64_i8 v[38:41], v[168:171], v[184:187], v[38:41]
	v_mfma_i32_16x16x64_i8 v[26:29], v[160:163], v[194:197], v[26:29]
	v_mfma_i32_16x16x64_i8 v[22:25], v[168:171], v[194:197], v[22:25]
	v_mfma_i32_16x16x64_i8 v[10:13], v[160:163], v[202:205], v[10:13]
	v_mfma_i32_16x16x64_i8 v[6:9], v[168:171], v[202:205], v[6:9]
	v_mfma_i32_16x16x64_i8 v[62:65], v[164:167], v[180:183], v[62:65]
	v_mfma_i32_16x16x64_i8 v[54:57], v[172:175], v[180:183], v[54:57]
	v_mfma_i32_16x16x64_i8 v[46:49], v[164:167], v[188:191], v[46:49]
	v_mfma_i32_16x16x64_i8 v[38:41], v[172:175], v[188:191], v[38:41]
	v_mfma_i32_16x16x64_i8 v[26:29], v[164:167], v[198:201], v[26:29]
	v_mfma_i32_16x16x64_i8 v[22:25], v[172:175], v[198:201], v[22:25]
	v_mfma_i32_16x16x64_i8 v[10:13], v[164:167], v[206:209], v[10:13]
	v_mfma_i32_16x16x64_i8 v[6:9], v[172:175], v[206:209], v[6:9]
	s_setprio 0
	s_barrier
	ds_read_b128 v[134:137], v132
	ds_read_b128 v[138:141], v132 offset:1024
	ds_read_b128 v[142:145], v132 offset:2048
	ds_read_b128 v[156:159], v132 offset:3072
	ds_read_b128 v[160:163], v133
	ds_read_b128 v[164:167], v133 offset:1024
	ds_read_b128 v[168:171], v133 offset:2048
	ds_read_b128 v[172:175], v133 offset:3072
	s_add_u32 s34, s34, 0x20000
	s_addc_u32 s35, s35, 0
	s_mov_b32 m0, s71
	v_lshl_add_u64 v[218:219], s[34:35], 0, v[150:151]
	ds_read_b128 v[176:179], v193 offset:32768
	ds_read_b128 v[180:183], v193 offset:33792
	ds_read_b128 v[184:187], v193 offset:34816
	ds_read_b128 v[188:191], v193 offset:35840
	ds_read_b128 v[194:197], v193 offset:36864
	ds_read_b128 v[198:201], v193 offset:37888
	ds_read_b128 v[202:205], v193 offset:38912
	ds_read_b128 v[206:209], v193 offset:39936
	global_load_lds_dwordx4 v[218:219], off
	v_lshl_add_u64 v[218:219], s[34:35], 0, v[148:149]
	s_mov_b32 m0, s75
	s_nop 0
	global_load_lds_dwordx4 v[218:219], off
	s_waitcnt vmcnt(8)
	s_waitcnt lgkmcnt(0)
	s_barrier
	s_setprio 1
	s_waitcnt lgkmcnt(0)
	v_mfma_i32_16x16x64_i8 v[122:125], v[134:137], v[176:179], v[122:125]
	v_mfma_i32_16x16x64_i8 v[114:117], v[142:145], v[176:179], v[114:117]
	v_mfma_i32_16x16x64_i8 v[106:109], v[134:137], v[184:187], v[106:109]
	v_mfma_i32_16x16x64_i8 v[98:101], v[142:145], v[184:187], v[98:101]
	v_mfma_i32_16x16x64_i8 v[90:93], v[134:137], v[194:197], v[90:93]
	v_mfma_i32_16x16x64_i8 v[82:85], v[142:145], v[194:197], v[82:85]
	v_mfma_i32_16x16x64_i8 v[74:77], v[134:137], v[202:205], v[74:77]
	v_mfma_i32_16x16x64_i8 v[66:69], v[142:145], v[202:205], v[66:69]
	v_mfma_i32_16x16x64_i8 v[122:125], v[138:141], v[180:183], v[122:125]
	v_mfma_i32_16x16x64_i8 v[114:117], v[156:159], v[180:183], v[114:117]
	v_mfma_i32_16x16x64_i8 v[106:109], v[138:141], v[188:191], v[106:109]
	v_mfma_i32_16x16x64_i8 v[98:101], v[156:159], v[188:191], v[98:101]
	v_mfma_i32_16x16x64_i8 v[90:93], v[138:141], v[198:201], v[90:93]
	v_mfma_i32_16x16x64_i8 v[82:85], v[156:159], v[198:201], v[82:85]
	v_mfma_i32_16x16x64_i8 v[74:77], v[138:141], v[206:209], v[74:77]
	v_mfma_i32_16x16x64_i8 v[66:69], v[156:159], v[206:209], v[66:69]
	s_setprio 0
	s_setprio 1
	v_mfma_i32_16x16x64_i8 v[126:129], v[160:163], v[176:179], v[126:129]
	v_mfma_i32_16x16x64_i8 v[118:121], v[168:171], v[176:179], v[118:121]
	v_mfma_i32_16x16x64_i8 v[110:113], v[160:163], v[184:187], v[110:113]
	v_mfma_i32_16x16x64_i8 v[102:105], v[168:171], v[184:187], v[102:105]
	v_mfma_i32_16x16x64_i8 v[94:97], v[160:163], v[194:197], v[94:97]
	v_mfma_i32_16x16x64_i8 v[86:89], v[168:171], v[194:197], v[86:89]
	v_mfma_i32_16x16x64_i8 v[78:81], v[160:163], v[202:205], v[78:81]
	v_mfma_i32_16x16x64_i8 v[70:73], v[168:171], v[202:205], v[70:73]
	v_mfma_i32_16x16x64_i8 v[126:129], v[164:167], v[180:183], v[126:129]
	v_mfma_i32_16x16x64_i8 v[118:121], v[172:175], v[180:183], v[118:121]
	v_mfma_i32_16x16x64_i8 v[110:113], v[164:167], v[188:191], v[110:113]
	v_mfma_i32_16x16x64_i8 v[102:105], v[172:175], v[188:191], v[102:105]
	v_mfma_i32_16x16x64_i8 v[94:97], v[164:167], v[198:201], v[94:97]
	v_mfma_i32_16x16x64_i8 v[86:89], v[172:175], v[198:201], v[86:89]
	v_mfma_i32_16x16x64_i8 v[78:81], v[164:167], v[206:209], v[78:81]
	v_mfma_i32_16x16x64_i8 v[70:73], v[172:175], v[206:209], v[70:73]
	s_setprio 0
	s_barrier
	s_mov_b32 m0, s50
	v_lshl_add_u64 v[210:211], v[210:211], 0, s[56:57]
	s_add_u32 s8, s8, 0x20080
	ds_read_b128 v[176:179], v193 offset:49152
	ds_read_b128 v[180:183], v193 offset:50176
	ds_read_b128 v[184:187], v193 offset:51200
	ds_read_b128 v[188:191], v193 offset:52224
	ds_read_b128 v[194:197], v193 offset:53248
	ds_read_b128 v[198:201], v193 offset:54272
	ds_read_b128 v[202:205], v193 offset:55296
	ds_read_b128 v[206:209], v193 offset:56320
	global_load_lds_dwordx4 v[210:211], off
	v_lshl_add_u64 v[210:211], v[212:213], 0, s[56:57]
	s_mov_b32 m0, s51
	s_addc_u32 s9, s9, 0
	global_load_lds_dwordx4 v[210:211], off
	v_lshl_add_u64 v[210:211], s[8:9], 0, v[0:1]
	s_mov_b32 m0, s94
	s_nop 0
	global_load_lds_dwordx4 v[210:211], off
	v_lshl_add_u64 v[210:211], s[8:9], 0, v[146:147]
	s_mov_b32 m0, s95
	s_nop 0
	global_load_lds_dwordx4 v[210:211], off
	v_lshl_add_u64 v[210:211], v[214:215], 0, s[56:57]
	s_mov_b32 m0, s59
	s_nop 0
	global_load_lds_dwordx4 v[210:211], off
	v_lshl_add_u64 v[210:211], v[216:217], 0, s[56:57]
	s_mov_b32 m0, s33
	s_nop 0
	global_load_lds_dwordx4 v[210:211], off
	s_waitcnt vmcnt(8)
	s_waitcnt lgkmcnt(0)
	s_barrier
	s_setprio 1
	s_waitcnt lgkmcnt(0)
	v_mfma_i32_16x16x64_i8 v[58:61], v[134:137], v[176:179], v[58:61]
	v_mfma_i32_16x16x64_i8 v[50:53], v[142:145], v[176:179], v[50:53]
	v_mfma_i32_16x16x64_i8 v[42:45], v[134:137], v[184:187], v[42:45]
	v_mfma_i32_16x16x64_i8 v[34:37], v[142:145], v[184:187], v[34:37]
	v_mfma_i32_16x16x64_i8 v[30:33], v[134:137], v[194:197], v[30:33]
	v_mfma_i32_16x16x64_i8 v[18:21], v[142:145], v[194:197], v[18:21]
	v_mfma_i32_16x16x64_i8 v[14:17], v[134:137], v[202:205], v[14:17]
	v_mfma_i32_16x16x64_i8 v[2:5], v[142:145], v[202:205], v[2:5]
	v_mfma_i32_16x16x64_i8 v[58:61], v[138:141], v[180:183], v[58:61]
	v_mfma_i32_16x16x64_i8 v[50:53], v[156:159], v[180:183], v[50:53]
	v_mfma_i32_16x16x64_i8 v[42:45], v[138:141], v[188:191], v[42:45]
	v_mfma_i32_16x16x64_i8 v[34:37], v[156:159], v[188:191], v[34:37]
	v_mfma_i32_16x16x64_i8 v[30:33], v[138:141], v[198:201], v[30:33]
	v_mfma_i32_16x16x64_i8 v[18:21], v[156:159], v[198:201], v[18:21]
	v_mfma_i32_16x16x64_i8 v[14:17], v[138:141], v[206:209], v[14:17]
	v_mfma_i32_16x16x64_i8 v[2:5], v[156:159], v[206:209], v[2:5]
	s_setprio 0
	s_setprio 1
	v_mfma_i32_16x16x64_i8 v[62:65], v[160:163], v[176:179], v[62:65]
	v_mfma_i32_16x16x64_i8 v[54:57], v[168:171], v[176:179], v[54:57]
	v_mfma_i32_16x16x64_i8 v[46:49], v[160:163], v[184:187], v[46:49]
	v_mfma_i32_16x16x64_i8 v[38:41], v[168:171], v[184:187], v[38:41]
	v_mfma_i32_16x16x64_i8 v[26:29], v[160:163], v[194:197], v[26:29]
	v_mfma_i32_16x16x64_i8 v[22:25], v[168:171], v[194:197], v[22:25]
	v_mfma_i32_16x16x64_i8 v[10:13], v[160:163], v[202:205], v[10:13]
	v_mfma_i32_16x16x64_i8 v[6:9], v[168:171], v[202:205], v[6:9]
	v_mfma_i32_16x16x64_i8 v[62:65], v[164:167], v[180:183], v[62:65]
	v_mfma_i32_16x16x64_i8 v[54:57], v[172:175], v[180:183], v[54:57]
	v_mfma_i32_16x16x64_i8 v[46:49], v[164:167], v[188:191], v[46:49]
	v_mfma_i32_16x16x64_i8 v[38:41], v[172:175], v[188:191], v[38:41]
	v_mfma_i32_16x16x64_i8 v[26:29], v[164:167], v[198:201], v[26:29]
	v_mfma_i32_16x16x64_i8 v[22:25], v[172:175], v[198:201], v[22:25]
	v_mfma_i32_16x16x64_i8 v[10:13], v[164:167], v[206:209], v[10:13]
	v_mfma_i32_16x16x64_i8 v[6:9], v[172:175], v[206:209], v[6:9]
	s_setprio 0
	s_add_i32 vcc_lo, vcc_lo, 2
	s_add_u32 s30, s30, 0x100
	s_addc_u32 s31, s31, 0
	s_add_u32 s48, s48, 0x100
	s_addc_u32 s58, s58, 0
	s_cmp_gt_u32 vcc_lo, 5
	s_barrier
	s_cbranch_scc0 .LBB0_135
	s_lshl_b32 s4, s44, 8
	s_add_i32 s4, s4, s68
	v_mbcnt_lo_u32_b32 v130, -1, 0
	v_mbcnt_hi_u32_b32 v130, -1, v130
	s_and_b64 vcc, exec, s[20:21]
	v_and_or_b32 v168, v130, 15, s4
	v_ashrrev_i32_e32 v169, 31, v168
	v_lshl_add_u64 v[138:139], v[168:169], 2, s[18:19]
	global_load_dword v131, v[138:139], off
	global_load_dword v132, v[138:139], off offset:64
	global_load_dword v133, v[138:139], off offset:128
	global_load_dword v134, v[138:139], off offset:192
	global_load_dword v135, v[138:139], off offset:512
	global_load_dword v136, v[138:139], off offset:576
	global_load_dword v137, v[138:139], off offset:640
	s_nop 0
	global_load_dword v138, v[138:139], off offset:704
	s_cbranch_vccz .LBB0_138
	s_barrier

.LBB0_195:
	s_add_u32 s4, s26, 0xfffe0080
	s_addc_u32 s5, s27, -1
	s_add_i32 s48, 0, 0x10000
	s_cmp_eq_u32 s88, 4
	s_cselect_b32 s31, s21, s5
	s_cselect_b32 s30, s70, s4
	s_cselect_b32 s29, s19, s80
	s_cselect_b32 s28, s71, s75
	s_add_i32 s50, 0, 0x14000
	v_add_u32_e32 v142, s48, v161
	v_add_u32_e32 v160, s50, v161
	ds_read_b128 v[130:133], v142
	ds_read_b128 v[134:137], v142 offset:1024
	ds_read_b128 v[138:141], v142 offset:2048
	ds_read_b128 v[142:145], v142 offset:3072
	ds_read_b128 v[156:159], v160
	ds_read_b128 v[164:167], v160 offset:1024
	ds_read_b128 v[168:171], v160 offset:2048
	ds_read_b128 v[172:175], v160 offset:3072
	v_lshl_add_u64 v[208:209], s[26:27], 0, v[152:153]
	s_add_i32 m0, s40, 0xc000
	ds_read_b128 v[176:179], v163
	ds_read_b128 v[180:183], v163 offset:1024
	ds_read_b128 v[184:187], v163 offset:2048
	ds_read_b128 v[188:191], v163 offset:3072
	ds_read_b128 v[192:195], v163 offset:4096
	ds_read_b128 v[196:199], v163 offset:5120
	ds_read_b128 v[200:203], v163 offset:6144
	ds_read_b128 v[204:207], v163 offset:7168
	global_load_lds_dwordx4 v[208:209], off
	v_lshl_add_u64 v[208:209], s[26:27], 0, v[154:155]
	s_add_i32 m0, s40, 0xe000
	s_nop 0
	global_load_lds_dwordx4 v[208:209], off
	s_waitcnt vmcnt(8)
	s_waitcnt lgkmcnt(0)
	s_barrier
	s_setprio 1
	s_waitcnt lgkmcnt(0)
	v_mfma_i32_16x16x64_i8 v[126:129], v[130:133], v[176:179], v[126:129]
	v_mfma_i32_16x16x64_i8 v[122:125], v[138:141], v[176:179], v[122:125]
	v_mfma_i32_16x16x64_i8 v[110:113], v[130:133], v[184:187], v[110:113]
	v_mfma_i32_16x16x64_i8 v[106:109], v[138:141], v[184:187], v[106:109]
	v_mfma_i32_16x16x64_i8 v[94:97], v[130:133], v[192:195], v[94:97]
	v_mfma_i32_16x16x64_i8 v[90:93], v[138:141], v[192:195], v[90:93]
	v_mfma_i32_16x16x64_i8 v[78:81], v[130:133], v[200:203], v[78:81]
	v_mfma_i32_16x16x64_i8 v[74:77], v[138:141], v[200:203], v[74:77]
	v_mfma_i32_16x16x64_i8 v[126:129], v[134:137], v[180:183], v[126:129]
	v_mfma_i32_16x16x64_i8 v[122:125], v[142:145], v[180:183], v[122:125]
	v_mfma_i32_16x16x64_i8 v[110:113], v[134:137], v[188:191], v[110:113]
	v_mfma_i32_16x16x64_i8 v[106:109], v[142:145], v[188:191], v[106:109]
	v_mfma_i32_16x16x64_i8 v[94:97], v[134:137], v[196:199], v[94:97]
	v_mfma_i32_16x16x64_i8 v[90:93], v[142:145], v[196:199], v[90:93]
	v_mfma_i32_16x16x64_i8 v[78:81], v[134:137], v[204:207], v[78:81]
	v_mfma_i32_16x16x64_i8 v[74:77], v[142:145], v[204:207], v[74:77]
	s_setprio 0
	s_setprio 1
	v_mfma_i32_16x16x64_i8 v[118:121], v[156:159], v[176:179], v[118:121]
	v_mfma_i32_16x16x64_i8 v[114:117], v[168:171], v[176:179], v[114:117]
	v_mfma_i32_16x16x64_i8 v[102:105], v[156:159], v[184:187], v[102:105]
	v_mfma_i32_16x16x64_i8 v[98:101], v[168:171], v[184:187], v[98:101]
	v_mfma_i32_16x16x64_i8 v[86:89], v[156:159], v[192:195], v[86:89]
	v_mfma_i32_16x16x64_i8 v[82:85], v[168:171], v[192:195], v[82:85]
	v_mfma_i32_16x16x64_i8 v[70:73], v[156:159], v[200:203], v[70:73]
	v_mfma_i32_16x16x64_i8 v[66:69], v[168:171], v[200:203], v[66:69]
	v_mfma_i32_16x16x64_i8 v[118:121], v[164:167], v[180:183], v[118:121]
	v_mfma_i32_16x16x64_i8 v[114:117], v[172:175], v[180:183], v[114:117]
	v_mfma_i32_16x16x64_i8 v[102:105], v[164:167], v[188:191], v[102:105]
	v_mfma_i32_16x16x64_i8 v[98:101], v[172:175], v[188:191], v[98:101]
	v_mfma_i32_16x16x64_i8 v[86:89], v[164:167], v[196:199], v[86:89]
	v_mfma_i32_16x16x64_i8 v[82:85], v[172:175], v[196:199], v[82:85]
	v_mfma_i32_16x16x64_i8 v[70:73], v[164:167], v[204:207], v[70:73]
	v_mfma_i32_16x16x64_i8 v[66:69], v[172:175], v[204:207], v[66:69]
	s_setprio 0
	s_barrier
	s_add_i32 s4, s48, s37
	v_lshl_add_u64 v[208:209], s[28:29], 0, v[0:1]
	s_mov_b32 m0, s4
	ds_read_b128 v[176:179], v163 offset:16384
	ds_read_b128 v[180:183], v163 offset:17408
	ds_read_b128 v[184:187], v163 offset:18432
	ds_read_b128 v[188:191], v163 offset:19456
	ds_read_b128 v[192:195], v163 offset:20480
	ds_read_b128 v[196:199], v163 offset:21504
	ds_read_b128 v[200:203], v163 offset:22528
	ds_read_b128 v[204:207], v163 offset:23552
	global_load_lds_dwordx4 v[208:209], off
	s_add_i32 m0, s4, 0x2000
	s_add_u32 s4, s28, 0x20000
	v_lshl_add_u64 v[210:211], s[28:29], 0, v[146:147]
	s_addc_u32 s5, s29, 0
	s_add_i32 s48, s50, s37
	global_load_lds_dwordx4 v[210:211], off
	v_lshl_add_u64 v[212:213], s[4:5], 0, v[0:1]
	s_mov_b32 m0, s48
	v_lshl_add_u64 v[214:215], s[30:31], 0, v[148:149]
	global_load_lds_dwordx4 v[212:213], off
	v_lshl_add_u64 v[212:213], s[4:5], 0, v[146:147]
	s_add_i32 m0, s48, 0x2000
	s_nop 0
	global_load_lds_dwordx4 v[212:213], off
	v_lshl_add_u64 v[212:213], s[30:31], 0, v[150:151]
	s_mov_b32 m0, s40
	s_nop 0
	global_load_lds_dwordx4 v[212:213], off
	s_mov_b32 m0, s41
	s_nop 0
	global_load_lds_dwordx4 v[214:215], off
	s_waitcnt vmcnt(8)
	s_waitcnt lgkmcnt(0)
	s_barrier
	s_setprio 1
	s_waitcnt lgkmcnt(0)
	v_mfma_i32_16x16x64_i8 v[62:65], v[130:133], v[176:179], v[62:65]
	v_mfma_i32_16x16x64_i8 v[58:61], v[138:141], v[176:179], v[58:61]
	v_mfma_i32_16x16x64_i8 v[46:49], v[130:133], v[184:187], v[46:49]
	v_mfma_i32_16x16x64_i8 v[42:45], v[138:141], v[184:187], v[42:45]
	v_mfma_i32_16x16x64_i8 v[30:33], v[130:133], v[192:195], v[30:33]
	v_mfma_i32_16x16x64_i8 v[26:29], v[138:141], v[192:195], v[26:29]
	v_mfma_i32_16x16x64_i8 v[14:17], v[130:133], v[200:203], v[14:17]
	v_mfma_i32_16x16x64_i8 v[10:13], v[138:141], v[200:203], v[10:13]
	v_mfma_i32_16x16x64_i8 v[62:65], v[134:137], v[180:183], v[62:65]
	v_mfma_i32_16x16x64_i8 v[58:61], v[142:145], v[180:183], v[58:61]
	v_mfma_i32_16x16x64_i8 v[46:49], v[134:137], v[188:191], v[46:49]
	v_mfma_i32_16x16x64_i8 v[42:45], v[142:145], v[188:191], v[42:45]
	v_mfma_i32_16x16x64_i8 v[30:33], v[134:137], v[196:199], v[30:33]
	v_mfma_i32_16x16x64_i8 v[26:29], v[142:145], v[196:199], v[26:29]
	v_mfma_i32_16x16x64_i8 v[14:17], v[134:137], v[204:207], v[14:17]
	v_mfma_i32_16x16x64_i8 v[10:13], v[142:145], v[204:207], v[10:13]
	s_setprio 0
	s_setprio 1
	v_mfma_i32_16x16x64_i8 v[54:57], v[156:159], v[176:179], v[54:57]
	v_mfma_i32_16x16x64_i8 v[50:53], v[168:171], v[176:179], v[50:53]
	v_mfma_i32_16x16x64_i8 v[38:41], v[156:159], v[184:187], v[38:41]
	v_mfma_i32_16x16x64_i8 v[34:37], v[168:171], v[184:187], v[34:37]
	v_mfma_i32_16x16x64_i8 v[22:25], v[156:159], v[192:195], v[22:25]
	v_mfma_i32_16x16x64_i8 v[18:21], v[168:171], v[192:195], v[18:21]
	v_mfma_i32_16x16x64_i8 v[6:9], v[156:159], v[200:203], v[6:9]
	v_mfma_i32_16x16x64_i8 v[2:5], v[168:171], v[200:203], v[2:5]
	v_mfma_i32_16x16x64_i8 v[54:57], v[164:167], v[180:183], v[54:57]
	v_mfma_i32_16x16x64_i8 v[50:53], v[172:175], v[180:183], v[50:53]
	v_mfma_i32_16x16x64_i8 v[38:41], v[164:167], v[188:191], v[38:41]
	v_mfma_i32_16x16x64_i8 v[34:37], v[172:175], v[188:191], v[34:37]
	v_mfma_i32_16x16x64_i8 v[22:25], v[164:167], v[196:199], v[22:25]
	v_mfma_i32_16x16x64_i8 v[18:21], v[172:175], v[196:199], v[18:21]
	v_mfma_i32_16x16x64_i8 v[6:9], v[164:167], v[204:207], v[6:9]
	v_mfma_i32_16x16x64_i8 v[2:5], v[172:175], v[204:207], v[2:5]
	s_setprio 0
	s_barrier
	s_add_i32 s48, 0, 0x18000
	s_add_i32 s50, 0, 0x1c000
	v_add_u32_e32 v142, s48, v161
	v_add_u32_e32 v160, s50, v161
	ds_read_b128 v[130:133], v142
	ds_read_b128 v[134:137], v142 offset:1024
	ds_read_b128 v[138:141], v142 offset:2048
	ds_read_b128 v[142:145], v142 offset:3072
	ds_read_b128 v[156:159], v160
	ds_read_b128 v[164:167], v160 offset:1024
	ds_read_b128 v[168:171], v160 offset:2048
	ds_read_b128 v[172:175], v160 offset:3072
	s_add_u32 s4, s30, 0x20000
	s_addc_u32 s5, s31, 0
	s_mov_b32 m0, s49
	v_lshl_add_u64 v[216:217], s[4:5], 0, v[150:151]
	ds_read_b128 v[176:179], v163 offset:32768
	ds_read_b128 v[180:183], v163 offset:33792
	ds_read_b128 v[184:187], v163 offset:34816
	ds_read_b128 v[188:191], v163 offset:35840
	ds_read_b128 v[192:195], v163 offset:36864
	ds_read_b128 v[196:199], v163 offset:37888
	ds_read_b128 v[200:203], v163 offset:38912
	ds_read_b128 v[204:207], v163 offset:39936
	global_load_lds_dwordx4 v[216:217], off
	v_lshl_add_u64 v[216:217], s[4:5], 0, v[148:149]
	s_mov_b32 m0, s52
	s_nop 0
	global_load_lds_dwordx4 v[216:217], off
	s_waitcnt vmcnt(8)
	s_waitcnt lgkmcnt(0)
	s_barrier
	s_setprio 1
	s_waitcnt lgkmcnt(0)
	v_mfma_i32_16x16x64_i8 v[126:129], v[130:133], v[176:179], v[126:129]
	v_mfma_i32_16x16x64_i8 v[122:125], v[138:141], v[176:179], v[122:125]
	v_mfma_i32_16x16x64_i8 v[110:113], v[130:133], v[184:187], v[110:113]
	v_mfma_i32_16x16x64_i8 v[106:109], v[138:141], v[184:187], v[106:109]
	v_mfma_i32_16x16x64_i8 v[94:97], v[130:133], v[192:195], v[94:97]
	v_mfma_i32_16x16x64_i8 v[90:93], v[138:141], v[192:195], v[90:93]
	v_mfma_i32_16x16x64_i8 v[78:81], v[130:133], v[200:203], v[78:81]
	v_mfma_i32_16x16x64_i8 v[74:77], v[138:141], v[200:203], v[74:77]
	v_mfma_i32_16x16x64_i8 v[126:129], v[134:137], v[180:183], v[126:129]
	v_mfma_i32_16x16x64_i8 v[122:125], v[142:145], v[180:183], v[122:125]
	v_mfma_i32_16x16x64_i8 v[110:113], v[134:137], v[188:191], v[110:113]
	v_mfma_i32_16x16x64_i8 v[106:109], v[142:145], v[188:191], v[106:109]
	v_mfma_i32_16x16x64_i8 v[94:97], v[134:137], v[196:199], v[94:97]
	v_mfma_i32_16x16x64_i8 v[90:93], v[142:145], v[196:199], v[90:93]
	v_mfma_i32_16x16x64_i8 v[78:81], v[134:137], v[204:207], v[78:81]
	v_mfma_i32_16x16x64_i8 v[74:77], v[142:145], v[204:207], v[74:77]
	s_setprio 0
	s_setprio 1
	v_mfma_i32_16x16x64_i8 v[118:121], v[156:159], v[176:179], v[118:121]
	v_mfma_i32_16x16x64_i8 v[114:117], v[168:171], v[176:179], v[114:117]
	v_mfma_i32_16x16x64_i8 v[102:105], v[156:159], v[184:187], v[102:105]
	v_mfma_i32_16x16x64_i8 v[98:101], v[168:171], v[184:187], v[98:101]
	v_mfma_i32_16x16x64_i8 v[86:89], v[156:159], v[192:195], v[86:89]
	v_mfma_i32_16x16x64_i8 v[82:85], v[168:171], v[192:195], v[82:85]
	v_mfma_i32_16x16x64_i8 v[70:73], v[156:159], v[200:203], v[70:73]
	v_mfma_i32_16x16x64_i8 v[66:69], v[168:171], v[200:203], v[66:69]
	v_mfma_i32_16x16x64_i8 v[118:121], v[164:167], v[180:183], v[118:121]
	v_mfma_i32_16x16x64_i8 v[114:117], v[172:175], v[180:183], v[114:117]
	v_mfma_i32_16x16x64_i8 v[102:105], v[164:167], v[188:191], v[102:105]
	v_mfma_i32_16x16x64_i8 v[98:101], v[172:175], v[188:191], v[98:101]
	v_mfma_i32_16x16x64_i8 v[86:89], v[164:167], v[196:199], v[86:89]
	v_mfma_i32_16x16x64_i8 v[82:85], v[172:175], v[196:199], v[82:85]
	v_mfma_i32_16x16x64_i8 v[70:73], v[164:167], v[204:207], v[70:73]
	v_mfma_i32_16x16x64_i8 v[66:69], v[172:175], v[204:207], v[66:69]
	s_setprio 0
	s_barrier
	s_add_i32 s4, s48, s37
	v_lshl_add_u64 v[208:209], v[208:209], 0, s[56:57]
	s_mov_b32 m0, s4
	ds_read_b128 v[176:179], v163 offset:49152
	ds_read_b128 v[180:183], v163 offset:50176
	ds_read_b128 v[184:187], v163 offset:51200
	ds_read_b128 v[188:191], v163 offset:52224
	ds_read_b128 v[192:195], v163 offset:53248
	ds_read_b128 v[196:199], v163 offset:54272
	ds_read_b128 v[200:203], v163 offset:55296
	ds_read_b128 v[204:207], v163 offset:56320
	global_load_lds_dwordx4 v[208:209], off
	s_add_i32 m0, s4, 0x2000
	s_add_u32 s4, s28, 0x20080
	v_lshl_add_u64 v[208:209], v[210:211], 0, s[56:57]
	s_addc_u32 s5, s29, 0
	s_add_i32 s28, s50, s37
	global_load_lds_dwordx4 v[208:209], off
	v_lshl_add_u64 v[208:209], s[4:5], 0, v[0:1]
	s_mov_b32 m0, s28
	s_nop 0
	global_load_lds_dwordx4 v[208:209], off
	v_lshl_add_u64 v[208:209], s[4:5], 0, v[146:147]
	s_add_i32 m0, s28, 0x2000
	s_nop 0
	global_load_lds_dwordx4 v[208:209], off
	v_lshl_add_u64 v[208:209], v[212:213], 0, s[56:57]
	s_mov_b32 m0, s62
	s_nop 0
	global_load_lds_dwordx4 v[208:209], off
	v_lshl_add_u64 v[208:209], v[214:215], 0, s[56:57]
	s_mov_b32 m0, s63
	s_nop 0
	global_load_lds_dwordx4 v[208:209], off
	s_waitcnt vmcnt(8)
	s_waitcnt lgkmcnt(0)
	s_barrier
	s_setprio 1
	s_waitcnt lgkmcnt(0)
	v_mfma_i32_16x16x64_i8 v[62:65], v[130:133], v[176:179], v[62:65]
	v_mfma_i32_16x16x64_i8 v[58:61], v[138:141], v[176:179], v[58:61]
	v_mfma_i32_16x16x64_i8 v[46:49], v[130:133], v[184:187], v[46:49]
	v_mfma_i32_16x16x64_i8 v[42:45], v[138:141], v[184:187], v[42:45]
	v_mfma_i32_16x16x64_i8 v[30:33], v[130:133], v[192:195], v[30:33]
	v_mfma_i32_16x16x64_i8 v[26:29], v[138:141], v[192:195], v[26:29]
	v_mfma_i32_16x16x64_i8 v[14:17], v[130:133], v[200:203], v[14:17]
	v_mfma_i32_16x16x64_i8 v[10:13], v[138:141], v[200:203], v[10:13]
	v_mfma_i32_16x16x64_i8 v[62:65], v[134:137], v[180:183], v[62:65]
	v_mfma_i32_16x16x64_i8 v[58:61], v[142:145], v[180:183], v[58:61]
	v_mfma_i32_16x16x64_i8 v[46:49], v[134:137], v[188:191], v[46:49]
	v_mfma_i32_16x16x64_i8 v[42:45], v[142:145], v[188:191], v[42:45]
	v_mfma_i32_16x16x64_i8 v[30:33], v[134:137], v[196:199], v[30:33]
	v_mfma_i32_16x16x64_i8 v[26:29], v[142:145], v[196:199], v[26:29]
	v_mfma_i32_16x16x64_i8 v[14:17], v[134:137], v[204:207], v[14:17]
	v_mfma_i32_16x16x64_i8 v[10:13], v[142:145], v[204:207], v[10:13]
	s_setprio 0
	s_setprio 1
	v_mfma_i32_16x16x64_i8 v[54:57], v[156:159], v[176:179], v[54:57]
	v_mfma_i32_16x16x64_i8 v[50:53], v[168:171], v[176:179], v[50:53]
	v_mfma_i32_16x16x64_i8 v[38:41], v[156:159], v[184:187], v[38:41]
	v_mfma_i32_16x16x64_i8 v[34:37], v[168:171], v[184:187], v[34:37]
	v_mfma_i32_16x16x64_i8 v[22:25], v[156:159], v[192:195], v[22:25]
	v_mfma_i32_16x16x64_i8 v[18:21], v[168:171], v[192:195], v[18:21]
	v_mfma_i32_16x16x64_i8 v[6:9], v[156:159], v[200:203], v[6:9]
	v_mfma_i32_16x16x64_i8 v[2:5], v[168:171], v[200:203], v[2:5]
	v_mfma_i32_16x16x64_i8 v[54:57], v[164:167], v[180:183], v[54:57]
	v_mfma_i32_16x16x64_i8 v[50:53], v[172:175], v[180:183], v[50:53]
	v_mfma_i32_16x16x64_i8 v[38:41], v[164:167], v[188:191], v[38:41]
	v_mfma_i32_16x16x64_i8 v[34:37], v[172:175], v[188:191], v[34:37]
	v_mfma_i32_16x16x64_i8 v[22:25], v[164:167], v[196:199], v[22:25]
	v_mfma_i32_16x16x64_i8 v[18:21], v[172:175], v[196:199], v[18:21]
	v_mfma_i32_16x16x64_i8 v[6:9], v[164:167], v[204:207], v[6:9]
	v_mfma_i32_16x16x64_i8 v[2:5], v[172:175], v[204:207], v[2:5]
	s_setprio 0
	s_add_i32 s88, s88, 2
	s_add_u32 s26, s26, 0x100
	s_addc_u32 s27, s27, 0
	s_add_u32 s75, s75, 0x100
	s_addc_u32 s80, s80, 0
	s_cmp_gt_u32 s88, 5
	s_barrier
	s_cbranch_scc0 .LBB0_195
	v_mbcnt_lo_u32_b32 v156, -1, 0
	v_mbcnt_hi_u32_b32 v156, -1, v156
	s_lshl_b32 s4, s44, 8
	s_lshl_b32 s5, s69, 8
	v_ashrrev_i32_e32 v130, 1, v156
	s_add_i32 s4, s4, s45
	s_or_b32 s5, s5, s59
	v_and_b32_e32 v130, -8, v130
	v_add_u32_e32 v168, s5, v130
	v_and_or_b32 v170, v156, 15, s4
	v_ashrrev_i32_e32 v169, 31, v168
	v_ashrrev_i32_e32 v171, 31, v170
	v_lshl_add_u64 v[134:135], v[168:169], 2, s[12:13]
	v_lshl_add_u64 v[156:157], v[170:171], 2, s[14:15]
	global_load_dwordx4 v[138:141], v[134:135], off offset:16
	global_load_dwordx4 v[142:145], v[134:135], off
	global_load_dwordx4 v[130:133], v[134:135], off offset:528
	s_nop 0
	global_load_dwordx4 v[134:137], v[134:135], off offset:512
	s_nop 0
	global_load_dword v160, v[156:157], off
	global_load_dword v162, v[156:157], off offset:64
	global_load_dword v164, v[156:157], off offset:128
	global_load_dword v165, v[156:157], off offset:192
	global_load_dword v167, v[156:157], off offset:512
	global_load_dword v173, v[156:157], off offset:576
	global_load_dword v175, v[156:157], off offset:640
	global_load_dword v176, v[156:157], off offset:704
	s_and_b64 vcc, exec, s[16:17]
	s_mov_b64 s[88:89], 0xe0080
	s_cbranch_vccz .LBB0_198
	s_barrier

.LBB0_215:
	s_add_u32 s4, s28, 0xfffe0080
	s_addc_u32 s5, s29, -1
	s_add_i32 s48, 0, 0x10000
	s_cmp_eq_u32 s96, 4
	s_cselect_b32 s35, s23, s5
	s_cselect_b32 s34, s75, s4
	s_cselect_b32 s31, s21, s89
	s_cselect_b32 s30, s80, s88
	s_add_i32 s49, 0, 0x14000
	v_add_u32_e32 v156, s48, v153
	v_add_u32_e32 v172, s49, v153
	ds_read_b128 v[140:143], v156
	ds_read_b128 v[144:147], v156 offset:1024
	ds_read_b128 v[148:151], v156 offset:2048
	ds_read_b128 v[156:159], v156 offset:3072
	ds_read_b128 v[160:163], v172
	ds_read_b128 v[164:167], v172 offset:1024
	ds_read_b128 v[168:171], v172 offset:2048
	ds_read_b128 v[172:175], v172 offset:3072
	v_lshl_add_u64 v[208:209], s[28:29], 0, v[136:137]
	s_add_i32 m0, s52, 0xc000
	ds_read_b128 v[176:179], v155
	ds_read_b128 v[180:183], v155 offset:1024
	ds_read_b128 v[184:187], v155 offset:2048
	ds_read_b128 v[188:191], v155 offset:3072
	ds_read_b128 v[192:195], v155 offset:4096
	ds_read_b128 v[196:199], v155 offset:5120
	ds_read_b128 v[200:203], v155 offset:6144
	ds_read_b128 v[204:207], v155 offset:7168
	global_load_lds_dwordx4 v[208:209], off
	v_lshl_add_u64 v[208:209], s[28:29], 0, v[138:139]
	s_add_i32 m0, s52, 0xe000
	s_nop 0
	global_load_lds_dwordx4 v[208:209], off
	s_waitcnt vmcnt(8)
	s_waitcnt lgkmcnt(0)
	s_barrier
	s_setprio 1
	s_waitcnt lgkmcnt(0)
	v_mfma_i32_16x16x64_i8 v[126:129], v[140:143], v[176:179], v[126:129]
	v_mfma_i32_16x16x64_i8 v[122:125], v[148:151], v[176:179], v[122:125]
	v_mfma_i32_16x16x64_i8 v[118:121], v[140:143], v[184:187], v[118:121]
	v_mfma_i32_16x16x64_i8 v[114:117], v[148:151], v[184:187], v[114:117]
	v_mfma_i32_16x16x64_i8 v[110:113], v[140:143], v[192:195], v[110:113]
	v_mfma_i32_16x16x64_i8 v[106:109], v[148:151], v[192:195], v[106:109]
	v_mfma_i32_16x16x64_i8 v[102:105], v[140:143], v[200:203], v[102:105]
	v_mfma_i32_16x16x64_i8 v[98:101], v[148:151], v[200:203], v[98:101]
	v_mfma_i32_16x16x64_i8 v[126:129], v[144:147], v[180:183], v[126:129]
	v_mfma_i32_16x16x64_i8 v[122:125], v[156:159], v[180:183], v[122:125]
	v_mfma_i32_16x16x64_i8 v[118:121], v[144:147], v[188:191], v[118:121]
	v_mfma_i32_16x16x64_i8 v[114:117], v[156:159], v[188:191], v[114:117]
	v_mfma_i32_16x16x64_i8 v[110:113], v[144:147], v[196:199], v[110:113]
	v_mfma_i32_16x16x64_i8 v[106:109], v[156:159], v[196:199], v[106:109]
	v_mfma_i32_16x16x64_i8 v[102:105], v[144:147], v[204:207], v[102:105]
	v_mfma_i32_16x16x64_i8 v[98:101], v[156:159], v[204:207], v[98:101]
	s_setprio 0
	s_setprio 1
	v_mfma_i32_16x16x64_i8 v[62:65], v[160:163], v[176:179], v[62:65]
	v_mfma_i32_16x16x64_i8 v[58:61], v[168:171], v[176:179], v[58:61]
	v_mfma_i32_16x16x64_i8 v[54:57], v[160:163], v[184:187], v[54:57]
	v_mfma_i32_16x16x64_i8 v[50:53], v[168:171], v[184:187], v[50:53]
	v_mfma_i32_16x16x64_i8 v[46:49], v[160:163], v[192:195], v[46:49]
	v_mfma_i32_16x16x64_i8 v[42:45], v[168:171], v[192:195], v[42:45]
	v_mfma_i32_16x16x64_i8 v[38:41], v[160:163], v[200:203], v[38:41]
	v_mfma_i32_16x16x64_i8 v[34:37], v[168:171], v[200:203], v[34:37]
	v_mfma_i32_16x16x64_i8 v[62:65], v[164:167], v[180:183], v[62:65]
	v_mfma_i32_16x16x64_i8 v[58:61], v[172:175], v[180:183], v[58:61]
	v_mfma_i32_16x16x64_i8 v[54:57], v[164:167], v[188:191], v[54:57]
	v_mfma_i32_16x16x64_i8 v[50:53], v[172:175], v[188:191], v[50:53]
	v_mfma_i32_16x16x64_i8 v[46:49], v[164:167], v[196:199], v[46:49]
	v_mfma_i32_16x16x64_i8 v[42:45], v[172:175], v[196:199], v[42:45]
	v_mfma_i32_16x16x64_i8 v[38:41], v[164:167], v[204:207], v[38:41]
	v_mfma_i32_16x16x64_i8 v[34:37], v[172:175], v[204:207], v[34:37]
	s_setprio 0
	s_barrier
	s_add_i32 s4, s48, s45
	v_lshl_add_u64 v[208:209], s[30:31], 0, v[0:1]
	s_mov_b32 m0, s4
	ds_read_b128 v[176:179], v155 offset:16384
	ds_read_b128 v[180:183], v155 offset:17408
	ds_read_b128 v[184:187], v155 offset:18432
	ds_read_b128 v[188:191], v155 offset:19456
	ds_read_b128 v[192:195], v155 offset:20480
	ds_read_b128 v[196:199], v155 offset:21504
	ds_read_b128 v[200:203], v155 offset:22528
	ds_read_b128 v[204:207], v155 offset:23552
	global_load_lds_dwordx4 v[208:209], off
	s_add_i32 m0, s4, 0x2000
	s_add_u32 s4, s30, 0x20000
	v_lshl_add_u64 v[210:211], s[30:31], 0, v[130:131]
	s_addc_u32 s5, s31, 0
	s_add_i32 s48, s49, s45
	global_load_lds_dwordx4 v[210:211], off
	v_lshl_add_u64 v[212:213], s[4:5], 0, v[0:1]
	s_mov_b32 m0, s48
	v_lshl_add_u64 v[214:215], s[34:35], 0, v[132:133]
	global_load_lds_dwordx4 v[212:213], off
	v_lshl_add_u64 v[212:213], s[4:5], 0, v[130:131]
	s_add_i32 m0, s48, 0x2000
	s_nop 0
	global_load_lds_dwordx4 v[212:213], off
	v_lshl_add_u64 v[212:213], s[34:35], 0, v[134:135]
	s_mov_b32 m0, s52
	s_nop 0
	global_load_lds_dwordx4 v[212:213], off
	s_mov_b32 m0, s59
	s_nop 0
	global_load_lds_dwordx4 v[214:215], off
	s_waitcnt vmcnt(8)
	s_waitcnt lgkmcnt(0)
	s_barrier
	s_setprio 1
	s_waitcnt lgkmcnt(0)
	v_mfma_i32_16x16x64_i8 v[94:97], v[140:143], v[176:179], v[94:97]
	v_mfma_i32_16x16x64_i8 v[90:93], v[148:151], v[176:179], v[90:93]
	v_mfma_i32_16x16x64_i8 v[86:89], v[140:143], v[184:187], v[86:89]
	v_mfma_i32_16x16x64_i8 v[82:85], v[148:151], v[184:187], v[82:85]
	v_mfma_i32_16x16x64_i8 v[78:81], v[140:143], v[192:195], v[78:81]
	v_mfma_i32_16x16x64_i8 v[74:77], v[148:151], v[192:195], v[74:77]
	v_mfma_i32_16x16x64_i8 v[70:73], v[140:143], v[200:203], v[70:73]
	v_mfma_i32_16x16x64_i8 v[66:69], v[148:151], v[200:203], v[66:69]
	v_mfma_i32_16x16x64_i8 v[94:97], v[144:147], v[180:183], v[94:97]
	v_mfma_i32_16x16x64_i8 v[90:93], v[156:159], v[180:183], v[90:93]
	v_mfma_i32_16x16x64_i8 v[86:89], v[144:147], v[188:191], v[86:89]
	v_mfma_i32_16x16x64_i8 v[82:85], v[156:159], v[188:191], v[82:85]
	v_mfma_i32_16x16x64_i8 v[78:81], v[144:147], v[196:199], v[78:81]
	v_mfma_i32_16x16x64_i8 v[74:77], v[156:159], v[196:199], v[74:77]
	v_mfma_i32_16x16x64_i8 v[70:73], v[144:147], v[204:207], v[70:73]
	v_mfma_i32_16x16x64_i8 v[66:69], v[156:159], v[204:207], v[66:69]
	s_setprio 0
	s_setprio 1
	v_mfma_i32_16x16x64_i8 v[30:33], v[160:163], v[176:179], v[30:33]
	v_mfma_i32_16x16x64_i8 v[26:29], v[168:171], v[176:179], v[26:29]
	v_mfma_i32_16x16x64_i8 v[22:25], v[160:163], v[184:187], v[22:25]
	v_mfma_i32_16x16x64_i8 v[18:21], v[168:171], v[184:187], v[18:21]
	v_mfma_i32_16x16x64_i8 v[14:17], v[160:163], v[192:195], v[14:17]
	v_mfma_i32_16x16x64_i8 v[10:13], v[168:171], v[192:195], v[10:13]
	v_mfma_i32_16x16x64_i8 v[6:9], v[160:163], v[200:203], v[6:9]
	v_mfma_i32_16x16x64_i8 v[2:5], v[168:171], v[200:203], v[2:5]
	v_mfma_i32_16x16x64_i8 v[30:33], v[164:167], v[180:183], v[30:33]
	v_mfma_i32_16x16x64_i8 v[26:29], v[172:175], v[180:183], v[26:29]
	v_mfma_i32_16x16x64_i8 v[22:25], v[164:167], v[188:191], v[22:25]
	v_mfma_i32_16x16x64_i8 v[18:21], v[172:175], v[188:191], v[18:21]
	v_mfma_i32_16x16x64_i8 v[14:17], v[164:167], v[196:199], v[14:17]
	v_mfma_i32_16x16x64_i8 v[10:13], v[172:175], v[196:199], v[10:13]
	v_mfma_i32_16x16x64_i8 v[6:9], v[164:167], v[204:207], v[6:9]
	v_mfma_i32_16x16x64_i8 v[2:5], v[172:175], v[204:207], v[2:5]
	s_setprio 0
	s_barrier
	s_add_i32 s48, 0, 0x18000
	s_add_i32 s49, 0, 0x1c000
	v_add_u32_e32 v156, s48, v153
	v_add_u32_e32 v172, s49, v153
	ds_read_b128 v[140:143], v156
	ds_read_b128 v[144:147], v156 offset:1024
	ds_read_b128 v[148:151], v156 offset:2048
	ds_read_b128 v[156:159], v156 offset:3072
	ds_read_b128 v[160:163], v172
	ds_read_b128 v[164:167], v172 offset:1024
	ds_read_b128 v[168:171], v172 offset:2048
	ds_read_b128 v[172:175], v172 offset:3072
	s_add_u32 s4, s34, 0x20000
	s_addc_u32 s5, s35, 0
	s_mov_b32 m0, s62
	v_lshl_add_u64 v[216:217], s[4:5], 0, v[134:135]
	ds_read_b128 v[176:179], v155 offset:32768
	ds_read_b128 v[180:183], v155 offset:33792
	ds_read_b128 v[184:187], v155 offset:34816
	ds_read_b128 v[188:191], v155 offset:35840
	ds_read_b128 v[192:195], v155 offset:36864
	ds_read_b128 v[196:199], v155 offset:37888
	ds_read_b128 v[200:203], v155 offset:38912
	ds_read_b128 v[204:207], v155 offset:39936
	global_load_lds_dwordx4 v[216:217], off
	v_lshl_add_u64 v[216:217], s[4:5], 0, v[132:133]
	s_mov_b32 m0, s63
	s_nop 0
	global_load_lds_dwordx4 v[216:217], off
	s_waitcnt vmcnt(8)
	s_waitcnt lgkmcnt(0)
	s_barrier
	s_setprio 1
	s_waitcnt lgkmcnt(0)
	v_mfma_i32_16x16x64_i8 v[126:129], v[140:143], v[176:179], v[126:129]
	v_mfma_i32_16x16x64_i8 v[122:125], v[148:151], v[176:179], v[122:125]
	v_mfma_i32_16x16x64_i8 v[118:121], v[140:143], v[184:187], v[118:121]
	v_mfma_i32_16x16x64_i8 v[114:117], v[148:151], v[184:187], v[114:117]
	v_mfma_i32_16x16x64_i8 v[110:113], v[140:143], v[192:195], v[110:113]
	v_mfma_i32_16x16x64_i8 v[106:109], v[148:151], v[192:195], v[106:109]
	v_mfma_i32_16x16x64_i8 v[102:105], v[140:143], v[200:203], v[102:105]
	v_mfma_i32_16x16x64_i8 v[98:101], v[148:151], v[200:203], v[98:101]
	v_mfma_i32_16x16x64_i8 v[126:129], v[144:147], v[180:183], v[126:129]
	v_mfma_i32_16x16x64_i8 v[122:125], v[156:159], v[180:183], v[122:125]
	v_mfma_i32_16x16x64_i8 v[118:121], v[144:147], v[188:191], v[118:121]
	v_mfma_i32_16x16x64_i8 v[114:117], v[156:159], v[188:191], v[114:117]
	v_mfma_i32_16x16x64_i8 v[110:113], v[144:147], v[196:199], v[110:113]
	v_mfma_i32_16x16x64_i8 v[106:109], v[156:159], v[196:199], v[106:109]
	v_mfma_i32_16x16x64_i8 v[102:105], v[144:147], v[204:207], v[102:105]
	v_mfma_i32_16x16x64_i8 v[98:101], v[156:159], v[204:207], v[98:101]
	s_setprio 0
	s_setprio 1
	v_mfma_i32_16x16x64_i8 v[62:65], v[160:163], v[176:179], v[62:65]
	v_mfma_i32_16x16x64_i8 v[58:61], v[168:171], v[176:179], v[58:61]
	v_mfma_i32_16x16x64_i8 v[54:57], v[160:163], v[184:187], v[54:57]
	v_mfma_i32_16x16x64_i8 v[50:53], v[168:171], v[184:187], v[50:53]
	v_mfma_i32_16x16x64_i8 v[46:49], v[160:163], v[192:195], v[46:49]
	v_mfma_i32_16x16x64_i8 v[42:45], v[168:171], v[192:195], v[42:45]
	v_mfma_i32_16x16x64_i8 v[38:41], v[160:163], v[200:203], v[38:41]
	v_mfma_i32_16x16x64_i8 v[34:37], v[168:171], v[200:203], v[34:37]
	v_mfma_i32_16x16x64_i8 v[62:65], v[164:167], v[180:183], v[62:65]
	v_mfma_i32_16x16x64_i8 v[58:61], v[172:175], v[180:183], v[58:61]
	v_mfma_i32_16x16x64_i8 v[54:57], v[164:167], v[188:191], v[54:57]
	v_mfma_i32_16x16x64_i8 v[50:53], v[172:175], v[188:191], v[50:53]
	v_mfma_i32_16x16x64_i8 v[46:49], v[164:167], v[196:199], v[46:49]
	v_mfma_i32_16x16x64_i8 v[42:45], v[172:175], v[196:199], v[42:45]
	v_mfma_i32_16x16x64_i8 v[38:41], v[164:167], v[204:207], v[38:41]
	v_mfma_i32_16x16x64_i8 v[34:37], v[172:175], v[204:207], v[34:37]
	s_setprio 0
	s_barrier
	s_add_i32 s4, s48, s45
	v_lshl_add_u64 v[208:209], v[208:209], 0, s[56:57]
	s_mov_b32 m0, s4
	ds_read_b128 v[176:179], v155 offset:49152
	ds_read_b128 v[180:183], v155 offset:50176
	ds_read_b128 v[184:187], v155 offset:51200
	ds_read_b128 v[188:191], v155 offset:52224
	ds_read_b128 v[192:195], v155 offset:53248
	ds_read_b128 v[196:199], v155 offset:54272
	ds_read_b128 v[200:203], v155 offset:55296
	ds_read_b128 v[204:207], v155 offset:56320
	global_load_lds_dwordx4 v[208:209], off
	s_add_i32 m0, s4, 0x2000
	s_add_u32 s4, s30, 0x20080
	v_lshl_add_u64 v[208:209], v[210:211], 0, s[56:57]
	s_addc_u32 s5, s31, 0
	s_add_i32 s30, s49, s45
	global_load_lds_dwordx4 v[208:209], off
	v_lshl_add_u64 v[208:209], s[4:5], 0, v[0:1]
	s_mov_b32 m0, s30
	s_nop 0
	global_load_lds_dwordx4 v[208:209], off
	v_lshl_add_u64 v[208:209], s[4:5], 0, v[130:131]
	s_add_i32 m0, s30, 0x2000
	s_nop 0
	global_load_lds_dwordx4 v[208:209], off
	v_lshl_add_u64 v[208:209], v[212:213], 0, s[56:57]
	s_mov_b32 m0, s68
	s_nop 0
	global_load_lds_dwordx4 v[208:209], off
	v_lshl_add_u64 v[208:209], v[214:215], 0, s[56:57]
	s_mov_b32 m0, s69
	s_nop 0
	global_load_lds_dwordx4 v[208:209], off
	s_waitcnt vmcnt(8)
	s_waitcnt lgkmcnt(0)
	s_barrier
	s_setprio 1
	s_waitcnt lgkmcnt(0)
	v_mfma_i32_16x16x64_i8 v[94:97], v[140:143], v[176:179], v[94:97]
	v_mfma_i32_16x16x64_i8 v[90:93], v[148:151], v[176:179], v[90:93]
	v_mfma_i32_16x16x64_i8 v[86:89], v[140:143], v[184:187], v[86:89]
	v_mfma_i32_16x16x64_i8 v[82:85], v[148:151], v[184:187], v[82:85]
	v_mfma_i32_16x16x64_i8 v[78:81], v[140:143], v[192:195], v[78:81]
	v_mfma_i32_16x16x64_i8 v[74:77], v[148:151], v[192:195], v[74:77]
	v_mfma_i32_16x16x64_i8 v[70:73], v[140:143], v[200:203], v[70:73]
	v_mfma_i32_16x16x64_i8 v[66:69], v[148:151], v[200:203], v[66:69]
	v_mfma_i32_16x16x64_i8 v[94:97], v[144:147], v[180:183], v[94:97]
	v_mfma_i32_16x16x64_i8 v[90:93], v[156:159], v[180:183], v[90:93]
	v_mfma_i32_16x16x64_i8 v[86:89], v[144:147], v[188:191], v[86:89]
	v_mfma_i32_16x16x64_i8 v[82:85], v[156:159], v[188:191], v[82:85]
	v_mfma_i32_16x16x64_i8 v[78:81], v[144:147], v[196:199], v[78:81]
	v_mfma_i32_16x16x64_i8 v[74:77], v[156:159], v[196:199], v[74:77]
	v_mfma_i32_16x16x64_i8 v[70:73], v[144:147], v[204:207], v[70:73]
	v_mfma_i32_16x16x64_i8 v[66:69], v[156:159], v[204:207], v[66:69]
	s_setprio 0
	s_setprio 1
	v_mfma_i32_16x16x64_i8 v[30:33], v[160:163], v[176:179], v[30:33]
	v_mfma_i32_16x16x64_i8 v[26:29], v[168:171], v[176:179], v[26:29]
	v_mfma_i32_16x16x64_i8 v[22:25], v[160:163], v[184:187], v[22:25]
	v_mfma_i32_16x16x64_i8 v[18:21], v[168:171], v[184:187], v[18:21]
	v_mfma_i32_16x16x64_i8 v[14:17], v[160:163], v[192:195], v[14:17]
	v_mfma_i32_16x16x64_i8 v[10:13], v[168:171], v[192:195], v[10:13]
	v_mfma_i32_16x16x64_i8 v[6:9], v[160:163], v[200:203], v[6:9]
	v_mfma_i32_16x16x64_i8 v[2:5], v[168:171], v[200:203], v[2:5]
	v_mfma_i32_16x16x64_i8 v[30:33], v[164:167], v[180:183], v[30:33]
	v_mfma_i32_16x16x64_i8 v[26:29], v[172:175], v[180:183], v[26:29]
	v_mfma_i32_16x16x64_i8 v[22:25], v[164:167], v[188:191], v[22:25]
	v_mfma_i32_16x16x64_i8 v[18:21], v[172:175], v[188:191], v[18:21]
	v_mfma_i32_16x16x64_i8 v[14:17], v[164:167], v[196:199], v[14:17]
	v_mfma_i32_16x16x64_i8 v[10:13], v[172:175], v[196:199], v[10:13]
	v_mfma_i32_16x16x64_i8 v[6:9], v[164:167], v[204:207], v[6:9]
	v_mfma_i32_16x16x64_i8 v[2:5], v[172:175], v[204:207], v[2:5]
	s_setprio 0
	s_add_i32 s96, s96, 2
	s_add_u32 s28, s28, 0x100
	s_addc_u32 s29, s29, 0
	s_add_u32 s88, s88, 0x100
	s_addc_u32 s89, s89, 0
	s_cmp_gt_u32 s96, 5
	s_barrier
	s_cbranch_scc0 .LBB0_215
	s_and_b64 vcc, exec, s[16:17]
	s_cbranch_vccz .LBB0_218
	s_barrier

.LBB0_883:
	s_add_u32 s4, s10, 0xfffc0080
	s_addc_u32 s5, s11, -1
	s_add_i32 s48, 0, 0x10000
	s_cmp_eq_u32 s75, 12
	s_cselect_b32 s31, s23, s5
	s_cselect_b32 s30, s68, s4
	s_cselect_b32 s29, s21, s71
	s_cselect_b32 s28, s69, s70
	s_add_i32 s50, 0, 0x14000
	v_add_u32_e32 v142, s48, v248
	v_add_u32_e32 v158, s50, v248
	ds_read_b128 v[130:133], v142
	ds_read_b128 v[134:137], v142 offset:1024
	ds_read_b128 v[138:141], v142 offset:2048
	ds_read_b128 v[142:145], v142 offset:3072
	ds_read_b128 v[146:149], v158
	ds_read_b128 v[150:153], v158 offset:1024
	ds_read_b128 v[154:157], v158 offset:2048
	ds_read_b128 v[158:161], v158 offset:3072
	v_lshl_add_u64 v[194:195], s[10:11], 0, v[204:205]
	s_add_i32 m0, s38, 0xc000
	ds_read_b128 v[162:165], v250
	ds_read_b128 v[166:169], v250 offset:1024
	ds_read_b128 v[170:173], v250 offset:2048
	ds_read_b128 v[174:177], v250 offset:3072
	ds_read_b128 v[178:181], v250 offset:4096
	ds_read_b128 v[182:185], v250 offset:5120
	ds_read_b128 v[186:189], v250 offset:6144
	ds_read_b128 v[190:193], v250 offset:7168
	global_load_lds_dwordx4 v[194:195], off
	v_lshl_add_u64 v[194:195], s[10:11], 0, v[206:207]
	s_add_i32 m0, s38, 0xe000
	s_nop 0
	global_load_lds_dwordx4 v[194:195], off
	s_waitcnt vmcnt(8)
	s_waitcnt lgkmcnt(0)
	s_barrier
	s_setprio 1
	s_waitcnt lgkmcnt(0)
	v_mfma_f32_16x16x32_bf16 v[126:129], v[130:133], v[162:165], v[126:129]
	v_mfma_f32_16x16x32_bf16 v[122:125], v[138:141], v[162:165], v[122:125]
	v_mfma_f32_16x16x32_bf16 v[118:121], v[130:133], v[170:173], v[118:121]
	v_mfma_f32_16x16x32_bf16 v[110:113], v[138:141], v[170:173], v[110:113]
	v_mfma_f32_16x16x32_bf16 v[102:105], v[130:133], v[178:181], v[102:105]
	v_mfma_f32_16x16x32_bf16 v[94:97], v[138:141], v[178:181], v[94:97]
	v_mfma_f32_16x16x32_bf16 v[86:89], v[130:133], v[186:189], v[86:89]
	v_mfma_f32_16x16x32_bf16 v[78:81], v[138:141], v[186:189], v[78:81]
	v_mfma_f32_16x16x32_bf16 v[126:129], v[134:137], v[166:169], v[126:129]
	v_mfma_f32_16x16x32_bf16 v[122:125], v[142:145], v[166:169], v[122:125]
	v_mfma_f32_16x16x32_bf16 v[118:121], v[134:137], v[174:177], v[118:121]
	v_mfma_f32_16x16x32_bf16 v[110:113], v[142:145], v[174:177], v[110:113]
	v_mfma_f32_16x16x32_bf16 v[102:105], v[134:137], v[182:185], v[102:105]
	v_mfma_f32_16x16x32_bf16 v[94:97], v[142:145], v[182:185], v[94:97]
	v_mfma_f32_16x16x32_bf16 v[86:89], v[134:137], v[190:193], v[86:89]
	v_mfma_f32_16x16x32_bf16 v[78:81], v[142:145], v[190:193], v[78:81]
	s_setprio 0
	s_setprio 1
	v_mfma_f32_16x16x32_bf16 v[114:117], v[146:149], v[162:165], v[114:117]
	v_mfma_f32_16x16x32_bf16 v[106:109], v[154:157], v[162:165], v[106:109]
	v_mfma_f32_16x16x32_bf16 v[98:101], v[146:149], v[170:173], v[98:101]
	v_mfma_f32_16x16x32_bf16 v[90:93], v[154:157], v[170:173], v[90:93]
	v_mfma_f32_16x16x32_bf16 v[82:85], v[146:149], v[178:181], v[82:85]
	v_mfma_f32_16x16x32_bf16 v[74:77], v[154:157], v[178:181], v[74:77]
	v_mfma_f32_16x16x32_bf16 v[70:73], v[146:149], v[186:189], v[70:73]
	v_mfma_f32_16x16x32_bf16 v[66:69], v[154:157], v[186:189], v[66:69]
	v_mfma_f32_16x16x32_bf16 v[114:117], v[150:153], v[166:169], v[114:117]
	v_mfma_f32_16x16x32_bf16 v[106:109], v[158:161], v[166:169], v[106:109]
	v_mfma_f32_16x16x32_bf16 v[98:101], v[150:153], v[174:177], v[98:101]
	v_mfma_f32_16x16x32_bf16 v[90:93], v[158:161], v[174:177], v[90:93]
	v_mfma_f32_16x16x32_bf16 v[82:85], v[150:153], v[182:185], v[82:85]
	v_mfma_f32_16x16x32_bf16 v[74:77], v[158:161], v[182:185], v[74:77]
	v_mfma_f32_16x16x32_bf16 v[70:73], v[150:153], v[190:193], v[70:73]
	v_mfma_f32_16x16x32_bf16 v[66:69], v[158:161], v[190:193], v[66:69]
	s_setprio 0
	s_barrier
	s_add_i32 s4, s48, s33
	v_lshl_add_u64 v[194:195], s[28:29], 0, v[0:1]
	s_mov_b32 m0, s4
	ds_read_b128 v[162:165], v250 offset:16384
	ds_read_b128 v[166:169], v250 offset:17408
	ds_read_b128 v[170:173], v250 offset:18432
	ds_read_b128 v[174:177], v250 offset:19456
	ds_read_b128 v[178:181], v250 offset:20480
	ds_read_b128 v[182:185], v250 offset:21504
	ds_read_b128 v[186:189], v250 offset:22528
	ds_read_b128 v[190:193], v250 offset:23552
	global_load_lds_dwordx4 v[194:195], off
	s_add_i32 m0, s4, 0x2000
	s_add_u32 s4, s28, 0x40000
	v_lshl_add_u64 v[196:197], s[28:29], 0, v[198:199]
	s_addc_u32 s5, s29, 0
	s_add_i32 s48, s50, s33
	global_load_lds_dwordx4 v[196:197], off
	v_lshl_add_u64 v[208:209], s[4:5], 0, v[0:1]
	s_mov_b32 m0, s48
	v_lshl_add_u64 v[210:211], s[30:31], 0, v[200:201]
	global_load_lds_dwordx4 v[208:209], off
	v_lshl_add_u64 v[208:209], s[4:5], 0, v[198:199]
	s_add_i32 m0, s48, 0x2000
	s_nop 0
	global_load_lds_dwordx4 v[208:209], off
	v_lshl_add_u64 v[208:209], s[30:31], 0, v[202:203]
	s_mov_b32 m0, s38
	s_nop 0
	global_load_lds_dwordx4 v[208:209], off
	s_mov_b32 m0, s39
	s_nop 0
	global_load_lds_dwordx4 v[210:211], off
	s_waitcnt vmcnt(8)
	s_waitcnt lgkmcnt(0)
	s_barrier
	s_setprio 1
	s_waitcnt lgkmcnt(0)
	v_mfma_f32_16x16x32_bf16 v[62:65], v[130:133], v[162:165], v[62:65]
	v_mfma_f32_16x16x32_bf16 v[58:61], v[138:141], v[162:165], v[58:61]
	v_mfma_f32_16x16x32_bf16 v[54:57], v[130:133], v[170:173], v[54:57]
	v_mfma_f32_16x16x32_bf16 v[46:49], v[138:141], v[170:173], v[46:49]
	v_mfma_f32_16x16x32_bf16 v[38:41], v[130:133], v[178:181], v[38:41]
	v_mfma_f32_16x16x32_bf16 v[30:33], v[138:141], v[178:181], v[30:33]
	v_mfma_f32_16x16x32_bf16 v[22:25], v[130:133], v[186:189], v[22:25]
	v_mfma_f32_16x16x32_bf16 v[14:17], v[138:141], v[186:189], v[14:17]
	v_mfma_f32_16x16x32_bf16 v[62:65], v[134:137], v[166:169], v[62:65]
	v_mfma_f32_16x16x32_bf16 v[58:61], v[142:145], v[166:169], v[58:61]
	v_mfma_f32_16x16x32_bf16 v[54:57], v[134:137], v[174:177], v[54:57]
	v_mfma_f32_16x16x32_bf16 v[46:49], v[142:145], v[174:177], v[46:49]
	v_mfma_f32_16x16x32_bf16 v[38:41], v[134:137], v[182:185], v[38:41]
	v_mfma_f32_16x16x32_bf16 v[30:33], v[142:145], v[182:185], v[30:33]
	v_mfma_f32_16x16x32_bf16 v[22:25], v[134:137], v[190:193], v[22:25]
	v_mfma_f32_16x16x32_bf16 v[14:17], v[142:145], v[190:193], v[14:17]
	s_setprio 0
	s_setprio 1
	v_mfma_f32_16x16x32_bf16 v[50:53], v[146:149], v[162:165], v[50:53]
	v_mfma_f32_16x16x32_bf16 v[42:45], v[154:157], v[162:165], v[42:45]
	v_mfma_f32_16x16x32_bf16 v[34:37], v[146:149], v[170:173], v[34:37]
	v_mfma_f32_16x16x32_bf16 v[26:29], v[154:157], v[170:173], v[26:29]
	v_mfma_f32_16x16x32_bf16 v[18:21], v[146:149], v[178:181], v[18:21]
	v_mfma_f32_16x16x32_bf16 v[10:13], v[154:157], v[178:181], v[10:13]
	v_mfma_f32_16x16x32_bf16 v[6:9], v[146:149], v[186:189], v[6:9]
	v_mfma_f32_16x16x32_bf16 v[2:5], v[154:157], v[186:189], v[2:5]
	v_mfma_f32_16x16x32_bf16 v[50:53], v[150:153], v[166:169], v[50:53]
	v_mfma_f32_16x16x32_bf16 v[42:45], v[158:161], v[166:169], v[42:45]
	v_mfma_f32_16x16x32_bf16 v[34:37], v[150:153], v[174:177], v[34:37]
	v_mfma_f32_16x16x32_bf16 v[26:29], v[158:161], v[174:177], v[26:29]
	v_mfma_f32_16x16x32_bf16 v[18:21], v[150:153], v[182:185], v[18:21]
	v_mfma_f32_16x16x32_bf16 v[10:13], v[158:161], v[182:185], v[10:13]
	v_mfma_f32_16x16x32_bf16 v[6:9], v[150:153], v[190:193], v[6:9]
	v_mfma_f32_16x16x32_bf16 v[2:5], v[158:161], v[190:193], v[2:5]
	s_setprio 0
	s_barrier
	s_add_i32 s48, 0, 0x18000
	s_add_i32 s50, 0, 0x1c000
	v_add_u32_e32 v142, s48, v248
	v_add_u32_e32 v158, s50, v248
	ds_read_b128 v[130:133], v142
	ds_read_b128 v[134:137], v142 offset:1024
	ds_read_b128 v[138:141], v142 offset:2048
	ds_read_b128 v[142:145], v142 offset:3072
	ds_read_b128 v[146:149], v158
	ds_read_b128 v[150:153], v158 offset:1024
	ds_read_b128 v[154:157], v158 offset:2048
	ds_read_b128 v[158:161], v158 offset:3072
	s_add_u32 s4, s30, 0x40000
	s_addc_u32 s5, s31, 0
	s_mov_b32 m0, s40
	v_lshl_add_u64 v[212:213], s[4:5], 0, v[202:203]
	ds_read_b128 v[162:165], v250 offset:32768
	ds_read_b128 v[166:169], v250 offset:33792
	ds_read_b128 v[170:173], v250 offset:34816
	ds_read_b128 v[174:177], v250 offset:35840
	ds_read_b128 v[178:181], v250 offset:36864
	ds_read_b128 v[182:185], v250 offset:37888
	ds_read_b128 v[186:189], v250 offset:38912
	ds_read_b128 v[190:193], v250 offset:39936
	global_load_lds_dwordx4 v[212:213], off
	v_lshl_add_u64 v[212:213], s[4:5], 0, v[200:201]
	s_mov_b32 m0, s41
	s_nop 0
	global_load_lds_dwordx4 v[212:213], off
	s_waitcnt vmcnt(8)
	s_waitcnt lgkmcnt(0)
	s_barrier
	s_setprio 1
	s_waitcnt lgkmcnt(0)
	v_mfma_f32_16x16x32_bf16 v[126:129], v[130:133], v[162:165], v[126:129]
	v_mfma_f32_16x16x32_bf16 v[122:125], v[138:141], v[162:165], v[122:125]
	v_mfma_f32_16x16x32_bf16 v[118:121], v[130:133], v[170:173], v[118:121]
	v_mfma_f32_16x16x32_bf16 v[110:113], v[138:141], v[170:173], v[110:113]
	v_mfma_f32_16x16x32_bf16 v[102:105], v[130:133], v[178:181], v[102:105]
	v_mfma_f32_16x16x32_bf16 v[94:97], v[138:141], v[178:181], v[94:97]
	v_mfma_f32_16x16x32_bf16 v[86:89], v[130:133], v[186:189], v[86:89]
	v_mfma_f32_16x16x32_bf16 v[78:81], v[138:141], v[186:189], v[78:81]
	v_mfma_f32_16x16x32_bf16 v[126:129], v[134:137], v[166:169], v[126:129]
	v_mfma_f32_16x16x32_bf16 v[122:125], v[142:145], v[166:169], v[122:125]
	v_mfma_f32_16x16x32_bf16 v[118:121], v[134:137], v[174:177], v[118:121]
	v_mfma_f32_16x16x32_bf16 v[110:113], v[142:145], v[174:177], v[110:113]
	v_mfma_f32_16x16x32_bf16 v[102:105], v[134:137], v[182:185], v[102:105]
	v_mfma_f32_16x16x32_bf16 v[94:97], v[142:145], v[182:185], v[94:97]
	v_mfma_f32_16x16x32_bf16 v[86:89], v[134:137], v[190:193], v[86:89]
	v_mfma_f32_16x16x32_bf16 v[78:81], v[142:145], v[190:193], v[78:81]
	s_setprio 0
	s_setprio 1
	v_mfma_f32_16x16x32_bf16 v[114:117], v[146:149], v[162:165], v[114:117]
	v_mfma_f32_16x16x32_bf16 v[106:109], v[154:157], v[162:165], v[106:109]
	v_mfma_f32_16x16x32_bf16 v[98:101], v[146:149], v[170:173], v[98:101]
	v_mfma_f32_16x16x32_bf16 v[90:93], v[154:157], v[170:173], v[90:93]
	v_mfma_f32_16x16x32_bf16 v[82:85], v[146:149], v[178:181], v[82:85]
	v_mfma_f32_16x16x32_bf16 v[74:77], v[154:157], v[178:181], v[74:77]
	v_mfma_f32_16x16x32_bf16 v[70:73], v[146:149], v[186:189], v[70:73]
	v_mfma_f32_16x16x32_bf16 v[66:69], v[154:157], v[186:189], v[66:69]
	v_mfma_f32_16x16x32_bf16 v[114:117], v[150:153], v[166:169], v[114:117]
	v_mfma_f32_16x16x32_bf16 v[106:109], v[158:161], v[166:169], v[106:109]
	v_mfma_f32_16x16x32_bf16 v[98:101], v[150:153], v[174:177], v[98:101]
	v_mfma_f32_16x16x32_bf16 v[90:93], v[158:161], v[174:177], v[90:93]
	v_mfma_f32_16x16x32_bf16 v[82:85], v[150:153], v[182:185], v[82:85]
	v_mfma_f32_16x16x32_bf16 v[74:77], v[158:161], v[182:185], v[74:77]
	v_mfma_f32_16x16x32_bf16 v[70:73], v[150:153], v[190:193], v[70:73]
	v_mfma_f32_16x16x32_bf16 v[66:69], v[158:161], v[190:193], v[66:69]
	s_setprio 0
	s_barrier
	s_add_i32 s4, s48, s33
	v_lshl_add_u64 v[194:195], v[194:195], 0, s[56:57]
	s_mov_b32 m0, s4
	ds_read_b128 v[162:165], v250 offset:49152
	ds_read_b128 v[166:169], v250 offset:50176
	ds_read_b128 v[170:173], v250 offset:51200
	ds_read_b128 v[174:177], v250 offset:52224
	ds_read_b128 v[178:181], v250 offset:53248
	ds_read_b128 v[182:185], v250 offset:54272
	ds_read_b128 v[186:189], v250 offset:55296
	ds_read_b128 v[190:193], v250 offset:56320
	global_load_lds_dwordx4 v[194:195], off
	s_add_i32 m0, s4, 0x2000
	s_add_u32 s4, s28, 0x40080
	v_lshl_add_u64 v[194:195], v[196:197], 0, s[56:57]
	s_addc_u32 s5, s29, 0
	s_add_i32 s28, s50, s33
	global_load_lds_dwordx4 v[194:195], off
	v_lshl_add_u64 v[194:195], s[4:5], 0, v[0:1]
	s_mov_b32 m0, s28
	s_nop 0
	global_load_lds_dwordx4 v[194:195], off
	v_lshl_add_u64 v[194:195], s[4:5], 0, v[198:199]
	s_add_i32 m0, s28, 0x2000
	s_nop 0
	global_load_lds_dwordx4 v[194:195], off
	v_lshl_add_u64 v[194:195], v[208:209], 0, s[56:57]
	s_mov_b32 m0, s52
	s_nop 0
	global_load_lds_dwordx4 v[194:195], off
	v_lshl_add_u64 v[194:195], v[210:211], 0, s[56:57]
	s_mov_b32 m0, s59
	s_nop 0
	global_load_lds_dwordx4 v[194:195], off
	s_waitcnt vmcnt(8)
	s_waitcnt lgkmcnt(0)
	s_barrier
	s_setprio 1
	s_waitcnt lgkmcnt(0)
	v_mfma_f32_16x16x32_bf16 v[62:65], v[130:133], v[162:165], v[62:65]
	v_mfma_f32_16x16x32_bf16 v[58:61], v[138:141], v[162:165], v[58:61]
	v_mfma_f32_16x16x32_bf16 v[54:57], v[130:133], v[170:173], v[54:57]
	v_mfma_f32_16x16x32_bf16 v[46:49], v[138:141], v[170:173], v[46:49]
	v_mfma_f32_16x16x32_bf16 v[38:41], v[130:133], v[178:181], v[38:41]
	v_mfma_f32_16x16x32_bf16 v[30:33], v[138:141], v[178:181], v[30:33]
	v_mfma_f32_16x16x32_bf16 v[22:25], v[130:133], v[186:189], v[22:25]
	v_mfma_f32_16x16x32_bf16 v[14:17], v[138:141], v[186:189], v[14:17]
	v_mfma_f32_16x16x32_bf16 v[62:65], v[134:137], v[166:169], v[62:65]
	v_mfma_f32_16x16x32_bf16 v[58:61], v[142:145], v[166:169], v[58:61]
	v_mfma_f32_16x16x32_bf16 v[54:57], v[134:137], v[174:177], v[54:57]
	v_mfma_f32_16x16x32_bf16 v[46:49], v[142:145], v[174:177], v[46:49]
	v_mfma_f32_16x16x32_bf16 v[38:41], v[134:137], v[182:185], v[38:41]
	v_mfma_f32_16x16x32_bf16 v[30:33], v[142:145], v[182:185], v[30:33]
	v_mfma_f32_16x16x32_bf16 v[22:25], v[134:137], v[190:193], v[22:25]
	v_mfma_f32_16x16x32_bf16 v[14:17], v[142:145], v[190:193], v[14:17]
	s_setprio 0
	s_setprio 1
	v_mfma_f32_16x16x32_bf16 v[50:53], v[146:149], v[162:165], v[50:53]
	v_mfma_f32_16x16x32_bf16 v[42:45], v[154:157], v[162:165], v[42:45]
	v_mfma_f32_16x16x32_bf16 v[34:37], v[146:149], v[170:173], v[34:37]
	v_mfma_f32_16x16x32_bf16 v[26:29], v[154:157], v[170:173], v[26:29]
	v_mfma_f32_16x16x32_bf16 v[18:21], v[146:149], v[178:181], v[18:21]
	v_mfma_f32_16x16x32_bf16 v[10:13], v[154:157], v[178:181], v[10:13]
	v_mfma_f32_16x16x32_bf16 v[6:9], v[146:149], v[186:189], v[6:9]
	v_mfma_f32_16x16x32_bf16 v[2:5], v[154:157], v[186:189], v[2:5]
	v_mfma_f32_16x16x32_bf16 v[50:53], v[150:153], v[166:169], v[50:53]
	v_mfma_f32_16x16x32_bf16 v[42:45], v[158:161], v[166:169], v[42:45]
	v_mfma_f32_16x16x32_bf16 v[34:37], v[150:153], v[174:177], v[34:37]
	v_mfma_f32_16x16x32_bf16 v[26:29], v[158:161], v[174:177], v[26:29]
	v_mfma_f32_16x16x32_bf16 v[18:21], v[150:153], v[182:185], v[18:21]
	v_mfma_f32_16x16x32_bf16 v[10:13], v[158:161], v[182:185], v[10:13]
	v_mfma_f32_16x16x32_bf16 v[6:9], v[150:153], v[190:193], v[6:9]
	v_mfma_f32_16x16x32_bf16 v[2:5], v[158:161], v[190:193], v[2:5]
	s_setprio 0
	s_add_i32 s75, s75, 2
	s_add_u32 s10, s10, 0x100
	s_addc_u32 s11, s11, 0
	s_add_u32 s70, s70, 0x100
	s_addc_u32 s71, s71, 0
	s_cmp_gt_u32 s75, 13
	s_barrier
	s_cbranch_scc0 .LBB0_883
	s_and_b64 vcc, exec, s[16:17]
	s_cbranch_vccz .LBB0_886
	s_barrier

.LBB0_1174:
	ds_read_b128 v[146:149], v140
	ds_read_b128 v[150:153], v140 offset:1024
	ds_read_b128 v[154:157], v140 offset:2048
	ds_read_b128 v[158:161], v140 offset:3072
	ds_read_b128 v[162:165], v141
	ds_read_b128 v[166:169], v141 offset:1024
	ds_read_b128 v[170:173], v141 offset:2048
	ds_read_b128 v[174:177], v141 offset:3072
	s_add_u32 s30, s34, 0xfffe0080
	s_addc_u32 s31, s35, -1
	s_cmp_eq_u32 s5, 4
	s_cselect_b32 s37, s17, s31
	s_cselect_b32 s36, vcc_lo, s30
	s_cselect_b32 s31, s21, s54
	s_cselect_b32 s30, vcc_hi, s74
	s_mov_b32 m0, s27
	v_lshl_add_u64 v[210:211], s[34:35], 0, v[136:137]
	ds_read_b128 v[178:181], v145
	ds_read_b128 v[182:185], v145 offset:1024
	ds_read_b128 v[186:189], v145 offset:2048
	ds_read_b128 v[190:193], v145 offset:3072
	ds_read_b128 v[194:197], v145 offset:4096
	ds_read_b128 v[198:201], v145 offset:5120
	ds_read_b128 v[202:205], v145 offset:6144
	ds_read_b128 v[206:209], v145 offset:7168
	global_load_lds_dwordx4 v[210:211], off
	v_lshl_add_u64 v[210:211], s[34:35], 0, v[138:139]
	s_mov_b32 m0, s90
	s_nop 0
	global_load_lds_dwordx4 v[210:211], off
	s_waitcnt vmcnt(8)
	s_waitcnt lgkmcnt(0)
	s_barrier
	s_setprio 1
	s_waitcnt lgkmcnt(0)
	v_mfma_i32_16x16x64_i8 v[122:125], v[146:149], v[178:181], v[122:125]
	v_mfma_i32_16x16x64_i8 v[118:121], v[154:157], v[178:181], v[118:121]
	v_mfma_i32_16x16x64_i8 v[106:109], v[146:149], v[186:189], v[106:109]
	v_mfma_i32_16x16x64_i8 v[102:105], v[154:157], v[186:189], v[102:105]
	v_mfma_i32_16x16x64_i8 v[90:93], v[146:149], v[194:197], v[90:93]
	v_mfma_i32_16x16x64_i8 v[86:89], v[154:157], v[194:197], v[86:89]
	v_mfma_i32_16x16x64_i8 v[74:77], v[146:149], v[202:205], v[74:77]
	v_mfma_i32_16x16x64_i8 v[70:73], v[154:157], v[202:205], v[70:73]
	v_mfma_i32_16x16x64_i8 v[122:125], v[150:153], v[182:185], v[122:125]
	v_mfma_i32_16x16x64_i8 v[118:121], v[158:161], v[182:185], v[118:121]
	v_mfma_i32_16x16x64_i8 v[106:109], v[150:153], v[190:193], v[106:109]
	v_mfma_i32_16x16x64_i8 v[102:105], v[158:161], v[190:193], v[102:105]
	v_mfma_i32_16x16x64_i8 v[90:93], v[150:153], v[198:201], v[90:93]
	v_mfma_i32_16x16x64_i8 v[86:89], v[158:161], v[198:201], v[86:89]
	v_mfma_i32_16x16x64_i8 v[74:77], v[150:153], v[206:209], v[74:77]
	v_mfma_i32_16x16x64_i8 v[70:73], v[158:161], v[206:209], v[70:73]
	s_setprio 0
	s_setprio 1
	v_mfma_i32_16x16x64_i8 v[126:129], v[162:165], v[178:181], v[126:129]
	v_mfma_i32_16x16x64_i8 v[114:117], v[170:173], v[178:181], v[114:117]
	v_mfma_i32_16x16x64_i8 v[110:113], v[162:165], v[186:189], v[110:113]
	v_mfma_i32_16x16x64_i8 v[98:101], v[170:173], v[186:189], v[98:101]
	v_mfma_i32_16x16x64_i8 v[94:97], v[162:165], v[194:197], v[94:97]
	v_mfma_i32_16x16x64_i8 v[82:85], v[170:173], v[194:197], v[82:85]
	v_mfma_i32_16x16x64_i8 v[78:81], v[162:165], v[202:205], v[78:81]
	v_mfma_i32_16x16x64_i8 v[66:69], v[170:173], v[202:205], v[66:69]
	v_mfma_i32_16x16x64_i8 v[126:129], v[166:169], v[182:185], v[126:129]
	v_mfma_i32_16x16x64_i8 v[114:117], v[174:177], v[182:185], v[114:117]
	v_mfma_i32_16x16x64_i8 v[110:113], v[166:169], v[190:193], v[110:113]
	v_mfma_i32_16x16x64_i8 v[98:101], v[174:177], v[190:193], v[98:101]
	v_mfma_i32_16x16x64_i8 v[94:97], v[166:169], v[198:201], v[94:97]
	v_mfma_i32_16x16x64_i8 v[82:85], v[174:177], v[198:201], v[82:85]
	v_mfma_i32_16x16x64_i8 v[78:81], v[166:169], v[206:209], v[78:81]
	v_mfma_i32_16x16x64_i8 v[66:69], v[174:177], v[206:209], v[66:69]
	s_setprio 0
	s_barrier
	s_mov_b32 m0, s50
	v_lshl_add_u64 v[210:211], s[30:31], 0, v[0:1]
	s_add_u32 s76, s30, 0x20000
	ds_read_b128 v[178:181], v145 offset:16384
	ds_read_b128 v[182:185], v145 offset:17408
	ds_read_b128 v[186:189], v145 offset:18432
	ds_read_b128 v[190:193], v145 offset:19456
	ds_read_b128 v[194:197], v145 offset:20480
	ds_read_b128 v[198:201], v145 offset:21504
	ds_read_b128 v[202:205], v145 offset:22528
	ds_read_b128 v[206:209], v145 offset:23552
	global_load_lds_dwordx4 v[210:211], off
	v_lshl_add_u64 v[212:213], s[30:31], 0, v[134:135]
	s_mov_b32 m0, s51
	s_addc_u32 s77, s31, 0
	global_load_lds_dwordx4 v[212:213], off
	v_lshl_add_u64 v[214:215], s[76:77], 0, v[0:1]
	s_mov_b32 m0, s94
	v_lshl_add_u64 v[216:217], s[36:37], 0, v[132:133]
	global_load_lds_dwordx4 v[214:215], off
	v_lshl_add_u64 v[214:215], s[76:77], 0, v[134:135]
	s_mov_b32 m0, s95
	s_nop 0
	global_load_lds_dwordx4 v[214:215], off
	v_lshl_add_u64 v[214:215], s[36:37], 0, v[130:131]
	s_mov_b32 m0, s4
	s_nop 0
	global_load_lds_dwordx4 v[214:215], off
	s_mov_b32 m0, s29
	s_nop 0
	global_load_lds_dwordx4 v[216:217], off
	s_waitcnt vmcnt(8)
	s_waitcnt lgkmcnt(0)
	s_barrier
	s_setprio 1
	s_waitcnt lgkmcnt(0)
	v_mfma_i32_16x16x64_i8 v[58:61], v[146:149], v[178:181], v[58:61]
	v_mfma_i32_16x16x64_i8 v[54:57], v[154:157], v[178:181], v[54:57]
	v_mfma_i32_16x16x64_i8 v[42:45], v[146:149], v[186:189], v[42:45]
	v_mfma_i32_16x16x64_i8 v[38:41], v[154:157], v[186:189], v[38:41]
	v_mfma_i32_16x16x64_i8 v[26:29], v[146:149], v[194:197], v[26:29]
	v_mfma_i32_16x16x64_i8 v[22:25], v[154:157], v[194:197], v[22:25]
	v_mfma_i32_16x16x64_i8 v[10:13], v[146:149], v[202:205], v[10:13]
	v_mfma_i32_16x16x64_i8 v[6:9], v[154:157], v[202:205], v[6:9]
	v_mfma_i32_16x16x64_i8 v[58:61], v[150:153], v[182:185], v[58:61]
	v_mfma_i32_16x16x64_i8 v[54:57], v[158:161], v[182:185], v[54:57]
	v_mfma_i32_16x16x64_i8 v[42:45], v[150:153], v[190:193], v[42:45]
	v_mfma_i32_16x16x64_i8 v[38:41], v[158:161], v[190:193], v[38:41]
	v_mfma_i32_16x16x64_i8 v[26:29], v[150:153], v[198:201], v[26:29]
	v_mfma_i32_16x16x64_i8 v[22:25], v[158:161], v[198:201], v[22:25]
	v_mfma_i32_16x16x64_i8 v[10:13], v[150:153], v[206:209], v[10:13]
	v_mfma_i32_16x16x64_i8 v[6:9], v[158:161], v[206:209], v[6:9]
	s_setprio 0
	s_setprio 1
	v_mfma_i32_16x16x64_i8 v[62:65], v[162:165], v[178:181], v[62:65]
	v_mfma_i32_16x16x64_i8 v[50:53], v[170:173], v[178:181], v[50:53]
	v_mfma_i32_16x16x64_i8 v[46:49], v[162:165], v[186:189], v[46:49]
	v_mfma_i32_16x16x64_i8 v[34:37], v[170:173], v[186:189], v[34:37]
	v_mfma_i32_16x16x64_i8 v[30:33], v[162:165], v[194:197], v[30:33]
	v_mfma_i32_16x16x64_i8 v[18:21], v[170:173], v[194:197], v[18:21]
	v_mfma_i32_16x16x64_i8 v[14:17], v[162:165], v[202:205], v[14:17]
	v_mfma_i32_16x16x64_i8 v[2:5], v[170:173], v[202:205], v[2:5]
	v_mfma_i32_16x16x64_i8 v[62:65], v[166:169], v[182:185], v[62:65]
	v_mfma_i32_16x16x64_i8 v[50:53], v[174:177], v[182:185], v[50:53]
	v_mfma_i32_16x16x64_i8 v[46:49], v[166:169], v[190:193], v[46:49]
	v_mfma_i32_16x16x64_i8 v[34:37], v[174:177], v[190:193], v[34:37]
	v_mfma_i32_16x16x64_i8 v[30:33], v[166:169], v[198:201], v[30:33]
	v_mfma_i32_16x16x64_i8 v[18:21], v[174:177], v[198:201], v[18:21]
	v_mfma_i32_16x16x64_i8 v[14:17], v[166:169], v[206:209], v[14:17]
	v_mfma_i32_16x16x64_i8 v[2:5], v[174:177], v[206:209], v[2:5]
	s_setprio 0
	s_barrier
	ds_read_b128 v[146:149], v142
	ds_read_b128 v[150:153], v142 offset:1024
	ds_read_b128 v[154:157], v142 offset:2048
	ds_read_b128 v[158:161], v142 offset:3072
	ds_read_b128 v[162:165], v143
	ds_read_b128 v[166:169], v143 offset:1024
	ds_read_b128 v[170:173], v143 offset:2048
	ds_read_b128 v[174:177], v143 offset:3072
	s_add_u32 s36, s36, 0x20000
	s_addc_u32 s37, s37, 0
	s_mov_b32 m0, s96
	v_lshl_add_u64 v[218:219], s[36:37], 0, v[130:131]
	ds_read_b128 v[178:181], v145 offset:32768
	ds_read_b128 v[182:185], v145 offset:33792
	ds_read_b128 v[186:189], v145 offset:34816
	ds_read_b128 v[190:193], v145 offset:35840
	ds_read_b128 v[194:197], v145 offset:36864
	ds_read_b128 v[198:201], v145 offset:37888
	ds_read_b128 v[202:205], v145 offset:38912
	ds_read_b128 v[206:209], v145 offset:39936
	global_load_lds_dwordx4 v[218:219], off
	v_lshl_add_u64 v[218:219], s[36:37], 0, v[132:133]
	s_mov_b32 m0, s44
	s_nop 0
	global_load_lds_dwordx4 v[218:219], off
	s_waitcnt vmcnt(8)
	s_waitcnt lgkmcnt(0)
	s_barrier
	s_setprio 1
	s_waitcnt lgkmcnt(0)
	v_mfma_i32_16x16x64_i8 v[122:125], v[146:149], v[178:181], v[122:125]
	v_mfma_i32_16x16x64_i8 v[118:121], v[154:157], v[178:181], v[118:121]
	v_mfma_i32_16x16x64_i8 v[106:109], v[146:149], v[186:189], v[106:109]
	v_mfma_i32_16x16x64_i8 v[102:105], v[154:157], v[186:189], v[102:105]
	v_mfma_i32_16x16x64_i8 v[90:93], v[146:149], v[194:197], v[90:93]
	v_mfma_i32_16x16x64_i8 v[86:89], v[154:157], v[194:197], v[86:89]
	v_mfma_i32_16x16x64_i8 v[74:77], v[146:149], v[202:205], v[74:77]
	v_mfma_i32_16x16x64_i8 v[70:73], v[154:157], v[202:205], v[70:73]
	v_mfma_i32_16x16x64_i8 v[122:125], v[150:153], v[182:185], v[122:125]
	v_mfma_i32_16x16x64_i8 v[118:121], v[158:161], v[182:185], v[118:121]
	v_mfma_i32_16x16x64_i8 v[106:109], v[150:153], v[190:193], v[106:109]
	v_mfma_i32_16x16x64_i8 v[102:105], v[158:161], v[190:193], v[102:105]
	v_mfma_i32_16x16x64_i8 v[90:93], v[150:153], v[198:201], v[90:93]
	v_mfma_i32_16x16x64_i8 v[86:89], v[158:161], v[198:201], v[86:89]
	v_mfma_i32_16x16x64_i8 v[74:77], v[150:153], v[206:209], v[74:77]
	v_mfma_i32_16x16x64_i8 v[70:73], v[158:161], v[206:209], v[70:73]
	s_setprio 0
	s_setprio 1
	v_mfma_i32_16x16x64_i8 v[126:129], v[162:165], v[178:181], v[126:129]
	v_mfma_i32_16x16x64_i8 v[114:117], v[170:173], v[178:181], v[114:117]
	v_mfma_i32_16x16x64_i8 v[110:113], v[162:165], v[186:189], v[110:113]
	v_mfma_i32_16x16x64_i8 v[98:101], v[170:173], v[186:189], v[98:101]
	v_mfma_i32_16x16x64_i8 v[94:97], v[162:165], v[194:197], v[94:97]
	v_mfma_i32_16x16x64_i8 v[82:85], v[170:173], v[194:197], v[82:85]
	v_mfma_i32_16x16x64_i8 v[78:81], v[162:165], v[202:205], v[78:81]
	v_mfma_i32_16x16x64_i8 v[66:69], v[170:173], v[202:205], v[66:69]
	v_mfma_i32_16x16x64_i8 v[126:129], v[166:169], v[182:185], v[126:129]
	v_mfma_i32_16x16x64_i8 v[114:117], v[174:177], v[182:185], v[114:117]
	v_mfma_i32_16x16x64_i8 v[110:113], v[166:169], v[190:193], v[110:113]
	v_mfma_i32_16x16x64_i8 v[98:101], v[174:177], v[190:193], v[98:101]
	v_mfma_i32_16x16x64_i8 v[94:97], v[166:169], v[198:201], v[94:97]
	v_mfma_i32_16x16x64_i8 v[82:85], v[174:177], v[198:201], v[82:85]
	v_mfma_i32_16x16x64_i8 v[78:81], v[166:169], v[206:209], v[78:81]
	v_mfma_i32_16x16x64_i8 v[66:69], v[174:177], v[206:209], v[66:69]
	s_setprio 0
	s_barrier
	s_mov_b32 m0, s78
	v_lshl_add_u64 v[210:211], v[210:211], 0, s[56:57]
	s_add_u32 s30, s30, 0x20080
	ds_read_b128 v[178:181], v145 offset:49152
	ds_read_b128 v[182:185], v145 offset:50176
	ds_read_b128 v[186:189], v145 offset:51200
	ds_read_b128 v[190:193], v145 offset:52224
	ds_read_b128 v[194:197], v145 offset:53248
	ds_read_b128 v[198:201], v145 offset:54272
	ds_read_b128 v[202:205], v145 offset:55296
	ds_read_b128 v[206:209], v145 offset:56320
	global_load_lds_dwordx4 v[210:211], off
	v_lshl_add_u64 v[210:211], v[212:213], 0, s[56:57]
	s_mov_b32 m0, s79
	s_addc_u32 s31, s31, 0
	global_load_lds_dwordx4 v[210:211], off
	v_lshl_add_u64 v[210:211], s[30:31], 0, v[0:1]
	s_mov_b32 m0, s58
	s_nop 0
	global_load_lds_dwordx4 v[210:211], off
	v_lshl_add_u64 v[210:211], s[30:31], 0, v[134:135]
	s_mov_b32 m0, s48
	s_nop 0
	global_load_lds_dwordx4 v[210:211], off
	v_lshl_add_u64 v[210:211], v[214:215], 0, s[56:57]
	s_mov_b32 m0, s88
	s_nop 0
	global_load_lds_dwordx4 v[210:211], off
	v_lshl_add_u64 v[210:211], v[216:217], 0, s[56:57]
	s_mov_b32 m0, s89
	s_nop 0
	global_load_lds_dwordx4 v[210:211], off
	s_waitcnt vmcnt(8)
	s_waitcnt lgkmcnt(0)
	s_barrier
	s_setprio 1
	s_waitcnt lgkmcnt(0)
	v_mfma_i32_16x16x64_i8 v[58:61], v[146:149], v[178:181], v[58:61]
	v_mfma_i32_16x16x64_i8 v[54:57], v[154:157], v[178:181], v[54:57]
	v_mfma_i32_16x16x64_i8 v[42:45], v[146:149], v[186:189], v[42:45]
	v_mfma_i32_16x16x64_i8 v[38:41], v[154:157], v[186:189], v[38:41]
	v_mfma_i32_16x16x64_i8 v[26:29], v[146:149], v[194:197], v[26:29]
	v_mfma_i32_16x16x64_i8 v[22:25], v[154:157], v[194:197], v[22:25]
	v_mfma_i32_16x16x64_i8 v[10:13], v[146:149], v[202:205], v[10:13]
	v_mfma_i32_16x16x64_i8 v[6:9], v[154:157], v[202:205], v[6:9]
	v_mfma_i32_16x16x64_i8 v[58:61], v[150:153], v[182:185], v[58:61]
	v_mfma_i32_16x16x64_i8 v[54:57], v[158:161], v[182:185], v[54:57]
	v_mfma_i32_16x16x64_i8 v[42:45], v[150:153], v[190:193], v[42:45]
	v_mfma_i32_16x16x64_i8 v[38:41], v[158:161], v[190:193], v[38:41]
	v_mfma_i32_16x16x64_i8 v[26:29], v[150:153], v[198:201], v[26:29]
	v_mfma_i32_16x16x64_i8 v[22:25], v[158:161], v[198:201], v[22:25]
	v_mfma_i32_16x16x64_i8 v[10:13], v[150:153], v[206:209], v[10:13]
	v_mfma_i32_16x16x64_i8 v[6:9], v[158:161], v[206:209], v[6:9]
	s_setprio 0
	s_setprio 1
	v_mfma_i32_16x16x64_i8 v[62:65], v[162:165], v[178:181], v[62:65]
	v_mfma_i32_16x16x64_i8 v[50:53], v[170:173], v[178:181], v[50:53]
	v_mfma_i32_16x16x64_i8 v[46:49], v[162:165], v[186:189], v[46:49]
	v_mfma_i32_16x16x64_i8 v[34:37], v[170:173], v[186:189], v[34:37]
	v_mfma_i32_16x16x64_i8 v[30:33], v[162:165], v[194:197], v[30:33]
	v_mfma_i32_16x16x64_i8 v[18:21], v[170:173], v[194:197], v[18:21]
	v_mfma_i32_16x16x64_i8 v[14:17], v[162:165], v[202:205], v[14:17]
	v_mfma_i32_16x16x64_i8 v[2:5], v[170:173], v[202:205], v[2:5]
	v_mfma_i32_16x16x64_i8 v[62:65], v[166:169], v[182:185], v[62:65]
	v_mfma_i32_16x16x64_i8 v[50:53], v[174:177], v[182:185], v[50:53]
	v_mfma_i32_16x16x64_i8 v[46:49], v[166:169], v[190:193], v[46:49]
	v_mfma_i32_16x16x64_i8 v[34:37], v[174:177], v[190:193], v[34:37]
	v_mfma_i32_16x16x64_i8 v[30:33], v[166:169], v[198:201], v[30:33]
	v_mfma_i32_16x16x64_i8 v[18:21], v[174:177], v[198:201], v[18:21]
	v_mfma_i32_16x16x64_i8 v[14:17], v[166:169], v[206:209], v[14:17]
	v_mfma_i32_16x16x64_i8 v[2:5], v[174:177], v[206:209], v[2:5]
	s_setprio 0
	s_add_i32 s5, s5, 2
	s_add_u32 s34, s34, 0x100
	s_addc_u32 s35, s35, 0
	s_add_u32 s74, s74, 0x100
	s_addc_u32 s54, s54, 0
	s_cmp_gt_u32 s5, 5
	s_barrier
	s_cbranch_scc0 .LBB0_1174
	s_lshl_b32 s5, s26, 8
	s_add_i32 s5, s5, s6
	v_mbcnt_lo_u32_b32 v140, -1, 0
	v_mbcnt_hi_u32_b32 v140, -1, v140
	v_readlane_b32 s78, v255, 13
	v_and_or_b32 v142, v140, 15, s5
	v_ashrrev_i32_e32 v143, 31, v142
	v_lshl_add_u64 v[152:153], v[142:143], 2, s[12:13]
	global_load_dword v141, v[152:153], off
	global_load_dword v143, v[152:153], off offset:64
	global_load_dword v146, v[152:153], off offset:128
	global_load_dword v147, v[152:153], off offset:192
	global_load_dword v149, v[152:153], off offset:512
	global_load_dword v150, v[152:153], off offset:576
	global_load_dword v151, v[152:153], off offset:640
	s_nop 0
	global_load_dword v152, v[152:153], off offset:704
	s_and_b64 vcc, exec, s[14:15]
	v_readlane_b32 s79, v255, 14
	s_movk_i32 s74, 0x1000
	s_mov_b64 s[94:95], 0x1000
	s_cbranch_vccz .LBB0_1177
	s_barrier

.LBB0_1248:
	s_add_u32 s20, s22, 0x100
	s_addc_u32 s21, s23, 0
	s_add_i32 s4, 0, 0x10000
	s_cmp_eq_u32 s70, 24
	s_cselect_b32 s25, s19, s21
	s_cselect_b32 s24, s18, s20
	v_add_u32_e32 v0, s4, v189
	s_cselect_b64 vcc, -1, 0
	s_add_i32 s5, 0, 0x14000
	ds_read_b128 v[26:29], v0
	ds_read_b128 v[30:33], v0 offset:1024
	ds_read_b128 v[18:21], v0 offset:2048
	ds_read_b128 v[22:25], v0 offset:3072
	v_add_u32_e32 v0, s5, v189
	ds_read_b128 v[10:13], v0
	ds_read_b128 v[14:17], v0 offset:1024
	ds_read_b128 v[2:5], v0 offset:2048
	ds_read_b128 v[6:9], v0 offset:3072
	v_cndmask_b32_e32 v179, v177, v175, vcc
	v_cndmask_b32_e32 v178, v176, v174, vcc
	v_lshl_add_u64 v[194:195], s[22:23], 0, v[170:171]
	s_add_i32 m0, s40, 0xc000
	ds_read_b128 v[180:183], v191
	ds_read_b128 v[184:187], v191 offset:1024
	ds_read_b128 v[198:201], v191 offset:2048
	ds_read_b128 v[202:205], v191 offset:3072
	ds_read_b128 v[206:209], v191 offset:4096
	ds_read_b128 v[210:213], v191 offset:5120
	ds_read_b128 v[214:217], v191 offset:6144
	ds_read_b128 v[218:221], v191 offset:7168
	global_load_lds_dwordx4 v[194:195], off
	v_lshl_add_u64 v[194:195], s[22:23], 0, v[172:173]
	s_add_i32 m0, s40, 0xe000
	s_nop 0
	global_load_lds_dwordx4 v[194:195], off
	s_waitcnt vmcnt(8)
	s_waitcnt lgkmcnt(0)
	s_barrier
	s_setprio 1
	s_waitcnt lgkmcnt(0)
	s_nop 1
	v_mfma_f32_16x16x128_f8f6f4 v[158:161], v[26:33], v[180:187], v[158:161]
	s_nop 1
	v_mfma_f32_16x16x128_f8f6f4 v[154:157], v[18:25], v[180:187], v[154:157]
	s_nop 1
	v_mfma_f32_16x16x128_f8f6f4 v[142:145], v[26:33], v[198:205], v[142:145]
	s_nop 1
	v_mfma_f32_16x16x128_f8f6f4 v[138:141], v[18:25], v[198:205], v[138:141]
	s_nop 1
	v_mfma_f32_16x16x128_f8f6f4 v[126:129], v[26:33], v[206:213], v[126:129]
	s_nop 1
	v_mfma_f32_16x16x128_f8f6f4 v[122:125], v[18:25], v[206:213], v[122:125]
	s_nop 1
	v_mfma_f32_16x16x128_f8f6f4 v[110:113], v[26:33], v[214:221], v[110:113]
	s_nop 1
	v_mfma_f32_16x16x128_f8f6f4 v[106:109], v[18:25], v[214:221], v[106:109]
	s_setprio 0
	s_setprio 1
	s_nop 1
	v_mfma_f32_16x16x128_f8f6f4 v[150:153], v[10:17], v[180:187], v[150:153]
	s_nop 1
	v_mfma_f32_16x16x128_f8f6f4 v[146:149], v[2:9], v[180:187], v[146:149]
	s_nop 1
	v_mfma_f32_16x16x128_f8f6f4 v[134:137], v[10:17], v[198:205], v[134:137]
	s_nop 1
	v_mfma_f32_16x16x128_f8f6f4 v[130:133], v[2:9], v[198:205], v[130:133]
	s_nop 1
	v_mfma_f32_16x16x128_f8f6f4 v[118:121], v[10:17], v[206:213], v[118:121]
	s_nop 1
	v_mfma_f32_16x16x128_f8f6f4 v[114:117], v[2:9], v[206:213], v[114:117]
	s_nop 1
	v_mfma_f32_16x16x128_f8f6f4 v[102:105], v[10:17], v[214:221], v[102:105]
	s_nop 1
	v_mfma_f32_16x16x128_f8f6f4 v[98:101], v[2:9], v[214:221], v[98:101]
	s_setprio 0
	s_barrier
	s_add_i32 s4, s4, s39
	v_lshl_add_u64 v[180:181], v[178:179], 0, v[164:165]
	s_mov_b32 m0, s4
	ds_read_b128 v[198:201], v191 offset:16384
	ds_read_b128 v[202:205], v191 offset:17408
	ds_read_b128 v[206:209], v191 offset:18432
	ds_read_b128 v[210:213], v191 offset:19456
	ds_read_b128 v[214:217], v191 offset:20480
	ds_read_b128 v[218:221], v191 offset:21504
	ds_read_b128 v[222:225], v191 offset:22528
	ds_read_b128 v[226:229], v191 offset:23552
	global_load_lds_dwordx4 v[180:181], off
	v_lshl_add_u64 v[182:183], v[178:179], 0, v[168:169]
	s_add_i32 m0, s4, 0x2000
	v_lshl_add_u64 v[184:185], v[178:179], 0, s[54:55]
	s_add_i32 s4, s5, s39
	global_load_lds_dwordx4 v[182:183], off
	v_lshl_add_u64 v[186:187], v[184:185], 0, v[164:165]
	s_mov_b32 m0, s4
	v_lshl_add_u64 v[184:185], v[184:185], 0, v[168:169]
	global_load_lds_dwordx4 v[186:187], off
	s_add_i32 m0, s4, 0x2000
	v_lshl_add_u64 v[186:187], s[24:25], 0, v[166:167]
	global_load_lds_dwordx4 v[184:185], off
	v_lshl_add_u64 v[184:185], s[24:25], 0, v[162:163]
	s_mov_b32 m0, s40
	s_nop 0
	global_load_lds_dwordx4 v[184:185], off
	s_mov_b32 m0, s41
	s_nop 0
	global_load_lds_dwordx4 v[186:187], off
	s_waitcnt vmcnt(8)
	s_waitcnt lgkmcnt(0)
	s_barrier
	s_setprio 1
	s_waitcnt lgkmcnt(0)
	s_nop 1
	v_mfma_f32_16x16x128_f8f6f4 v[94:97], v[26:33], v[198:205], v[94:97]
	s_nop 1
	v_mfma_f32_16x16x128_f8f6f4 v[90:93], v[18:25], v[198:205], v[90:93]
	s_nop 1
	v_mfma_f32_16x16x128_f8f6f4 v[78:81], v[26:33], v[206:213], v[78:81]
	s_nop 1
	v_mfma_f32_16x16x128_f8f6f4 v[74:77], v[18:25], v[206:213], v[74:77]
	s_nop 1
	v_mfma_f32_16x16x128_f8f6f4 v[62:65], v[26:33], v[214:221], v[62:65]
	s_nop 1
	v_mfma_f32_16x16x128_f8f6f4 v[58:61], v[18:25], v[214:221], v[58:61]
	s_nop 1
	v_mfma_f32_16x16x128_f8f6f4 v[46:49], v[26:33], v[222:229], v[46:49]
	s_nop 1
	v_mfma_f32_16x16x128_f8f6f4 v[42:45], v[18:25], v[222:229], v[42:45]
	s_setprio 0
	s_setprio 1
	s_nop 1
	v_mfma_f32_16x16x128_f8f6f4 v[86:89], v[10:17], v[198:205], v[86:89]
	s_nop 1
	v_mfma_f32_16x16x128_f8f6f4 v[82:85], v[2:9], v[198:205], v[82:85]
	s_nop 1
	v_mfma_f32_16x16x128_f8f6f4 v[70:73], v[10:17], v[206:213], v[70:73]
	s_nop 1
	v_mfma_f32_16x16x128_f8f6f4 v[66:69], v[2:9], v[206:213], v[66:69]
	s_nop 1
	v_mfma_f32_16x16x128_f8f6f4 v[54:57], v[10:17], v[214:221], v[54:57]
	s_nop 1
	v_mfma_f32_16x16x128_f8f6f4 v[50:53], v[2:9], v[214:221], v[50:53]
	s_nop 1
	v_mfma_f32_16x16x128_f8f6f4 v[38:41], v[10:17], v[222:229], v[38:41]
	s_nop 1
	v_mfma_f32_16x16x128_f8f6f4 v[34:37], v[2:9], v[222:229], v[34:37]
	s_setprio 0
	s_barrier
	s_add_i32 s22, 0, 0x18000
	v_add_u32_e32 v0, s22, v189
	s_add_i32 s23, 0, 0x1c000
	ds_read_b128 v[2:5], v0
	ds_read_b128 v[6:9], v0 offset:1024
	ds_read_b128 v[10:13], v0 offset:2048
	ds_read_b128 v[14:17], v0 offset:3072
	v_add_u32_e32 v0, s23, v189
	ds_read_b128 v[18:21], v0
	ds_read_b128 v[22:25], v0 offset:1024
	ds_read_b128 v[26:29], v0 offset:2048
	ds_read_b128 v[30:33], v0 offset:3072
	s_add_u32 s4, s24, 0x70000
	s_addc_u32 s5, s25, 0
	s_mov_b32 m0, s45
	v_lshl_add_u64 v[194:195], s[4:5], 0, v[162:163]
	ds_read_b128 v[198:201], v191 offset:32768
	ds_read_b128 v[202:205], v191 offset:33792
	ds_read_b128 v[206:209], v191 offset:34816
	ds_read_b128 v[210:213], v191 offset:35840
	ds_read_b128 v[214:217], v191 offset:36864
	ds_read_b128 v[218:221], v191 offset:37888
	ds_read_b128 v[222:225], v191 offset:38912
	ds_read_b128 v[226:229], v191 offset:39936
	global_load_lds_dwordx4 v[194:195], off
	v_lshl_add_u64 v[194:195], s[4:5], 0, v[166:167]
	s_mov_b32 m0, s49
	s_nop 0
	global_load_lds_dwordx4 v[194:195], off
	s_waitcnt vmcnt(8)
	s_waitcnt lgkmcnt(0)
	s_barrier
	s_setprio 1
	s_waitcnt lgkmcnt(0)
	s_nop 1
	v_mfma_f32_16x16x128_f8f6f4 v[158:161], v[2:9], v[198:205], v[158:161]
	s_nop 1
	v_mfma_f32_16x16x128_f8f6f4 v[154:157], v[10:17], v[198:205], v[154:157]
	s_nop 1
	v_mfma_f32_16x16x128_f8f6f4 v[142:145], v[2:9], v[206:213], v[142:145]
	s_nop 1
	v_mfma_f32_16x16x128_f8f6f4 v[138:141], v[10:17], v[206:213], v[138:141]
	s_nop 1
	v_mfma_f32_16x16x128_f8f6f4 v[126:129], v[2:9], v[214:221], v[126:129]
	s_nop 1
	v_mfma_f32_16x16x128_f8f6f4 v[122:125], v[10:17], v[214:221], v[122:125]
	s_nop 1
	v_mfma_f32_16x16x128_f8f6f4 v[110:113], v[2:9], v[222:229], v[110:113]
	s_nop 1
	v_mfma_f32_16x16x128_f8f6f4 v[106:109], v[10:17], v[222:229], v[106:109]
	s_setprio 0
	s_setprio 1
	s_nop 1
	v_mfma_f32_16x16x128_f8f6f4 v[150:153], v[18:25], v[198:205], v[150:153]
	s_nop 1
	v_mfma_f32_16x16x128_f8f6f4 v[146:149], v[26:33], v[198:205], v[146:149]
	s_nop 1
	v_mfma_f32_16x16x128_f8f6f4 v[134:137], v[18:25], v[206:213], v[134:137]
	s_nop 1
	v_mfma_f32_16x16x128_f8f6f4 v[130:133], v[26:33], v[206:213], v[130:133]
	s_nop 1
	v_mfma_f32_16x16x128_f8f6f4 v[118:121], v[18:25], v[214:221], v[118:121]
	s_nop 1
	v_mfma_f32_16x16x128_f8f6f4 v[114:117], v[26:33], v[214:221], v[114:117]
	s_nop 1
	v_mfma_f32_16x16x128_f8f6f4 v[102:105], v[18:25], v[222:229], v[102:105]
	s_nop 1
	v_mfma_f32_16x16x128_f8f6f4 v[98:101], v[26:33], v[222:229], v[98:101]
	s_setprio 0
	s_barrier
	s_add_i32 s4, s22, s39
	v_lshl_add_u64 v[180:181], v[180:181], 0, s[56:57]
	s_mov_b32 m0, s4
	ds_read_b128 v[198:201], v191 offset:49152
	ds_read_b128 v[202:205], v191 offset:50176
	ds_read_b128 v[206:209], v191 offset:51200
	ds_read_b128 v[210:213], v191 offset:52224
	ds_read_b128 v[214:217], v191 offset:53248
	ds_read_b128 v[218:221], v191 offset:54272
	ds_read_b128 v[222:225], v191 offset:55296
	ds_read_b128 v[226:229], v191 offset:56320
	global_load_lds_dwordx4 v[180:181], off
	v_lshl_add_u64 v[180:181], v[182:183], 0, s[56:57]
	s_add_i32 m0, s4, 0x2000
	v_lshl_add_u64 v[178:179], v[178:179], 0, s[68:69]
	s_add_i32 s4, s23, s39
	global_load_lds_dwordx4 v[180:181], off
	v_lshl_add_u64 v[180:181], v[178:179], 0, v[164:165]
	s_mov_b32 m0, s4
	v_lshl_add_u64 v[178:179], v[178:179], 0, v[168:169]
	global_load_lds_dwordx4 v[180:181], off
	s_add_i32 m0, s4, 0x2000
	s_nop 0
	global_load_lds_dwordx4 v[178:179], off
	v_lshl_add_u64 v[178:179], v[184:185], 0, s[56:57]
	s_mov_b32 m0, s52
	s_nop 0
	global_load_lds_dwordx4 v[178:179], off
	v_lshl_add_u64 v[178:179], v[186:187], 0, s[56:57]
	s_mov_b32 m0, s59
	s_nop 0
	global_load_lds_dwordx4 v[178:179], off
	s_waitcnt vmcnt(8)
	s_waitcnt lgkmcnt(0)
	s_barrier
	s_setprio 1
	s_waitcnt lgkmcnt(0)
	s_nop 1
	v_mfma_f32_16x16x128_f8f6f4 v[94:97], v[2:9], v[198:205], v[94:97]
	s_nop 1
	v_mfma_f32_16x16x128_f8f6f4 v[90:93], v[10:17], v[198:205], v[90:93]
	s_nop 1
	v_mfma_f32_16x16x128_f8f6f4 v[78:81], v[2:9], v[206:213], v[78:81]
	s_nop 1
	v_mfma_f32_16x16x128_f8f6f4 v[74:77], v[10:17], v[206:213], v[74:77]
	s_nop 1
	v_mfma_f32_16x16x128_f8f6f4 v[62:65], v[2:9], v[214:221], v[62:65]
	s_nop 1
	v_mfma_f32_16x16x128_f8f6f4 v[58:61], v[10:17], v[214:221], v[58:61]
	s_nop 1
	v_mfma_f32_16x16x128_f8f6f4 v[46:49], v[2:9], v[222:229], v[46:49]
	s_nop 1
	v_mfma_f32_16x16x128_f8f6f4 v[42:45], v[10:17], v[222:229], v[42:45]
	s_setprio 0
	s_setprio 1
	s_nop 1
	v_mfma_f32_16x16x128_f8f6f4 v[86:89], v[18:25], v[198:205], v[86:89]
	s_nop 1
	v_mfma_f32_16x16x128_f8f6f4 v[82:85], v[26:33], v[198:205], v[82:85]
	s_nop 1
	v_mfma_f32_16x16x128_f8f6f4 v[70:73], v[18:25], v[206:213], v[70:73]
	s_nop 1
	v_mfma_f32_16x16x128_f8f6f4 v[66:69], v[26:33], v[206:213], v[66:69]
	s_nop 1
	v_mfma_f32_16x16x128_f8f6f4 v[54:57], v[18:25], v[214:221], v[54:57]
	s_nop 1
	v_mfma_f32_16x16x128_f8f6f4 v[50:53], v[26:33], v[214:221], v[50:53]
	s_nop 1
	v_mfma_f32_16x16x128_f8f6f4 v[38:41], v[18:25], v[222:229], v[38:41]
	s_nop 1
	v_mfma_f32_16x16x128_f8f6f4 v[34:37], v[26:33], v[222:229], v[34:37]
	s_setprio 0
	s_add_i32 s70, s70, 2
	v_lshl_add_u64 v[176:177], v[176:177], 0, s[92:93]
	s_cmp_gt_u32 s70, 25
	s_mov_b64 s[22:23], s[20:21]
	s_barrier
	s_cbranch_scc0 .LBB0_1248
	s_nop 15
	s_nop 15
	s_and_b64 vcc, exec, s[16:17]
	s_cbranch_vccz .LBB0_1251
	s_barrier

.LBB0_1294:
	s_add_u32 s22, s20, 0x100
	s_addc_u32 s23, s21, 0
	s_add_i32 s4, 0, 0x10000
	s_cmp_eq_u32 s63, 52
	s_cselect_b32 s25, s19, s23
	s_cselect_b32 s24, s18, s22
	v_add_u32_e32 v0, s4, v163
	s_cselect_b64 vcc, -1, 0
	s_add_i32 s5, 0, 0x14000
	ds_read_b128 v[148:151], v0
	ds_read_b128 v[152:155], v0 offset:1024
	ds_read_b128 v[156:159], v0 offset:2048
	ds_read_b128 v[168:171], v0 offset:3072
	v_add_u32_e32 v0, s5, v163
	ds_read_b128 v[172:175], v0
	ds_read_b128 v[176:179], v0 offset:1024
	ds_read_b128 v[180:183], v0 offset:2048
	ds_read_b128 v[184:187], v0 offset:3072
	v_cndmask_b32_e32 v161, v145, v143, vcc
	v_cndmask_b32_e32 v160, v144, v142, vcc
	v_lshl_add_u64 v[220:221], s[20:21], 0, v[138:139]
	s_add_i32 m0, s39, 0xc000
	ds_read_b128 v[188:191], v165
	ds_read_b128 v[192:195], v165 offset:1024
	ds_read_b128 v[196:199], v165 offset:2048
	ds_read_b128 v[200:203], v165 offset:3072
	ds_read_b128 v[204:207], v165 offset:4096
	ds_read_b128 v[208:211], v165 offset:5120
	ds_read_b128 v[212:215], v165 offset:6144
	ds_read_b128 v[216:219], v165 offset:7168
	global_load_lds_dwordx4 v[220:221], off
	v_lshl_add_u64 v[220:221], s[20:21], 0, v[140:141]
	s_add_i32 m0, s39, 0xe000
	s_nop 0
	global_load_lds_dwordx4 v[220:221], off
	s_waitcnt vmcnt(8)
	s_waitcnt lgkmcnt(0)
	s_barrier
	s_setprio 1
	s_waitcnt lgkmcnt(0)
	v_mfma_f32_16x16x32_bf16 v[126:129], v[148:151], v[188:191], v[126:129]
	v_mfma_f32_16x16x32_bf16 v[122:125], v[156:159], v[188:191], v[122:125]
	v_mfma_f32_16x16x32_bf16 v[110:113], v[148:151], v[196:199], v[110:113]
	v_mfma_f32_16x16x32_bf16 v[106:109], v[156:159], v[196:199], v[106:109]
	v_mfma_f32_16x16x32_bf16 v[94:97], v[148:151], v[204:207], v[94:97]
	v_mfma_f32_16x16x32_bf16 v[90:93], v[156:159], v[204:207], v[90:93]
	v_mfma_f32_16x16x32_bf16 v[78:81], v[148:151], v[212:215], v[78:81]
	v_mfma_f32_16x16x32_bf16 v[74:77], v[156:159], v[212:215], v[74:77]
	v_mfma_f32_16x16x32_bf16 v[126:129], v[152:155], v[192:195], v[126:129]
	v_mfma_f32_16x16x32_bf16 v[122:125], v[168:171], v[192:195], v[122:125]
	v_mfma_f32_16x16x32_bf16 v[110:113], v[152:155], v[200:203], v[110:113]
	v_mfma_f32_16x16x32_bf16 v[106:109], v[168:171], v[200:203], v[106:109]
	v_mfma_f32_16x16x32_bf16 v[94:97], v[152:155], v[208:211], v[94:97]
	v_mfma_f32_16x16x32_bf16 v[90:93], v[168:171], v[208:211], v[90:93]
	v_mfma_f32_16x16x32_bf16 v[78:81], v[152:155], v[216:219], v[78:81]
	v_mfma_f32_16x16x32_bf16 v[74:77], v[168:171], v[216:219], v[74:77]
	s_setprio 0
	s_setprio 1
	v_mfma_f32_16x16x32_bf16 v[118:121], v[172:175], v[188:191], v[118:121]
	v_mfma_f32_16x16x32_bf16 v[114:117], v[180:183], v[188:191], v[114:117]
	v_mfma_f32_16x16x32_bf16 v[102:105], v[172:175], v[196:199], v[102:105]
	v_mfma_f32_16x16x32_bf16 v[98:101], v[180:183], v[196:199], v[98:101]
	v_mfma_f32_16x16x32_bf16 v[86:89], v[172:175], v[204:207], v[86:89]
	v_mfma_f32_16x16x32_bf16 v[82:85], v[180:183], v[204:207], v[82:85]
	v_mfma_f32_16x16x32_bf16 v[70:73], v[172:175], v[212:215], v[70:73]
	v_mfma_f32_16x16x32_bf16 v[66:69], v[180:183], v[212:215], v[66:69]
	v_mfma_f32_16x16x32_bf16 v[118:121], v[176:179], v[192:195], v[118:121]
	v_mfma_f32_16x16x32_bf16 v[114:117], v[184:187], v[192:195], v[114:117]
	v_mfma_f32_16x16x32_bf16 v[102:105], v[176:179], v[200:203], v[102:105]
	v_mfma_f32_16x16x32_bf16 v[98:101], v[184:187], v[200:203], v[98:101]
	v_mfma_f32_16x16x32_bf16 v[86:89], v[176:179], v[208:211], v[86:89]
	v_mfma_f32_16x16x32_bf16 v[82:85], v[184:187], v[208:211], v[82:85]
	v_mfma_f32_16x16x32_bf16 v[70:73], v[176:179], v[216:219], v[70:73]
	v_mfma_f32_16x16x32_bf16 v[66:69], v[184:187], v[216:219], v[66:69]
	s_setprio 0
	s_barrier
	s_add_i32 s4, s4, s38
	v_lshl_add_u64 v[220:221], v[160:161], 0, v[132:133]
	s_mov_b32 m0, s4
	ds_read_b128 v[188:191], v165 offset:16384
	ds_read_b128 v[192:195], v165 offset:17408
	ds_read_b128 v[196:199], v165 offset:18432
	ds_read_b128 v[200:203], v165 offset:19456
	ds_read_b128 v[204:207], v165 offset:20480
	ds_read_b128 v[208:211], v165 offset:21504
	ds_read_b128 v[212:215], v165 offset:22528
	ds_read_b128 v[216:219], v165 offset:23552
	global_load_lds_dwordx4 v[220:221], off
	v_lshl_add_u64 v[222:223], v[160:161], 0, v[136:137]
	s_add_i32 m0, s4, 0x2000
	v_lshl_add_u64 v[224:225], v[160:161], 0, s[54:55]
	s_add_i32 s4, s5, s38
	global_load_lds_dwordx4 v[222:223], off
	v_lshl_add_u64 v[226:227], v[224:225], 0, v[132:133]
	s_mov_b32 m0, s4
	v_lshl_add_u64 v[224:225], v[224:225], 0, v[136:137]
	global_load_lds_dwordx4 v[226:227], off
	s_add_i32 m0, s4, 0x2000
	v_lshl_add_u64 v[226:227], s[24:25], 0, v[134:135]
	global_load_lds_dwordx4 v[224:225], off
	v_lshl_add_u64 v[224:225], s[24:25], 0, v[130:131]
	s_mov_b32 m0, s39
	s_nop 0
	global_load_lds_dwordx4 v[224:225], off
	s_mov_b32 m0, s40
	s_nop 0
	global_load_lds_dwordx4 v[226:227], off
	s_waitcnt vmcnt(8)
	s_waitcnt lgkmcnt(0)
	s_barrier
	s_setprio 1
	s_waitcnt lgkmcnt(0)
	v_mfma_f32_16x16x32_bf16 v[62:65], v[148:151], v[188:191], v[62:65]
	v_mfma_f32_16x16x32_bf16 v[58:61], v[156:159], v[188:191], v[58:61]
	v_mfma_f32_16x16x32_bf16 v[46:49], v[148:151], v[196:199], v[46:49]
	v_mfma_f32_16x16x32_bf16 v[42:45], v[156:159], v[196:199], v[42:45]
	v_mfma_f32_16x16x32_bf16 v[30:33], v[148:151], v[204:207], v[30:33]
	v_mfma_f32_16x16x32_bf16 v[26:29], v[156:159], v[204:207], v[26:29]
	v_mfma_f32_16x16x32_bf16 v[14:17], v[148:151], v[212:215], v[14:17]
	v_mfma_f32_16x16x32_bf16 v[10:13], v[156:159], v[212:215], v[10:13]
	v_mfma_f32_16x16x32_bf16 v[62:65], v[152:155], v[192:195], v[62:65]
	v_mfma_f32_16x16x32_bf16 v[58:61], v[168:171], v[192:195], v[58:61]
	v_mfma_f32_16x16x32_bf16 v[46:49], v[152:155], v[200:203], v[46:49]
	v_mfma_f32_16x16x32_bf16 v[42:45], v[168:171], v[200:203], v[42:45]
	v_mfma_f32_16x16x32_bf16 v[30:33], v[152:155], v[208:211], v[30:33]
	v_mfma_f32_16x16x32_bf16 v[26:29], v[168:171], v[208:211], v[26:29]
	v_mfma_f32_16x16x32_bf16 v[14:17], v[152:155], v[216:219], v[14:17]
	v_mfma_f32_16x16x32_bf16 v[10:13], v[168:171], v[216:219], v[10:13]
	s_setprio 0
	s_setprio 1
	v_mfma_f32_16x16x32_bf16 v[54:57], v[172:175], v[188:191], v[54:57]
	v_mfma_f32_16x16x32_bf16 v[50:53], v[180:183], v[188:191], v[50:53]
	v_mfma_f32_16x16x32_bf16 v[38:41], v[172:175], v[196:199], v[38:41]
	v_mfma_f32_16x16x32_bf16 v[34:37], v[180:183], v[196:199], v[34:37]
	v_mfma_f32_16x16x32_bf16 v[22:25], v[172:175], v[204:207], v[22:25]
	v_mfma_f32_16x16x32_bf16 v[18:21], v[180:183], v[204:207], v[18:21]
	v_mfma_f32_16x16x32_bf16 v[6:9], v[172:175], v[212:215], v[6:9]
	v_mfma_f32_16x16x32_bf16 v[2:5], v[180:183], v[212:215], v[2:5]
	v_mfma_f32_16x16x32_bf16 v[54:57], v[176:179], v[192:195], v[54:57]
	v_mfma_f32_16x16x32_bf16 v[50:53], v[184:187], v[192:195], v[50:53]
	v_mfma_f32_16x16x32_bf16 v[38:41], v[176:179], v[200:203], v[38:41]
	v_mfma_f32_16x16x32_bf16 v[34:37], v[184:187], v[200:203], v[34:37]
	v_mfma_f32_16x16x32_bf16 v[22:25], v[176:179], v[208:211], v[22:25]
	v_mfma_f32_16x16x32_bf16 v[18:21], v[184:187], v[208:211], v[18:21]
	v_mfma_f32_16x16x32_bf16 v[6:9], v[176:179], v[216:219], v[6:9]
	v_mfma_f32_16x16x32_bf16 v[2:5], v[184:187], v[216:219], v[2:5]
	s_setprio 0
	s_barrier
	s_add_i32 s20, 0, 0x18000
	v_add_u32_e32 v0, s20, v163
	s_add_i32 s21, 0, 0x1c000
	ds_read_b128 v[148:151], v0
	ds_read_b128 v[152:155], v0 offset:1024
	ds_read_b128 v[156:159], v0 offset:2048
	ds_read_b128 v[168:171], v0 offset:3072
	v_add_u32_e32 v0, s21, v163
	ds_read_b128 v[172:175], v0
	ds_read_b128 v[176:179], v0 offset:1024
	ds_read_b128 v[180:183], v0 offset:2048
	ds_read_b128 v[184:187], v0 offset:3072
	s_add_u32 s4, s24, 0xe0000
	s_addc_u32 s5, s25, 0
	s_mov_b32 m0, s41
	v_lshl_add_u64 v[228:229], s[4:5], 0, v[130:131]
	ds_read_b128 v[188:191], v165 offset:32768
	ds_read_b128 v[192:195], v165 offset:33792
	ds_read_b128 v[196:199], v165 offset:34816
	ds_read_b128 v[200:203], v165 offset:35840
	ds_read_b128 v[204:207], v165 offset:36864
	ds_read_b128 v[208:211], v165 offset:37888
	ds_read_b128 v[212:215], v165 offset:38912
	ds_read_b128 v[216:219], v165 offset:39936
	global_load_lds_dwordx4 v[228:229], off
	v_lshl_add_u64 v[228:229], s[4:5], 0, v[134:135]
	s_mov_b32 m0, s44
	s_nop 0
	global_load_lds_dwordx4 v[228:229], off
	s_waitcnt vmcnt(8)
	s_waitcnt lgkmcnt(0)
	s_barrier
	s_setprio 1
	s_waitcnt lgkmcnt(0)
	v_mfma_f32_16x16x32_bf16 v[126:129], v[148:151], v[188:191], v[126:129]
	v_mfma_f32_16x16x32_bf16 v[122:125], v[156:159], v[188:191], v[122:125]
	v_mfma_f32_16x16x32_bf16 v[110:113], v[148:151], v[196:199], v[110:113]
	v_mfma_f32_16x16x32_bf16 v[106:109], v[156:159], v[196:199], v[106:109]
	v_mfma_f32_16x16x32_bf16 v[94:97], v[148:151], v[204:207], v[94:97]
	v_mfma_f32_16x16x32_bf16 v[90:93], v[156:159], v[204:207], v[90:93]
	v_mfma_f32_16x16x32_bf16 v[78:81], v[148:151], v[212:215], v[78:81]
	v_mfma_f32_16x16x32_bf16 v[74:77], v[156:159], v[212:215], v[74:77]
	v_mfma_f32_16x16x32_bf16 v[126:129], v[152:155], v[192:195], v[126:129]
	v_mfma_f32_16x16x32_bf16 v[122:125], v[168:171], v[192:195], v[122:125]
	v_mfma_f32_16x16x32_bf16 v[110:113], v[152:155], v[200:203], v[110:113]
	v_mfma_f32_16x16x32_bf16 v[106:109], v[168:171], v[200:203], v[106:109]
	v_mfma_f32_16x16x32_bf16 v[94:97], v[152:155], v[208:211], v[94:97]
	v_mfma_f32_16x16x32_bf16 v[90:93], v[168:171], v[208:211], v[90:93]
	v_mfma_f32_16x16x32_bf16 v[78:81], v[152:155], v[216:219], v[78:81]
	v_mfma_f32_16x16x32_bf16 v[74:77], v[168:171], v[216:219], v[74:77]
	s_setprio 0
	s_setprio 1
	v_mfma_f32_16x16x32_bf16 v[118:121], v[172:175], v[188:191], v[118:121]
	v_mfma_f32_16x16x32_bf16 v[114:117], v[180:183], v[188:191], v[114:117]
	v_mfma_f32_16x16x32_bf16 v[102:105], v[172:175], v[196:199], v[102:105]
	v_mfma_f32_16x16x32_bf16 v[98:101], v[180:183], v[196:199], v[98:101]
	v_mfma_f32_16x16x32_bf16 v[86:89], v[172:175], v[204:207], v[86:89]
	v_mfma_f32_16x16x32_bf16 v[82:85], v[180:183], v[204:207], v[82:85]
	v_mfma_f32_16x16x32_bf16 v[70:73], v[172:175], v[212:215], v[70:73]
	v_mfma_f32_16x16x32_bf16 v[66:69], v[180:183], v[212:215], v[66:69]
	v_mfma_f32_16x16x32_bf16 v[118:121], v[176:179], v[192:195], v[118:121]
	v_mfma_f32_16x16x32_bf16 v[114:117], v[184:187], v[192:195], v[114:117]
	v_mfma_f32_16x16x32_bf16 v[102:105], v[176:179], v[200:203], v[102:105]
	v_mfma_f32_16x16x32_bf16 v[98:101], v[184:187], v[200:203], v[98:101]
	v_mfma_f32_16x16x32_bf16 v[86:89], v[176:179], v[208:211], v[86:89]
	v_mfma_f32_16x16x32_bf16 v[82:85], v[184:187], v[208:211], v[82:85]
	v_mfma_f32_16x16x32_bf16 v[70:73], v[176:179], v[216:219], v[70:73]
	v_mfma_f32_16x16x32_bf16 v[66:69], v[184:187], v[216:219], v[66:69]
	s_setprio 0
	s_barrier
	s_add_i32 s4, s20, s38
	v_lshl_add_u64 v[220:221], v[220:221], 0, s[56:57]
	s_mov_b32 m0, s4
	ds_read_b128 v[188:191], v165 offset:49152
	ds_read_b128 v[192:195], v165 offset:50176
	ds_read_b128 v[196:199], v165 offset:51200
	ds_read_b128 v[200:203], v165 offset:52224
	ds_read_b128 v[204:207], v165 offset:53248
	ds_read_b128 v[208:211], v165 offset:54272
	ds_read_b128 v[212:215], v165 offset:55296
	ds_read_b128 v[216:219], v165 offset:56320
	global_load_lds_dwordx4 v[220:221], off
	v_lshl_add_u64 v[220:221], v[222:223], 0, s[56:57]
	s_add_i32 m0, s4, 0x2000
	v_lshl_add_u64 v[160:161], v[160:161], 0, s[88:89]
	s_add_i32 s4, s21, s38
	global_load_lds_dwordx4 v[220:221], off
	v_lshl_add_u64 v[220:221], v[160:161], 0, v[132:133]
	s_mov_b32 m0, s4
	v_lshl_add_u64 v[160:161], v[160:161], 0, v[136:137]
	global_load_lds_dwordx4 v[220:221], off
	s_add_i32 m0, s4, 0x2000
	s_nop 0
	global_load_lds_dwordx4 v[160:161], off
	v_lshl_add_u64 v[160:161], v[224:225], 0, s[56:57]
	s_mov_b32 m0, s45
	s_nop 0
	global_load_lds_dwordx4 v[160:161], off
	v_lshl_add_u64 v[160:161], v[226:227], 0, s[56:57]
	s_mov_b32 m0, s49
	s_nop 0
	global_load_lds_dwordx4 v[160:161], off
	s_waitcnt vmcnt(8)
	s_waitcnt lgkmcnt(0)
	s_barrier
	s_setprio 1
	s_waitcnt lgkmcnt(0)
	v_mfma_f32_16x16x32_bf16 v[62:65], v[148:151], v[188:191], v[62:65]
	v_mfma_f32_16x16x32_bf16 v[58:61], v[156:159], v[188:191], v[58:61]
	v_mfma_f32_16x16x32_bf16 v[46:49], v[148:151], v[196:199], v[46:49]
	v_mfma_f32_16x16x32_bf16 v[42:45], v[156:159], v[196:199], v[42:45]
	v_mfma_f32_16x16x32_bf16 v[30:33], v[148:151], v[204:207], v[30:33]
	v_mfma_f32_16x16x32_bf16 v[26:29], v[156:159], v[204:207], v[26:29]
	v_mfma_f32_16x16x32_bf16 v[14:17], v[148:151], v[212:215], v[14:17]
	v_mfma_f32_16x16x32_bf16 v[10:13], v[156:159], v[212:215], v[10:13]
	v_mfma_f32_16x16x32_bf16 v[62:65], v[152:155], v[192:195], v[62:65]
	v_mfma_f32_16x16x32_bf16 v[58:61], v[168:171], v[192:195], v[58:61]
	v_mfma_f32_16x16x32_bf16 v[46:49], v[152:155], v[200:203], v[46:49]
	v_mfma_f32_16x16x32_bf16 v[42:45], v[168:171], v[200:203], v[42:45]
	v_mfma_f32_16x16x32_bf16 v[30:33], v[152:155], v[208:211], v[30:33]
	v_mfma_f32_16x16x32_bf16 v[26:29], v[168:171], v[208:211], v[26:29]
	v_mfma_f32_16x16x32_bf16 v[14:17], v[152:155], v[216:219], v[14:17]
	v_mfma_f32_16x16x32_bf16 v[10:13], v[168:171], v[216:219], v[10:13]
	s_setprio 0
	s_setprio 1
	v_mfma_f32_16x16x32_bf16 v[54:57], v[172:175], v[188:191], v[54:57]
	v_mfma_f32_16x16x32_bf16 v[50:53], v[180:183], v[188:191], v[50:53]
	v_mfma_f32_16x16x32_bf16 v[38:41], v[172:175], v[196:199], v[38:41]
	v_mfma_f32_16x16x32_bf16 v[34:37], v[180:183], v[196:199], v[34:37]
	v_mfma_f32_16x16x32_bf16 v[22:25], v[172:175], v[204:207], v[22:25]
	v_mfma_f32_16x16x32_bf16 v[18:21], v[180:183], v[204:207], v[18:21]
	v_mfma_f32_16x16x32_bf16 v[6:9], v[172:175], v[212:215], v[6:9]
	v_mfma_f32_16x16x32_bf16 v[2:5], v[180:183], v[212:215], v[2:5]
	v_mfma_f32_16x16x32_bf16 v[54:57], v[176:179], v[192:195], v[54:57]
	v_mfma_f32_16x16x32_bf16 v[50:53], v[184:187], v[192:195], v[50:53]
	v_mfma_f32_16x16x32_bf16 v[38:41], v[176:179], v[200:203], v[38:41]
	v_mfma_f32_16x16x32_bf16 v[34:37], v[184:187], v[200:203], v[34:37]
	v_mfma_f32_16x16x32_bf16 v[22:25], v[176:179], v[208:211], v[22:25]
	v_mfma_f32_16x16x32_bf16 v[18:21], v[184:187], v[208:211], v[18:21]
	v_mfma_f32_16x16x32_bf16 v[6:9], v[176:179], v[216:219], v[6:9]
	v_mfma_f32_16x16x32_bf16 v[2:5], v[184:187], v[216:219], v[2:5]
	s_setprio 0
	s_add_i32 s63, s63, 2
	v_lshl_add_u64 v[144:145], v[144:145], 0, s[92:93]
	s_cmp_gt_u32 s63, 53
	s_mov_b64 s[20:21], s[22:23]
	s_barrier
	s_cbranch_scc0 .LBB0_1294
	s_and_b64 vcc, exec, s[16:17]
	s_cbranch_vccz .LBB0_1297
	s_barrier

.LBB0_1373:
	ds_read_b128 v[146:149], v140
	ds_read_b128 v[150:153], v140 offset:1024
	ds_read_b128 v[154:157], v140 offset:2048
	ds_read_b128 v[158:161], v140 offset:3072
	ds_read_b128 v[162:165], v141
	ds_read_b128 v[166:169], v141 offset:1024
	ds_read_b128 v[170:173], v141 offset:2048
	ds_read_b128 v[174:177], v141 offset:3072
	s_add_u32 s10, s26, 0xfffe0080
	s_addc_u32 s11, s27, -1
	s_cmp_eq_u32 s5, 4
	s_cselect_b32 s29, s21, s11
	s_cselect_b32 s28, s62, s10
	s_cselect_b32 s11, s19, s74
	s_cselect_b32 s10, s63, s80
	s_mov_b32 m0, s70
	v_lshl_add_u64 v[210:211], s[26:27], 0, v[136:137]
	ds_read_b128 v[178:181], v145
	ds_read_b128 v[182:185], v145 offset:1024
	ds_read_b128 v[186:189], v145 offset:2048
	ds_read_b128 v[190:193], v145 offset:3072
	ds_read_b128 v[194:197], v145 offset:4096
	ds_read_b128 v[198:201], v145 offset:5120
	ds_read_b128 v[202:205], v145 offset:6144
	ds_read_b128 v[206:209], v145 offset:7168
	global_load_lds_dwordx4 v[210:211], off
	v_lshl_add_u64 v[210:211], s[26:27], 0, v[138:139]
	s_mov_b32 m0, s4
	s_nop 0
	global_load_lds_dwordx4 v[210:211], off
	s_waitcnt vmcnt(8)
	s_waitcnt lgkmcnt(0)
	s_barrier
	s_setprio 1
	s_waitcnt lgkmcnt(0)
	v_mfma_i32_16x16x64_i8 v[122:125], v[146:149], v[178:181], v[122:125]
	v_mfma_i32_16x16x64_i8 v[118:121], v[154:157], v[178:181], v[118:121]
	v_mfma_i32_16x16x64_i8 v[106:109], v[146:149], v[186:189], v[106:109]
	v_mfma_i32_16x16x64_i8 v[102:105], v[154:157], v[186:189], v[102:105]
	v_mfma_i32_16x16x64_i8 v[90:93], v[146:149], v[194:197], v[90:93]
	v_mfma_i32_16x16x64_i8 v[86:89], v[154:157], v[194:197], v[86:89]
	v_mfma_i32_16x16x64_i8 v[74:77], v[146:149], v[202:205], v[74:77]
	v_mfma_i32_16x16x64_i8 v[70:73], v[154:157], v[202:205], v[70:73]
	v_mfma_i32_16x16x64_i8 v[122:125], v[150:153], v[182:185], v[122:125]
	v_mfma_i32_16x16x64_i8 v[118:121], v[158:161], v[182:185], v[118:121]
	v_mfma_i32_16x16x64_i8 v[106:109], v[150:153], v[190:193], v[106:109]
	v_mfma_i32_16x16x64_i8 v[102:105], v[158:161], v[190:193], v[102:105]
	v_mfma_i32_16x16x64_i8 v[90:93], v[150:153], v[198:201], v[90:93]
	v_mfma_i32_16x16x64_i8 v[86:89], v[158:161], v[198:201], v[86:89]
	v_mfma_i32_16x16x64_i8 v[74:77], v[150:153], v[206:209], v[74:77]
	v_mfma_i32_16x16x64_i8 v[70:73], v[158:161], v[206:209], v[70:73]
	s_setprio 0
	s_setprio 1
	v_mfma_i32_16x16x64_i8 v[126:129], v[162:165], v[178:181], v[126:129]
	v_mfma_i32_16x16x64_i8 v[114:117], v[170:173], v[178:181], v[114:117]
	v_mfma_i32_16x16x64_i8 v[110:113], v[162:165], v[186:189], v[110:113]
	v_mfma_i32_16x16x64_i8 v[98:101], v[170:173], v[186:189], v[98:101]
	v_mfma_i32_16x16x64_i8 v[94:97], v[162:165], v[194:197], v[94:97]
	v_mfma_i32_16x16x64_i8 v[82:85], v[170:173], v[194:197], v[82:85]
	v_mfma_i32_16x16x64_i8 v[78:81], v[162:165], v[202:205], v[78:81]
	v_mfma_i32_16x16x64_i8 v[66:69], v[170:173], v[202:205], v[66:69]
	v_mfma_i32_16x16x64_i8 v[126:129], v[166:169], v[182:185], v[126:129]
	v_mfma_i32_16x16x64_i8 v[114:117], v[174:177], v[182:185], v[114:117]
	v_mfma_i32_16x16x64_i8 v[110:113], v[166:169], v[190:193], v[110:113]
	v_mfma_i32_16x16x64_i8 v[98:101], v[174:177], v[190:193], v[98:101]
	v_mfma_i32_16x16x64_i8 v[94:97], v[166:169], v[198:201], v[94:97]
	v_mfma_i32_16x16x64_i8 v[82:85], v[174:177], v[198:201], v[82:85]
	v_mfma_i32_16x16x64_i8 v[78:81], v[166:169], v[206:209], v[78:81]
	v_mfma_i32_16x16x64_i8 v[66:69], v[174:177], v[206:209], v[66:69]
	s_setprio 0
	s_barrier
	s_mov_b32 m0, s50
	v_lshl_add_u64 v[210:211], s[10:11], 0, v[0:1]
	s_add_u32 s54, s10, 0x20000
	ds_read_b128 v[178:181], v145 offset:16384
	ds_read_b128 v[182:185], v145 offset:17408
	ds_read_b128 v[186:189], v145 offset:18432
	ds_read_b128 v[190:193], v145 offset:19456
	ds_read_b128 v[194:197], v145 offset:20480
	ds_read_b128 v[198:201], v145 offset:21504
	ds_read_b128 v[202:205], v145 offset:22528
	ds_read_b128 v[206:209], v145 offset:23552
	global_load_lds_dwordx4 v[210:211], off
	v_lshl_add_u64 v[212:213], s[10:11], 0, v[130:131]
	s_mov_b32 m0, s51
	s_addc_u32 s55, s11, 0
	global_load_lds_dwordx4 v[212:213], off
	v_lshl_add_u64 v[214:215], s[54:55], 0, v[0:1]
	s_mov_b32 m0, s71
	v_lshl_add_u64 v[216:217], s[28:29], 0, v[132:133]
	global_load_lds_dwordx4 v[214:215], off
	v_lshl_add_u64 v[214:215], s[54:55], 0, v[130:131]
	s_mov_b32 m0, s75
	s_nop 0
	global_load_lds_dwordx4 v[214:215], off
	v_lshl_add_u64 v[214:215], s[28:29], 0, v[134:135]
	s_mov_b32 m0, s36
	s_nop 0
	global_load_lds_dwordx4 v[214:215], off
	s_mov_b32 m0, s37
	s_nop 0
	global_load_lds_dwordx4 v[216:217], off
	s_waitcnt vmcnt(8)
	s_waitcnt lgkmcnt(0)
	s_barrier
	s_setprio 1
	s_waitcnt lgkmcnt(0)
	v_mfma_i32_16x16x64_i8 v[58:61], v[146:149], v[178:181], v[58:61]
	v_mfma_i32_16x16x64_i8 v[54:57], v[154:157], v[178:181], v[54:57]
	v_mfma_i32_16x16x64_i8 v[42:45], v[146:149], v[186:189], v[42:45]
	v_mfma_i32_16x16x64_i8 v[38:41], v[154:157], v[186:189], v[38:41]
	v_mfma_i32_16x16x64_i8 v[26:29], v[146:149], v[194:197], v[26:29]
	v_mfma_i32_16x16x64_i8 v[22:25], v[154:157], v[194:197], v[22:25]
	v_mfma_i32_16x16x64_i8 v[10:13], v[146:149], v[202:205], v[10:13]
	v_mfma_i32_16x16x64_i8 v[6:9], v[154:157], v[202:205], v[6:9]
	v_mfma_i32_16x16x64_i8 v[58:61], v[150:153], v[182:185], v[58:61]
	v_mfma_i32_16x16x64_i8 v[54:57], v[158:161], v[182:185], v[54:57]
	v_mfma_i32_16x16x64_i8 v[42:45], v[150:153], v[190:193], v[42:45]
	v_mfma_i32_16x16x64_i8 v[38:41], v[158:161], v[190:193], v[38:41]
	v_mfma_i32_16x16x64_i8 v[26:29], v[150:153], v[198:201], v[26:29]
	v_mfma_i32_16x16x64_i8 v[22:25], v[158:161], v[198:201], v[22:25]
	v_mfma_i32_16x16x64_i8 v[10:13], v[150:153], v[206:209], v[10:13]
	v_mfma_i32_16x16x64_i8 v[6:9], v[158:161], v[206:209], v[6:9]
	s_setprio 0
	s_setprio 1
	v_mfma_i32_16x16x64_i8 v[62:65], v[162:165], v[178:181], v[62:65]
	v_mfma_i32_16x16x64_i8 v[50:53], v[170:173], v[178:181], v[50:53]
	v_mfma_i32_16x16x64_i8 v[46:49], v[162:165], v[186:189], v[46:49]
	v_mfma_i32_16x16x64_i8 v[34:37], v[170:173], v[186:189], v[34:37]
	v_mfma_i32_16x16x64_i8 v[30:33], v[162:165], v[194:197], v[30:33]
	v_mfma_i32_16x16x64_i8 v[18:21], v[170:173], v[194:197], v[18:21]
	v_mfma_i32_16x16x64_i8 v[14:17], v[162:165], v[202:205], v[14:17]
	v_mfma_i32_16x16x64_i8 v[2:5], v[170:173], v[202:205], v[2:5]
	v_mfma_i32_16x16x64_i8 v[62:65], v[166:169], v[182:185], v[62:65]
	v_mfma_i32_16x16x64_i8 v[50:53], v[174:177], v[182:185], v[50:53]
	v_mfma_i32_16x16x64_i8 v[46:49], v[166:169], v[190:193], v[46:49]
	v_mfma_i32_16x16x64_i8 v[34:37], v[174:177], v[190:193], v[34:37]
	v_mfma_i32_16x16x64_i8 v[30:33], v[166:169], v[198:201], v[30:33]
	v_mfma_i32_16x16x64_i8 v[18:21], v[174:177], v[198:201], v[18:21]
	v_mfma_i32_16x16x64_i8 v[14:17], v[166:169], v[206:209], v[14:17]
	v_mfma_i32_16x16x64_i8 v[2:5], v[174:177], v[206:209], v[2:5]
	s_setprio 0
	s_barrier
	ds_read_b128 v[146:149], v142
	ds_read_b128 v[150:153], v142 offset:1024
	ds_read_b128 v[154:157], v142 offset:2048
	ds_read_b128 v[158:161], v142 offset:3072
	ds_read_b128 v[162:165], v143
	ds_read_b128 v[166:169], v143 offset:1024
	ds_read_b128 v[170:173], v143 offset:2048
	ds_read_b128 v[174:177], v143 offset:3072
	s_add_u32 s28, s28, 0x20000
	s_addc_u32 s29, s29, 0
	s_mov_b32 m0, s38
	v_lshl_add_u64 v[218:219], s[28:29], 0, v[134:135]
	ds_read_b128 v[178:181], v145 offset:32768
	ds_read_b128 v[182:185], v145 offset:33792
	ds_read_b128 v[186:189], v145 offset:34816
	ds_read_b128 v[190:193], v145 offset:35840
	ds_read_b128 v[194:197], v145 offset:36864
	ds_read_b128 v[198:201], v145 offset:37888
	ds_read_b128 v[202:205], v145 offset:38912
	ds_read_b128 v[206:209], v145 offset:39936
	global_load_lds_dwordx4 v[218:219], off
	v_lshl_add_u64 v[218:219], s[28:29], 0, v[132:133]
	s_mov_b32 m0, s39
	s_nop 0
	global_load_lds_dwordx4 v[218:219], off
	s_waitcnt vmcnt(8)
	s_waitcnt lgkmcnt(0)
	s_barrier
	s_setprio 1
	s_waitcnt lgkmcnt(0)
	v_mfma_i32_16x16x64_i8 v[122:125], v[146:149], v[178:181], v[122:125]
	v_mfma_i32_16x16x64_i8 v[118:121], v[154:157], v[178:181], v[118:121]
	v_mfma_i32_16x16x64_i8 v[106:109], v[146:149], v[186:189], v[106:109]
	v_mfma_i32_16x16x64_i8 v[102:105], v[154:157], v[186:189], v[102:105]
	v_mfma_i32_16x16x64_i8 v[90:93], v[146:149], v[194:197], v[90:93]
	v_mfma_i32_16x16x64_i8 v[86:89], v[154:157], v[194:197], v[86:89]
	v_mfma_i32_16x16x64_i8 v[74:77], v[146:149], v[202:205], v[74:77]
	v_mfma_i32_16x16x64_i8 v[70:73], v[154:157], v[202:205], v[70:73]
	v_mfma_i32_16x16x64_i8 v[122:125], v[150:153], v[182:185], v[122:125]
	v_mfma_i32_16x16x64_i8 v[118:121], v[158:161], v[182:185], v[118:121]
	v_mfma_i32_16x16x64_i8 v[106:109], v[150:153], v[190:193], v[106:109]
	v_mfma_i32_16x16x64_i8 v[102:105], v[158:161], v[190:193], v[102:105]
	v_mfma_i32_16x16x64_i8 v[90:93], v[150:153], v[198:201], v[90:93]
	v_mfma_i32_16x16x64_i8 v[86:89], v[158:161], v[198:201], v[86:89]
	v_mfma_i32_16x16x64_i8 v[74:77], v[150:153], v[206:209], v[74:77]
	v_mfma_i32_16x16x64_i8 v[70:73], v[158:161], v[206:209], v[70:73]
	s_setprio 0
	s_setprio 1
	v_mfma_i32_16x16x64_i8 v[126:129], v[162:165], v[178:181], v[126:129]
	v_mfma_i32_16x16x64_i8 v[114:117], v[170:173], v[178:181], v[114:117]
	v_mfma_i32_16x16x64_i8 v[110:113], v[162:165], v[186:189], v[110:113]
	v_mfma_i32_16x16x64_i8 v[98:101], v[170:173], v[186:189], v[98:101]
	v_mfma_i32_16x16x64_i8 v[94:97], v[162:165], v[194:197], v[94:97]
	v_mfma_i32_16x16x64_i8 v[82:85], v[170:173], v[194:197], v[82:85]
	v_mfma_i32_16x16x64_i8 v[78:81], v[162:165], v[202:205], v[78:81]
	v_mfma_i32_16x16x64_i8 v[66:69], v[170:173], v[202:205], v[66:69]
	v_mfma_i32_16x16x64_i8 v[126:129], v[166:169], v[182:185], v[126:129]
	v_mfma_i32_16x16x64_i8 v[114:117], v[174:177], v[182:185], v[114:117]
	v_mfma_i32_16x16x64_i8 v[110:113], v[166:169], v[190:193], v[110:113]
	v_mfma_i32_16x16x64_i8 v[98:101], v[174:177], v[190:193], v[98:101]
	v_mfma_i32_16x16x64_i8 v[94:97], v[166:169], v[198:201], v[94:97]
	v_mfma_i32_16x16x64_i8 v[82:85], v[174:177], v[198:201], v[82:85]
	v_mfma_i32_16x16x64_i8 v[78:81], v[166:169], v[206:209], v[78:81]
	v_mfma_i32_16x16x64_i8 v[66:69], v[174:177], v[206:209], v[66:69]
	s_setprio 0
	s_barrier
	s_mov_b32 m0, s78
	v_lshl_add_u64 v[210:211], v[210:211], 0, s[56:57]
	s_add_u32 s10, s10, 0x20080
	ds_read_b128 v[178:181], v145 offset:49152
	ds_read_b128 v[182:185], v145 offset:50176
	ds_read_b128 v[186:189], v145 offset:51200
	ds_read_b128 v[190:193], v145 offset:52224
	ds_read_b128 v[194:197], v145 offset:53248
	ds_read_b128 v[198:201], v145 offset:54272
	ds_read_b128 v[202:205], v145 offset:55296
	ds_read_b128 v[206:209], v145 offset:56320
	global_load_lds_dwordx4 v[210:211], off
	v_lshl_add_u64 v[210:211], v[212:213], 0, s[56:57]
	s_mov_b32 m0, s79
	s_addc_u32 s11, s11, 0
	global_load_lds_dwordx4 v[210:211], off
	v_lshl_add_u64 v[210:211], s[10:11], 0, v[0:1]
	s_mov_b32 m0, s58
	s_nop 0
	global_load_lds_dwordx4 v[210:211], off
	v_lshl_add_u64 v[210:211], s[10:11], 0, v[130:131]
	s_mov_b32 m0, s48
	s_nop 0
	global_load_lds_dwordx4 v[210:211], off
	v_lshl_add_u64 v[210:211], v[214:215], 0, s[56:57]
	s_mov_b32 m0, s45
	s_nop 0
	global_load_lds_dwordx4 v[210:211], off
	v_lshl_add_u64 v[210:211], v[216:217], 0, s[56:57]
	s_mov_b32 m0, s49
	s_nop 0
	global_load_lds_dwordx4 v[210:211], off
	s_waitcnt vmcnt(8)
	s_waitcnt lgkmcnt(0)
	s_barrier
	s_setprio 1
	s_waitcnt lgkmcnt(0)
	v_mfma_i32_16x16x64_i8 v[58:61], v[146:149], v[178:181], v[58:61]
	v_mfma_i32_16x16x64_i8 v[54:57], v[154:157], v[178:181], v[54:57]
	v_mfma_i32_16x16x64_i8 v[42:45], v[146:149], v[186:189], v[42:45]
	v_mfma_i32_16x16x64_i8 v[38:41], v[154:157], v[186:189], v[38:41]
	v_mfma_i32_16x16x64_i8 v[26:29], v[146:149], v[194:197], v[26:29]
	v_mfma_i32_16x16x64_i8 v[22:25], v[154:157], v[194:197], v[22:25]
	v_mfma_i32_16x16x64_i8 v[10:13], v[146:149], v[202:205], v[10:13]
	v_mfma_i32_16x16x64_i8 v[6:9], v[154:157], v[202:205], v[6:9]
	v_mfma_i32_16x16x64_i8 v[58:61], v[150:153], v[182:185], v[58:61]
	v_mfma_i32_16x16x64_i8 v[54:57], v[158:161], v[182:185], v[54:57]
	v_mfma_i32_16x16x64_i8 v[42:45], v[150:153], v[190:193], v[42:45]
	v_mfma_i32_16x16x64_i8 v[38:41], v[158:161], v[190:193], v[38:41]
	v_mfma_i32_16x16x64_i8 v[26:29], v[150:153], v[198:201], v[26:29]
	v_mfma_i32_16x16x64_i8 v[22:25], v[158:161], v[198:201], v[22:25]
	v_mfma_i32_16x16x64_i8 v[10:13], v[150:153], v[206:209], v[10:13]
	v_mfma_i32_16x16x64_i8 v[6:9], v[158:161], v[206:209], v[6:9]
	s_setprio 0
	s_setprio 1
	v_mfma_i32_16x16x64_i8 v[62:65], v[162:165], v[178:181], v[62:65]
	v_mfma_i32_16x16x64_i8 v[50:53], v[170:173], v[178:181], v[50:53]
	v_mfma_i32_16x16x64_i8 v[46:49], v[162:165], v[186:189], v[46:49]
	v_mfma_i32_16x16x64_i8 v[34:37], v[170:173], v[186:189], v[34:37]
	v_mfma_i32_16x16x64_i8 v[30:33], v[162:165], v[194:197], v[30:33]
	v_mfma_i32_16x16x64_i8 v[18:21], v[170:173], v[194:197], v[18:21]
	v_mfma_i32_16x16x64_i8 v[14:17], v[162:165], v[202:205], v[14:17]
	v_mfma_i32_16x16x64_i8 v[2:5], v[170:173], v[202:205], v[2:5]
	v_mfma_i32_16x16x64_i8 v[62:65], v[166:169], v[182:185], v[62:65]
	v_mfma_i32_16x16x64_i8 v[50:53], v[174:177], v[182:185], v[50:53]
	v_mfma_i32_16x16x64_i8 v[46:49], v[166:169], v[190:193], v[46:49]
	v_mfma_i32_16x16x64_i8 v[34:37], v[174:177], v[190:193], v[34:37]
	v_mfma_i32_16x16x64_i8 v[30:33], v[166:169], v[198:201], v[30:33]
	v_mfma_i32_16x16x64_i8 v[18:21], v[174:177], v[198:201], v[18:21]
	v_mfma_i32_16x16x64_i8 v[14:17], v[166:169], v[206:209], v[14:17]
	v_mfma_i32_16x16x64_i8 v[2:5], v[174:177], v[206:209], v[2:5]
	s_setprio 0
	s_add_i32 s5, s5, 2
	s_add_u32 s26, s26, 0x100
	s_addc_u32 s27, s27, 0
	s_add_u32 s80, s80, 0x100
	s_addc_u32 s74, s74, 0
	s_cmp_gt_u32 s5, 5
	s_barrier
	s_cbranch_scc0 .LBB0_1373
	s_lshl_b32 s4, s59, 8
	s_add_i32 s4, s4, s40
	v_mbcnt_lo_u32_b32 v140, -1, 0
	v_mbcnt_hi_u32_b32 v140, -1, v140
	s_and_b64 vcc, exec, s[16:17]
	v_and_or_b32 v142, v140, 15, s4
	v_ashrrev_i32_e32 v143, 31, v142
	v_lshl_add_u64 v[152:153], v[142:143], 2, s[14:15]
	global_load_dword v141, v[152:153], off
	global_load_dword v151, v[152:153], off offset:64
	global_load_dword v150, v[152:153], off offset:128
	global_load_dword v149, v[152:153], off offset:192
	global_load_dword v148, v[152:153], off offset:512
	global_load_dword v147, v[152:153], off offset:576
	global_load_dword v146, v[152:153], off offset:640
	global_load_dword v143, v[152:153], off offset:704
	s_cbranch_vccz .LBB0_1376
	s_barrier

.LBB0_1475:
	s_add_u32 s18, s20, 0x100
	s_addc_u32 s19, s21, 0
	s_add_i32 s4, 0, 0x10000
	s_cmp_eq_u32 s52, 18
	s_cselect_b32 s25, s11, s19
	s_cselect_b32 s24, s10, s18
	s_cselect_b32 s23, s17, s49
	s_cselect_b32 s22, s16, s45
	s_add_i32 s5, 0, 0x14000
	v_add_u32_e32 v2, s4, v207
	v_add_u32_e32 v6, s5, v207
	ds_read_b128 v[26:29], v2
	ds_read_b128 v[30:33], v2 offset:1024
	ds_read_b128 v[18:21], v2 offset:2048
	ds_read_b128 v[22:25], v2 offset:3072
	ds_read_b128 v[10:13], v6
	ds_read_b128 v[14:17], v6 offset:1024
	ds_read_b128 v[2:5], v6 offset:2048
	ds_read_b128 v[6:9], v6 offset:3072
	v_lshl_add_u64 v[188:189], s[20:21], 0, v[168:169]
	s_add_i32 m0, s31, 0xc000
	ds_read_b128 v[172:175], v209
	ds_read_b128 v[176:179], v209 offset:1024
	ds_read_b128 v[180:183], v209 offset:2048
	ds_read_b128 v[184:187], v209 offset:3072
	ds_read_b128 v[198:201], v209 offset:4096
	ds_read_b128 v[202:205], v209 offset:5120
	ds_read_b128 v[210:213], v209 offset:6144
	ds_read_b128 v[214:217], v209 offset:7168
	global_load_lds_dwordx4 v[188:189], off
	v_lshl_add_u64 v[188:189], s[20:21], 0, v[170:171]
	s_add_i32 m0, s31, 0xe000
	s_nop 0
	global_load_lds_dwordx4 v[188:189], off
	s_waitcnt vmcnt(8)
	s_waitcnt lgkmcnt(0)
	s_barrier
	s_setprio 1
	s_waitcnt lgkmcnt(0)
	s_nop 1
	v_mfma_f32_16x16x128_f8f6f4 v[158:161], v[26:33], v[172:179], v[158:161]
	s_nop 1
	v_mfma_f32_16x16x128_f8f6f4 v[154:157], v[18:25], v[172:179], v[154:157]
	s_nop 1
	v_mfma_f32_16x16x128_f8f6f4 v[146:149], v[26:33], v[180:187], v[146:149]
	s_nop 1
	v_mfma_f32_16x16x128_f8f6f4 v[142:145], v[18:25], v[180:187], v[142:145]
	s_nop 1
	v_mfma_f32_16x16x128_f8f6f4 v[134:137], v[26:33], v[198:205], v[134:137]
	s_nop 1
	v_mfma_f32_16x16x128_f8f6f4 v[130:133], v[18:25], v[198:205], v[130:133]
	s_nop 1
	v_mfma_f32_16x16x128_f8f6f4 v[118:121], v[26:33], v[210:217], v[118:121]
	s_nop 1
	v_mfma_f32_16x16x128_f8f6f4 v[114:117], v[18:25], v[210:217], v[114:117]
	s_setprio 0
	s_setprio 1
	s_nop 1
	v_mfma_f32_16x16x128_f8f6f4 v[150:153], v[10:17], v[172:179], v[150:153]
	s_nop 1
	v_mfma_f32_16x16x128_f8f6f4 v[138:141], v[2:9], v[172:179], v[138:141]
	s_nop 1
	v_mfma_f32_16x16x128_f8f6f4 v[126:129], v[10:17], v[180:187], v[126:129]
	s_nop 1
	v_mfma_f32_16x16x128_f8f6f4 v[122:125], v[2:9], v[180:187], v[122:125]
	s_nop 1
	v_mfma_f32_16x16x128_f8f6f4 v[110:113], v[10:17], v[198:205], v[110:113]
	s_nop 1
	v_mfma_f32_16x16x128_f8f6f4 v[106:109], v[2:9], v[198:205], v[106:109]
	s_nop 1
	v_mfma_f32_16x16x128_f8f6f4 v[102:105], v[10:17], v[210:217], v[102:105]
	s_nop 1
	v_mfma_f32_16x16x128_f8f6f4 v[98:101], v[2:9], v[210:217], v[98:101]
	s_setprio 0
	s_barrier
	s_add_i32 s4, s4, s30
	v_lshl_add_u64 v[172:173], s[22:23], 0, v[0:1]
	s_mov_b32 m0, s4
	ds_read_b128 v[180:183], v209 offset:16384
	ds_read_b128 v[184:187], v209 offset:17408
	ds_read_b128 v[198:201], v209 offset:18432
	ds_read_b128 v[202:205], v209 offset:19456
	ds_read_b128 v[210:213], v209 offset:20480
	ds_read_b128 v[214:217], v209 offset:21504
	ds_read_b128 v[218:221], v209 offset:22528
	ds_read_b128 v[222:225], v209 offset:23552
	global_load_lds_dwordx4 v[172:173], off
	s_add_i32 m0, s4, 0x2000
	s_add_u32 s20, s22, 0x58000
	v_lshl_add_u64 v[174:175], s[22:23], 0, v[162:163]
	s_addc_u32 s21, s23, 0
	s_add_i32 s4, s5, s30
	global_load_lds_dwordx4 v[174:175], off
	v_lshl_add_u64 v[176:177], s[20:21], 0, v[0:1]
	s_mov_b32 m0, s4
	v_lshl_add_u64 v[178:179], s[24:25], 0, v[164:165]
	global_load_lds_dwordx4 v[176:177], off
	v_lshl_add_u64 v[176:177], s[20:21], 0, v[162:163]
	s_add_i32 m0, s4, 0x2000
	s_nop 0
	global_load_lds_dwordx4 v[176:177], off
	v_lshl_add_u64 v[176:177], s[24:25], 0, v[166:167]
	s_mov_b32 m0, s31
	s_nop 0
	global_load_lds_dwordx4 v[176:177], off
	s_mov_b32 m0, s33
	s_nop 0
	global_load_lds_dwordx4 v[178:179], off
	s_waitcnt vmcnt(8)
	s_waitcnt lgkmcnt(0)
	s_barrier
	s_setprio 1
	s_waitcnt lgkmcnt(0)
	s_nop 1
	v_mfma_f32_16x16x128_f8f6f4 v[94:97], v[26:33], v[180:187], v[94:97]
	s_nop 1
	v_mfma_f32_16x16x128_f8f6f4 v[90:93], v[18:25], v[180:187], v[90:93]
	s_nop 1
	v_mfma_f32_16x16x128_f8f6f4 v[82:85], v[26:33], v[198:205], v[82:85]
	s_nop 1
	v_mfma_f32_16x16x128_f8f6f4 v[74:77], v[18:25], v[198:205], v[74:77]
	s_nop 1
	v_mfma_f32_16x16x128_f8f6f4 v[66:69], v[26:33], v[210:217], v[66:69]
	s_nop 1
	v_mfma_f32_16x16x128_f8f6f4 v[58:61], v[18:25], v[210:217], v[58:61]
	s_nop 1
	v_mfma_f32_16x16x128_f8f6f4 v[50:53], v[26:33], v[218:225], v[50:53]
	s_nop 1
	v_mfma_f32_16x16x128_f8f6f4 v[42:45], v[18:25], v[218:225], v[42:45]
	s_setprio 0
	s_setprio 1
	s_nop 1
	v_mfma_f32_16x16x128_f8f6f4 v[86:89], v[10:17], v[180:187], v[86:89]
	s_nop 1
	v_mfma_f32_16x16x128_f8f6f4 v[78:81], v[2:9], v[180:187], v[78:81]
	s_nop 1
	v_mfma_f32_16x16x128_f8f6f4 v[70:73], v[10:17], v[198:205], v[70:73]
	s_nop 1
	v_mfma_f32_16x16x128_f8f6f4 v[62:65], v[2:9], v[198:205], v[62:65]
	s_nop 1
	v_mfma_f32_16x16x128_f8f6f4 v[54:57], v[10:17], v[210:217], v[54:57]
	s_nop 1
	v_mfma_f32_16x16x128_f8f6f4 v[46:49], v[2:9], v[210:217], v[46:49]
	s_nop 1
	v_mfma_f32_16x16x128_f8f6f4 v[38:41], v[10:17], v[218:225], v[38:41]
	s_nop 1
	v_mfma_f32_16x16x128_f8f6f4 v[34:37], v[2:9], v[218:225], v[34:37]
	s_setprio 0
	s_barrier
	s_add_i32 s20, 0, 0x18000
	s_add_i32 s21, 0, 0x1c000
	v_add_u32_e32 v14, s20, v207
	v_add_u32_e32 v30, s21, v207
	ds_read_b128 v[2:5], v14
	ds_read_b128 v[6:9], v14 offset:1024
	ds_read_b128 v[10:13], v14 offset:2048
	ds_read_b128 v[14:17], v14 offset:3072
	ds_read_b128 v[18:21], v30
	ds_read_b128 v[22:25], v30 offset:1024
	ds_read_b128 v[26:29], v30 offset:2048
	ds_read_b128 v[30:33], v30 offset:3072
	s_add_u32 s4, s24, 0x58000
	s_addc_u32 s5, s25, 0
	s_mov_b32 m0, s34
	v_lshl_add_u64 v[188:189], s[4:5], 0, v[166:167]
	ds_read_b128 v[180:183], v209 offset:32768
	ds_read_b128 v[184:187], v209 offset:33792
	ds_read_b128 v[198:201], v209 offset:34816
	ds_read_b128 v[202:205], v209 offset:35840
	ds_read_b128 v[210:213], v209 offset:36864
	ds_read_b128 v[214:217], v209 offset:37888
	ds_read_b128 v[218:221], v209 offset:38912
	ds_read_b128 v[222:225], v209 offset:39936
	global_load_lds_dwordx4 v[188:189], off
	v_lshl_add_u64 v[188:189], s[4:5], 0, v[164:165]
	s_mov_b32 m0, s35
	s_nop 0
	global_load_lds_dwordx4 v[188:189], off
	s_waitcnt vmcnt(8)
	s_waitcnt lgkmcnt(0)
	s_barrier
	s_setprio 1
	s_waitcnt lgkmcnt(0)
	s_nop 1
	v_mfma_f32_16x16x128_f8f6f4 v[158:161], v[2:9], v[180:187], v[158:161]
	s_nop 1
	v_mfma_f32_16x16x128_f8f6f4 v[154:157], v[10:17], v[180:187], v[154:157]
	s_nop 1
	v_mfma_f32_16x16x128_f8f6f4 v[146:149], v[2:9], v[198:205], v[146:149]
	s_nop 1
	v_mfma_f32_16x16x128_f8f6f4 v[142:145], v[10:17], v[198:205], v[142:145]
	s_nop 1
	v_mfma_f32_16x16x128_f8f6f4 v[134:137], v[2:9], v[210:217], v[134:137]
	s_nop 1
	v_mfma_f32_16x16x128_f8f6f4 v[130:133], v[10:17], v[210:217], v[130:133]
	s_nop 1
	v_mfma_f32_16x16x128_f8f6f4 v[118:121], v[2:9], v[218:225], v[118:121]
	s_nop 1
	v_mfma_f32_16x16x128_f8f6f4 v[114:117], v[10:17], v[218:225], v[114:117]
	s_setprio 0
	s_setprio 1
	s_nop 1
	v_mfma_f32_16x16x128_f8f6f4 v[150:153], v[18:25], v[180:187], v[150:153]
	s_nop 1
	v_mfma_f32_16x16x128_f8f6f4 v[138:141], v[26:33], v[180:187], v[138:141]
	s_nop 1
	v_mfma_f32_16x16x128_f8f6f4 v[126:129], v[18:25], v[198:205], v[126:129]
	s_nop 1
	v_mfma_f32_16x16x128_f8f6f4 v[122:125], v[26:33], v[198:205], v[122:125]
	s_nop 1
	v_mfma_f32_16x16x128_f8f6f4 v[110:113], v[18:25], v[210:217], v[110:113]
	s_nop 1
	v_mfma_f32_16x16x128_f8f6f4 v[106:109], v[26:33], v[210:217], v[106:109]
	s_nop 1
	v_mfma_f32_16x16x128_f8f6f4 v[102:105], v[18:25], v[218:225], v[102:105]
	s_nop 1
	v_mfma_f32_16x16x128_f8f6f4 v[98:101], v[26:33], v[218:225], v[98:101]
	s_setprio 0
	s_barrier
	s_add_i32 s4, s20, s30
	v_lshl_add_u64 v[172:173], v[172:173], 0, s[56:57]
	s_mov_b32 m0, s4
	ds_read_b128 v[180:183], v209 offset:49152
	ds_read_b128 v[184:187], v209 offset:50176
	ds_read_b128 v[198:201], v209 offset:51200
	ds_read_b128 v[202:205], v209 offset:52224
	ds_read_b128 v[210:213], v209 offset:53248
	ds_read_b128 v[214:217], v209 offset:54272
	ds_read_b128 v[218:221], v209 offset:55296
	ds_read_b128 v[222:225], v209 offset:56320
	global_load_lds_dwordx4 v[172:173], off
	s_add_i32 m0, s4, 0x2000
	s_add_u32 s4, s22, 0x58080
	v_lshl_add_u64 v[172:173], v[174:175], 0, s[56:57]
	s_addc_u32 s5, s23, 0
	s_add_i32 s20, s21, s30
	global_load_lds_dwordx4 v[172:173], off
	v_lshl_add_u64 v[172:173], s[4:5], 0, v[0:1]
	s_mov_b32 m0, s20
	s_nop 0
	global_load_lds_dwordx4 v[172:173], off
	v_lshl_add_u64 v[172:173], s[4:5], 0, v[162:163]
	s_add_i32 m0, s20, 0x2000
	s_nop 0
	global_load_lds_dwordx4 v[172:173], off
	v_lshl_add_u64 v[172:173], v[176:177], 0, s[56:57]
	s_mov_b32 m0, s36
	s_nop 0
	global_load_lds_dwordx4 v[172:173], off
	v_lshl_add_u64 v[172:173], v[178:179], 0, s[56:57]
	s_mov_b32 m0, s37
	s_nop 0
	global_load_lds_dwordx4 v[172:173], off
	s_waitcnt vmcnt(8)
	s_waitcnt lgkmcnt(0)
	s_barrier
	s_setprio 1
	s_waitcnt lgkmcnt(0)
	s_nop 1
	v_mfma_f32_16x16x128_f8f6f4 v[94:97], v[2:9], v[180:187], v[94:97]
	s_nop 1
	v_mfma_f32_16x16x128_f8f6f4 v[90:93], v[10:17], v[180:187], v[90:93]
	s_nop 1
	v_mfma_f32_16x16x128_f8f6f4 v[82:85], v[2:9], v[198:205], v[82:85]
	s_nop 1
	v_mfma_f32_16x16x128_f8f6f4 v[74:77], v[10:17], v[198:205], v[74:77]
	s_nop 1
	v_mfma_f32_16x16x128_f8f6f4 v[66:69], v[2:9], v[210:217], v[66:69]
	s_nop 1
	v_mfma_f32_16x16x128_f8f6f4 v[58:61], v[10:17], v[210:217], v[58:61]
	s_nop 1
	v_mfma_f32_16x16x128_f8f6f4 v[50:53], v[2:9], v[218:225], v[50:53]
	s_nop 1
	v_mfma_f32_16x16x128_f8f6f4 v[42:45], v[10:17], v[218:225], v[42:45]
	s_setprio 0
	s_setprio 1
	s_nop 1
	v_mfma_f32_16x16x128_f8f6f4 v[86:89], v[18:25], v[180:187], v[86:89]
	s_nop 1
	v_mfma_f32_16x16x128_f8f6f4 v[78:81], v[26:33], v[180:187], v[78:81]
	s_nop 1
	v_mfma_f32_16x16x128_f8f6f4 v[70:73], v[18:25], v[198:205], v[70:73]
	s_nop 1
	v_mfma_f32_16x16x128_f8f6f4 v[62:65], v[26:33], v[198:205], v[62:65]
	s_nop 1
	v_mfma_f32_16x16x128_f8f6f4 v[54:57], v[18:25], v[210:217], v[54:57]
	s_nop 1
	v_mfma_f32_16x16x128_f8f6f4 v[46:49], v[26:33], v[210:217], v[46:49]
	s_nop 1
	v_mfma_f32_16x16x128_f8f6f4 v[38:41], v[18:25], v[218:225], v[38:41]
	s_nop 1
	v_mfma_f32_16x16x128_f8f6f4 v[34:37], v[26:33], v[218:225], v[34:37]
	s_setprio 0
	s_add_i32 s52, s52, 2
	s_add_u32 s45, s45, 0x100
	s_addc_u32 s49, s49, 0
	s_cmp_gt_u32 s52, 19
	s_mov_b64 s[20:21], s[18:19]
	s_barrier
	s_cbranch_scc0 .LBB0_1475
	s_nop 15
	s_nop 15
	s_and_b64 vcc, exec, s[14:15]
	s_cbranch_vccz .LBB0_1478
	s_barrier

.LBB0_1501:
	s_add_u32 s20, s18, 0x100
	s_addc_u32 s21, s19, 0
	s_add_i32 s4, 0, 0x10000
	s_cmp_eq_u32 s52, 40
	s_cselect_b32 s25, s9, s21
	s_cselect_b32 s24, s8, s20
	s_cselect_b32 s23, s17, s49
	s_cselect_b32 s22, s16, s45
	s_add_i32 s48, 0, 0x14000
	v_add_u32_e32 v152, s4, v207
	v_add_u32_e32 v168, s48, v207
	ds_read_b128 v[140:143], v152
	ds_read_b128 v[144:147], v152 offset:1024
	ds_read_b128 v[148:151], v152 offset:2048
	ds_read_b128 v[152:155], v152 offset:3072
	ds_read_b128 v[156:159], v168
	ds_read_b128 v[160:163], v168 offset:1024
	ds_read_b128 v[164:167], v168 offset:2048
	ds_read_b128 v[168:171], v168 offset:3072
	v_lshl_add_u64 v[204:205], s[18:19], 0, v[136:137]
	s_add_i32 m0, s31, 0xc000
	ds_read_b128 v[172:175], v209
	ds_read_b128 v[176:179], v209 offset:1024
	ds_read_b128 v[180:183], v209 offset:2048
	ds_read_b128 v[184:187], v209 offset:3072
	ds_read_b128 v[188:191], v209 offset:4096
	ds_read_b128 v[192:195], v209 offset:5120
	ds_read_b128 v[196:199], v209 offset:6144
	ds_read_b128 v[200:203], v209 offset:7168
	global_load_lds_dwordx4 v[204:205], off
	v_lshl_add_u64 v[204:205], s[18:19], 0, v[138:139]
	s_add_i32 m0, s31, 0xe000
	s_nop 0
	global_load_lds_dwordx4 v[204:205], off
	s_waitcnt vmcnt(8)
	s_waitcnt lgkmcnt(0)
	s_barrier
	s_setprio 1
	s_waitcnt lgkmcnt(0)
	v_mfma_f32_16x16x32_bf16 v[126:129], v[140:143], v[172:175], v[126:129]
	v_mfma_f32_16x16x32_bf16 v[122:125], v[148:151], v[172:175], v[122:125]
	v_mfma_f32_16x16x32_bf16 v[114:117], v[140:143], v[180:183], v[114:117]
	v_mfma_f32_16x16x32_bf16 v[110:113], v[148:151], v[180:183], v[110:113]
	v_mfma_f32_16x16x32_bf16 v[102:105], v[140:143], v[188:191], v[102:105]
	v_mfma_f32_16x16x32_bf16 v[98:101], v[148:151], v[188:191], v[98:101]
	v_mfma_f32_16x16x32_bf16 v[86:89], v[140:143], v[196:199], v[86:89]
	v_mfma_f32_16x16x32_bf16 v[82:85], v[148:151], v[196:199], v[82:85]
	v_mfma_f32_16x16x32_bf16 v[126:129], v[144:147], v[176:179], v[126:129]
	v_mfma_f32_16x16x32_bf16 v[122:125], v[152:155], v[176:179], v[122:125]
	v_mfma_f32_16x16x32_bf16 v[114:117], v[144:147], v[184:187], v[114:117]
	v_mfma_f32_16x16x32_bf16 v[110:113], v[152:155], v[184:187], v[110:113]
	v_mfma_f32_16x16x32_bf16 v[102:105], v[144:147], v[192:195], v[102:105]
	v_mfma_f32_16x16x32_bf16 v[98:101], v[152:155], v[192:195], v[98:101]
	v_mfma_f32_16x16x32_bf16 v[86:89], v[144:147], v[200:203], v[86:89]
	v_mfma_f32_16x16x32_bf16 v[82:85], v[152:155], v[200:203], v[82:85]
	s_setprio 0
	s_setprio 1
	v_mfma_f32_16x16x32_bf16 v[118:121], v[156:159], v[172:175], v[118:121]
	v_mfma_f32_16x16x32_bf16 v[106:109], v[164:167], v[172:175], v[106:109]
	v_mfma_f32_16x16x32_bf16 v[94:97], v[156:159], v[180:183], v[94:97]
	v_mfma_f32_16x16x32_bf16 v[90:93], v[164:167], v[180:183], v[90:93]
	v_mfma_f32_16x16x32_bf16 v[78:81], v[156:159], v[188:191], v[78:81]
	v_mfma_f32_16x16x32_bf16 v[74:77], v[164:167], v[188:191], v[74:77]
	v_mfma_f32_16x16x32_bf16 v[70:73], v[156:159], v[196:199], v[70:73]
	v_mfma_f32_16x16x32_bf16 v[66:69], v[164:167], v[196:199], v[66:69]
	v_mfma_f32_16x16x32_bf16 v[118:121], v[160:163], v[176:179], v[118:121]
	v_mfma_f32_16x16x32_bf16 v[106:109], v[168:171], v[176:179], v[106:109]
	v_mfma_f32_16x16x32_bf16 v[94:97], v[160:163], v[184:187], v[94:97]
	v_mfma_f32_16x16x32_bf16 v[90:93], v[168:171], v[184:187], v[90:93]
	v_mfma_f32_16x16x32_bf16 v[78:81], v[160:163], v[192:195], v[78:81]
	v_mfma_f32_16x16x32_bf16 v[74:77], v[168:171], v[192:195], v[74:77]
	v_mfma_f32_16x16x32_bf16 v[70:73], v[160:163], v[200:203], v[70:73]
	v_mfma_f32_16x16x32_bf16 v[66:69], v[168:171], v[200:203], v[66:69]
	s_setprio 0
	s_barrier
	s_add_i32 s4, s4, s30
	v_lshl_add_u64 v[204:205], s[22:23], 0, v[0:1]
	s_mov_b32 m0, s4
	ds_read_b128 v[172:175], v209 offset:16384
	ds_read_b128 v[176:179], v209 offset:17408
	ds_read_b128 v[180:183], v209 offset:18432
	ds_read_b128 v[184:187], v209 offset:19456
	ds_read_b128 v[188:191], v209 offset:20480
	ds_read_b128 v[192:195], v209 offset:21504
	ds_read_b128 v[196:199], v209 offset:22528
	ds_read_b128 v[200:203], v209 offset:23552
	global_load_lds_dwordx4 v[204:205], off
	s_add_i32 m0, s4, 0x2000
	s_add_u32 s4, s22, 0xb0000
	v_lshl_add_u64 v[210:211], s[22:23], 0, v[130:131]
	s_addc_u32 s5, s23, 0
	s_add_i32 s18, s48, s30
	global_load_lds_dwordx4 v[210:211], off
	v_lshl_add_u64 v[212:213], s[4:5], 0, v[0:1]
	s_mov_b32 m0, s18
	v_lshl_add_u64 v[214:215], s[24:25], 0, v[132:133]
	global_load_lds_dwordx4 v[212:213], off
	v_lshl_add_u64 v[212:213], s[4:5], 0, v[130:131]
	s_add_i32 m0, s18, 0x2000
	s_nop 0
	global_load_lds_dwordx4 v[212:213], off
	v_lshl_add_u64 v[212:213], s[24:25], 0, v[134:135]
	s_mov_b32 m0, s31
	s_nop 0
	global_load_lds_dwordx4 v[212:213], off
	s_mov_b32 m0, s33
	s_nop 0
	global_load_lds_dwordx4 v[214:215], off
	s_waitcnt vmcnt(8)
	s_waitcnt lgkmcnt(0)
	s_barrier
	s_setprio 1
	s_waitcnt lgkmcnt(0)
	v_mfma_f32_16x16x32_bf16 v[62:65], v[140:143], v[172:175], v[62:65]
	v_mfma_f32_16x16x32_bf16 v[58:61], v[148:151], v[172:175], v[58:61]
	v_mfma_f32_16x16x32_bf16 v[50:53], v[140:143], v[180:183], v[50:53]
	v_mfma_f32_16x16x32_bf16 v[42:45], v[148:151], v[180:183], v[42:45]
	v_mfma_f32_16x16x32_bf16 v[34:37], v[140:143], v[188:191], v[34:37]
	v_mfma_f32_16x16x32_bf16 v[26:29], v[148:151], v[188:191], v[26:29]
	v_mfma_f32_16x16x32_bf16 v[18:21], v[140:143], v[196:199], v[18:21]
	v_mfma_f32_16x16x32_bf16 v[10:13], v[148:151], v[196:199], v[10:13]
	v_mfma_f32_16x16x32_bf16 v[62:65], v[144:147], v[176:179], v[62:65]
	v_mfma_f32_16x16x32_bf16 v[58:61], v[152:155], v[176:179], v[58:61]
	v_mfma_f32_16x16x32_bf16 v[50:53], v[144:147], v[184:187], v[50:53]
	v_mfma_f32_16x16x32_bf16 v[42:45], v[152:155], v[184:187], v[42:45]
	v_mfma_f32_16x16x32_bf16 v[34:37], v[144:147], v[192:195], v[34:37]
	v_mfma_f32_16x16x32_bf16 v[26:29], v[152:155], v[192:195], v[26:29]
	v_mfma_f32_16x16x32_bf16 v[18:21], v[144:147], v[200:203], v[18:21]
	v_mfma_f32_16x16x32_bf16 v[10:13], v[152:155], v[200:203], v[10:13]
	s_setprio 0
	s_setprio 1
	v_mfma_f32_16x16x32_bf16 v[54:57], v[156:159], v[172:175], v[54:57]
	v_mfma_f32_16x16x32_bf16 v[46:49], v[164:167], v[172:175], v[46:49]
	v_mfma_f32_16x16x32_bf16 v[38:41], v[156:159], v[180:183], v[38:41]
	v_mfma_f32_16x16x32_bf16 v[30:33], v[164:167], v[180:183], v[30:33]
	v_mfma_f32_16x16x32_bf16 v[22:25], v[156:159], v[188:191], v[22:25]
	v_mfma_f32_16x16x32_bf16 v[14:17], v[164:167], v[188:191], v[14:17]
	v_mfma_f32_16x16x32_bf16 v[6:9], v[156:159], v[196:199], v[6:9]
	v_mfma_f32_16x16x32_bf16 v[2:5], v[164:167], v[196:199], v[2:5]
	v_mfma_f32_16x16x32_bf16 v[54:57], v[160:163], v[176:179], v[54:57]
	v_mfma_f32_16x16x32_bf16 v[46:49], v[168:171], v[176:179], v[46:49]
	v_mfma_f32_16x16x32_bf16 v[38:41], v[160:163], v[184:187], v[38:41]
	v_mfma_f32_16x16x32_bf16 v[30:33], v[168:171], v[184:187], v[30:33]
	v_mfma_f32_16x16x32_bf16 v[22:25], v[160:163], v[192:195], v[22:25]
	v_mfma_f32_16x16x32_bf16 v[14:17], v[168:171], v[192:195], v[14:17]
	v_mfma_f32_16x16x32_bf16 v[6:9], v[160:163], v[200:203], v[6:9]
	v_mfma_f32_16x16x32_bf16 v[2:5], v[168:171], v[200:203], v[2:5]
	s_setprio 0
	s_barrier
	s_add_i32 s18, 0, 0x18000
	s_add_i32 s19, 0, 0x1c000
	v_add_u32_e32 v152, s18, v207
	v_add_u32_e32 v168, s19, v207
	ds_read_b128 v[140:143], v152
	ds_read_b128 v[144:147], v152 offset:1024
	ds_read_b128 v[148:151], v152 offset:2048
	ds_read_b128 v[152:155], v152 offset:3072
	ds_read_b128 v[156:159], v168
	ds_read_b128 v[160:163], v168 offset:1024
	ds_read_b128 v[164:167], v168 offset:2048
	ds_read_b128 v[168:171], v168 offset:3072
	s_add_u32 s4, s24, 0xb0000
	s_addc_u32 s5, s25, 0
	s_mov_b32 m0, s34
	v_lshl_add_u64 v[216:217], s[4:5], 0, v[134:135]
	ds_read_b128 v[172:175], v209 offset:32768
	ds_read_b128 v[176:179], v209 offset:33792
	ds_read_b128 v[180:183], v209 offset:34816
	ds_read_b128 v[184:187], v209 offset:35840
	ds_read_b128 v[188:191], v209 offset:36864
	ds_read_b128 v[192:195], v209 offset:37888
	ds_read_b128 v[196:199], v209 offset:38912
	ds_read_b128 v[200:203], v209 offset:39936
	global_load_lds_dwordx4 v[216:217], off
	v_lshl_add_u64 v[216:217], s[4:5], 0, v[132:133]
	s_mov_b32 m0, s35
	s_nop 0
	global_load_lds_dwordx4 v[216:217], off
	s_waitcnt vmcnt(8)
	s_waitcnt lgkmcnt(0)
	s_barrier
	s_setprio 1
	s_waitcnt lgkmcnt(0)
	v_mfma_f32_16x16x32_bf16 v[126:129], v[140:143], v[172:175], v[126:129]
	v_mfma_f32_16x16x32_bf16 v[122:125], v[148:151], v[172:175], v[122:125]
	v_mfma_f32_16x16x32_bf16 v[114:117], v[140:143], v[180:183], v[114:117]
	v_mfma_f32_16x16x32_bf16 v[110:113], v[148:151], v[180:183], v[110:113]
	v_mfma_f32_16x16x32_bf16 v[102:105], v[140:143], v[188:191], v[102:105]
	v_mfma_f32_16x16x32_bf16 v[98:101], v[148:151], v[188:191], v[98:101]
	v_mfma_f32_16x16x32_bf16 v[86:89], v[140:143], v[196:199], v[86:89]
	v_mfma_f32_16x16x32_bf16 v[82:85], v[148:151], v[196:199], v[82:85]
	v_mfma_f32_16x16x32_bf16 v[126:129], v[144:147], v[176:179], v[126:129]
	v_mfma_f32_16x16x32_bf16 v[122:125], v[152:155], v[176:179], v[122:125]
	v_mfma_f32_16x16x32_bf16 v[114:117], v[144:147], v[184:187], v[114:117]
	v_mfma_f32_16x16x32_bf16 v[110:113], v[152:155], v[184:187], v[110:113]
	v_mfma_f32_16x16x32_bf16 v[102:105], v[144:147], v[192:195], v[102:105]
	v_mfma_f32_16x16x32_bf16 v[98:101], v[152:155], v[192:195], v[98:101]
	v_mfma_f32_16x16x32_bf16 v[86:89], v[144:147], v[200:203], v[86:89]
	v_mfma_f32_16x16x32_bf16 v[82:85], v[152:155], v[200:203], v[82:85]
	s_setprio 0
	s_setprio 1
	v_mfma_f32_16x16x32_bf16 v[118:121], v[156:159], v[172:175], v[118:121]
	v_mfma_f32_16x16x32_bf16 v[106:109], v[164:167], v[172:175], v[106:109]
	v_mfma_f32_16x16x32_bf16 v[94:97], v[156:159], v[180:183], v[94:97]
	v_mfma_f32_16x16x32_bf16 v[90:93], v[164:167], v[180:183], v[90:93]
	v_mfma_f32_16x16x32_bf16 v[78:81], v[156:159], v[188:191], v[78:81]
	v_mfma_f32_16x16x32_bf16 v[74:77], v[164:167], v[188:191], v[74:77]
	v_mfma_f32_16x16x32_bf16 v[70:73], v[156:159], v[196:199], v[70:73]
	v_mfma_f32_16x16x32_bf16 v[66:69], v[164:167], v[196:199], v[66:69]
	v_mfma_f32_16x16x32_bf16 v[118:121], v[160:163], v[176:179], v[118:121]
	v_mfma_f32_16x16x32_bf16 v[106:109], v[168:171], v[176:179], v[106:109]
	v_mfma_f32_16x16x32_bf16 v[94:97], v[160:163], v[184:187], v[94:97]
	v_mfma_f32_16x16x32_bf16 v[90:93], v[168:171], v[184:187], v[90:93]
	v_mfma_f32_16x16x32_bf16 v[78:81], v[160:163], v[192:195], v[78:81]
	v_mfma_f32_16x16x32_bf16 v[74:77], v[168:171], v[192:195], v[74:77]
	v_mfma_f32_16x16x32_bf16 v[70:73], v[160:163], v[200:203], v[70:73]
	v_mfma_f32_16x16x32_bf16 v[66:69], v[168:171], v[200:203], v[66:69]
	s_setprio 0
	s_barrier
	s_add_i32 s4, s18, s30
	v_lshl_add_u64 v[204:205], v[204:205], 0, s[56:57]
	s_mov_b32 m0, s4
	ds_read_b128 v[172:175], v209 offset:49152
	ds_read_b128 v[176:179], v209 offset:50176
	ds_read_b128 v[180:183], v209 offset:51200
	ds_read_b128 v[184:187], v209 offset:52224
	ds_read_b128 v[188:191], v209 offset:53248
	ds_read_b128 v[192:195], v209 offset:54272
	ds_read_b128 v[196:199], v209 offset:55296
	ds_read_b128 v[200:203], v209 offset:56320
	global_load_lds_dwordx4 v[204:205], off
	s_add_i32 m0, s4, 0x2000
	s_add_u32 s4, s22, 0xb0080
	v_lshl_add_u64 v[204:205], v[210:211], 0, s[56:57]
	s_addc_u32 s5, s23, 0
	s_add_i32 s18, s19, s30
	global_load_lds_dwordx4 v[204:205], off
	v_lshl_add_u64 v[204:205], s[4:5], 0, v[0:1]
	s_mov_b32 m0, s18
	s_nop 0
	global_load_lds_dwordx4 v[204:205], off
	v_lshl_add_u64 v[204:205], s[4:5], 0, v[130:131]
	s_add_i32 m0, s18, 0x2000
	s_nop 0
	global_load_lds_dwordx4 v[204:205], off
	v_lshl_add_u64 v[204:205], v[212:213], 0, s[56:57]
	s_mov_b32 m0, s36
	s_nop 0
	global_load_lds_dwordx4 v[204:205], off
	v_lshl_add_u64 v[204:205], v[214:215], 0, s[56:57]
	s_mov_b32 m0, s37
	s_nop 0
	global_load_lds_dwordx4 v[204:205], off
	s_waitcnt vmcnt(8)
	s_waitcnt lgkmcnt(0)
	s_barrier
	s_setprio 1
	s_waitcnt lgkmcnt(0)
	v_mfma_f32_16x16x32_bf16 v[62:65], v[140:143], v[172:175], v[62:65]
	v_mfma_f32_16x16x32_bf16 v[58:61], v[148:151], v[172:175], v[58:61]
	v_mfma_f32_16x16x32_bf16 v[50:53], v[140:143], v[180:183], v[50:53]
	v_mfma_f32_16x16x32_bf16 v[42:45], v[148:151], v[180:183], v[42:45]
	v_mfma_f32_16x16x32_bf16 v[34:37], v[140:143], v[188:191], v[34:37]
	v_mfma_f32_16x16x32_bf16 v[26:29], v[148:151], v[188:191], v[26:29]
	v_mfma_f32_16x16x32_bf16 v[18:21], v[140:143], v[196:199], v[18:21]
	v_mfma_f32_16x16x32_bf16 v[10:13], v[148:151], v[196:199], v[10:13]
	v_mfma_f32_16x16x32_bf16 v[62:65], v[144:147], v[176:179], v[62:65]
	v_mfma_f32_16x16x32_bf16 v[58:61], v[152:155], v[176:179], v[58:61]
	v_mfma_f32_16x16x32_bf16 v[50:53], v[144:147], v[184:187], v[50:53]
	v_mfma_f32_16x16x32_bf16 v[42:45], v[152:155], v[184:187], v[42:45]
	v_mfma_f32_16x16x32_bf16 v[34:37], v[144:147], v[192:195], v[34:37]
	v_mfma_f32_16x16x32_bf16 v[26:29], v[152:155], v[192:195], v[26:29]
	v_mfma_f32_16x16x32_bf16 v[18:21], v[144:147], v[200:203], v[18:21]
	v_mfma_f32_16x16x32_bf16 v[10:13], v[152:155], v[200:203], v[10:13]
	s_setprio 0
	s_setprio 1
	v_mfma_f32_16x16x32_bf16 v[54:57], v[156:159], v[172:175], v[54:57]
	v_mfma_f32_16x16x32_bf16 v[46:49], v[164:167], v[172:175], v[46:49]
	v_mfma_f32_16x16x32_bf16 v[38:41], v[156:159], v[180:183], v[38:41]
	v_mfma_f32_16x16x32_bf16 v[30:33], v[164:167], v[180:183], v[30:33]
	v_mfma_f32_16x16x32_bf16 v[22:25], v[156:159], v[188:191], v[22:25]
	v_mfma_f32_16x16x32_bf16 v[14:17], v[164:167], v[188:191], v[14:17]
	v_mfma_f32_16x16x32_bf16 v[6:9], v[156:159], v[196:199], v[6:9]
	v_mfma_f32_16x16x32_bf16 v[2:5], v[164:167], v[196:199], v[2:5]
	v_mfma_f32_16x16x32_bf16 v[54:57], v[160:163], v[176:179], v[54:57]
	v_mfma_f32_16x16x32_bf16 v[46:49], v[168:171], v[176:179], v[46:49]
	v_mfma_f32_16x16x32_bf16 v[38:41], v[160:163], v[184:187], v[38:41]
	v_mfma_f32_16x16x32_bf16 v[30:33], v[168:171], v[184:187], v[30:33]
	v_mfma_f32_16x16x32_bf16 v[22:25], v[160:163], v[192:195], v[22:25]
	v_mfma_f32_16x16x32_bf16 v[14:17], v[168:171], v[192:195], v[14:17]
	v_mfma_f32_16x16x32_bf16 v[6:9], v[160:163], v[200:203], v[6:9]
	v_mfma_f32_16x16x32_bf16 v[2:5], v[168:171], v[200:203], v[2:5]
	s_setprio 0
	s_add_i32 s52, s52, 2
	s_add_u32 s45, s45, 0x100
	s_addc_u32 s49, s49, 0
	s_cmp_gt_u32 s52, 41
	s_mov_b64 s[18:19], s[20:21]
	s_barrier
	s_cbranch_scc0 .LBB0_1501
	s_and_b64 vcc, exec, s[14:15]
	s_cbranch_vccz .LBB0_1504
	s_barrier
